# LDS-DMA loads in scalar-base form (drops one 64-bit VALU add per DMA) on top of v8
# speedup vs baseline: 1.0001x; 1.0001x over previous
.LBB0_564:
	s_load_dword s14, s[96:97], 0xc0
	v_mov_b32_e32 v135, v1
	s_waitcnt vmcnt(2)
	s_barrier
	v_mov_b32_e32 v131, v1
	s_waitcnt lgkmcnt(0)
	s_add_i32 s51, s20, s14
	s_lshl_b64 s[14:15], s[60:61], 2
	s_add_u32 s14, s34, s14
	s_addc_u32 s15, s35, s15
	s_add_u32 s14, s14, 0x190000
	s_addc_u32 s15, s15, 0
	s_add_i32 s30, s20, 0x400
	s_ashr_i32 s31, s30, 31
	s_lshr_b32 s31, s31, 26
	s_add_i32 s30, s30, s31
	s_ashr_i32 s52, s30, 6
	s_add_i32 s53, s52, -2
	s_and_b64 s[0:1], s[0:1], exec
	s_movk_i32 s0, 0x80
	s_cselect_b32 s54, s0, 0x8000
	s_lshl_b32 s0, s28, 5
	s_and_b32 s28, s0, 0x60
	s_lshl_b32 s30, s27, 13
	s_lshl_b32 s31, s28, 7
	s_add_u32 s0, s18, s54
	s_addc_u32 s1, s19, 0
	s_add_i32 s55, s26, 0x18000
	s_add_i32 s56, s55, s29
	s_mov_b32 m0, s56
	s_add_i32 s57, s56, 0x2000
	global_load_lds_dwordx4 v0, s[0:1]
	v_lshl_add_u64 v[4:5], s[0:1], 0, v[134:135]
	s_add_u32 s0, s2, s54
	s_mov_b32 m0, s57
	s_addc_u32 s1, s3, 0
	s_add_i32 s58, s47, 0x8000
	v_mov_b32_e32 v133, v1
	global_load_lds_dwordx4 v[4:5], off
	s_mov_b32 m0, s58
	s_add_i32 s59, s47, 0xa000
	global_load_lds_dwordx4 v130, s[0:1]
	v_lshl_add_u64 v[4:5], s[0:1], 0, v[132:133]
	s_add_u32 s0, s16, s54
	s_addc_u32 s1, s17, 0
	s_add_i32 s60, s26, 0x1c000
	s_mov_b32 m0, s59
	s_add_i32 s62, s60, s29
	global_load_lds_dwordx4 v[4:5], off
	s_mov_b32 m0, s62
	s_add_i32 s63, s62, 0x2000
	global_load_lds_dwordx4 v0, s[0:1]
	s_mov_b32 m0, s63
	v_and_b32_e32 v3, 15, v2
	global_load_lds_dwordx4 v134, s[0:1]
	v_lshrrev_b32_e32 v4, 1, v2
	v_and_b32_e32 v4, 24, v4
	v_lshlrev_b32_e32 v5, 1, v4
	v_lshlrev_b32_e32 v2, 2, v2
	v_lshl_or_b32 v154, s27, 6, v3
	v_lshl_or_b32 v3, v3, 6, v5
	v_and_b32_e32 v2, 32, v2
	s_waitcnt vmcnt(6)
	s_cmpk_gt_i32 s20, 0xfc3f
	v_bitop3_b32 v5, v3, s30, v2 bitop3:0xde
	s_cselect_b64 s[16:17], -1, 0
	s_cmpk_lt_u32 s21, 0x100
	s_mov_b32 s64, 0
	v_bitop3_b32 v155, s31, v3, v2 bitop3:0xf6
	s_cselect_b64 s[18:19], -1, 0
	v_or_b32_e32 v156, s28, v4
	s_ashr_i32 s65, s51, 31
	s_ashr_i32 s66, s33, 31
	v_add_u32_e32 v157, s26, v5
	s_barrier
	s_branch .LBB0_567

.LBB0_575:
	s_add_i32 s28, s6, s77
	s_add_i32 s26, s28, 1
	s_cmp_ge_i32 s26, s52
	s_cselect_b32 s27, s52, 0
	s_sub_i32 s26, s26, s27
	s_ashr_i32 s27, s26, 31
	s_lshl_b64 s[78:79], s[26:27], s41
	s_add_i32 s28, s28, 2
	s_cmp_ge_i32 s28, s52
	s_cselect_b32 s26, s52, 0
	s_sub_i32 s26, s28, s26
	s_ashr_i32 s27, s26, 31
	s_lshl_b64 s[26:27], s[26:27], s41
	v_add_u32_e32 v148, s7, v155
	v_add_u32_e32 v152, s44, v155
	s_add_u32 s28, s22, s26
	ds_read_b128 v[136:139], v148
	ds_read_b128 v[140:143], v148 offset:1024
	ds_read_b128 v[144:147], v148 offset:2048
	ds_read_b128 v[148:151], v148 offset:3072
	ds_read_b128 v[158:161], v152
	ds_read_b128 v[172:175], v152 offset:1024
	ds_read_b128 v[176:179], v152 offset:2048
	ds_read_b128 v[180:183], v152 offset:3072
	s_addc_u32 s29, s23, s27
	s_add_u32 s26, s24, s26
	s_addc_u32 s27, s25, s27
	s_cmp_eq_u32 s53, s77
	s_cselect_b32 s30, s73, s28
	s_cselect_b32 s31, s74, s29
	s_cselect_b32 s29, s76, s27
	s_cselect_b32 s28, s75, s26
	s_add_u32 s26, s30, s54
	s_addc_u32 s27, s31, 0
	s_add_u32 s78, s71, s78
	s_addc_u32 s79, s72, s79
	s_add_i32 m0, s47, 0xc000
	ds_read_b128 v[184:187], v157
	ds_read_b128 v[188:191], v157 offset:1024
	ds_read_b128 v[192:195], v157 offset:2048
	ds_read_b128 v[196:199], v157 offset:3072
	ds_read_b128 v[212:215], v157 offset:4096
	ds_read_b128 v[216:219], v157 offset:5120
	ds_read_b128 v[220:223], v157 offset:6144
	ds_read_b128 v[224:227], v157 offset:7168
	global_load_lds_dwordx4 v130, s[78:79]
	s_add_i32 m0, s47, 0xe000
	s_nop 0
	global_load_lds_dwordx4 v132, s[78:79]
	s_waitcnt vmcnt(8)
	s_waitcnt lgkmcnt(0)
	s_barrier
	s_setprio 1
	s_waitcnt lgkmcnt(0)
	v_mfma_f32_16x16x32_bf16 v[126:129], v[136:139], v[184:187], v[126:129]
	v_mfma_f32_16x16x32_bf16 v[122:125], v[144:147], v[184:187], v[122:125]
	v_mfma_f32_16x16x32_bf16 v[110:113], v[136:139], v[192:195], v[110:113]
	v_mfma_f32_16x16x32_bf16 v[106:109], v[144:147], v[192:195], v[106:109]
	v_mfma_f32_16x16x32_bf16 v[94:97], v[136:139], v[212:215], v[94:97]
	v_mfma_f32_16x16x32_bf16 v[90:93], v[144:147], v[212:215], v[90:93]
	v_mfma_f32_16x16x32_bf16 v[78:81], v[136:139], v[220:223], v[78:81]
	v_mfma_f32_16x16x32_bf16 v[74:77], v[144:147], v[220:223], v[74:77]
	v_mfma_f32_16x16x32_bf16 v[126:129], v[140:143], v[188:191], v[126:129]
	v_mfma_f32_16x16x32_bf16 v[122:125], v[148:151], v[188:191], v[122:125]
	v_mfma_f32_16x16x32_bf16 v[110:113], v[140:143], v[196:199], v[110:113]
	v_mfma_f32_16x16x32_bf16 v[106:109], v[148:151], v[196:199], v[106:109]
	v_mfma_f32_16x16x32_bf16 v[94:97], v[140:143], v[216:219], v[94:97]
	v_mfma_f32_16x16x32_bf16 v[90:93], v[148:151], v[216:219], v[90:93]
	v_mfma_f32_16x16x32_bf16 v[78:81], v[140:143], v[224:227], v[78:81]
	v_mfma_f32_16x16x32_bf16 v[74:77], v[148:151], v[224:227], v[74:77]
	s_setprio 0
	s_setprio 1
	v_mfma_f32_16x16x32_bf16 v[118:121], v[158:161], v[184:187], v[118:121]
	v_mfma_f32_16x16x32_bf16 v[114:117], v[176:179], v[184:187], v[114:117]
	v_mfma_f32_16x16x32_bf16 v[102:105], v[158:161], v[192:195], v[102:105]
	v_mfma_f32_16x16x32_bf16 v[98:101], v[176:179], v[192:195], v[98:101]
	v_mfma_f32_16x16x32_bf16 v[86:89], v[158:161], v[212:215], v[86:89]
	v_mfma_f32_16x16x32_bf16 v[82:85], v[176:179], v[212:215], v[82:85]
	v_mfma_f32_16x16x32_bf16 v[70:73], v[158:161], v[220:223], v[70:73]
	v_mfma_f32_16x16x32_bf16 v[66:69], v[176:179], v[220:223], v[66:69]
	v_mfma_f32_16x16x32_bf16 v[118:121], v[172:175], v[188:191], v[118:121]
	v_mfma_f32_16x16x32_bf16 v[114:117], v[180:183], v[188:191], v[114:117]
	v_mfma_f32_16x16x32_bf16 v[102:105], v[172:175], v[196:199], v[102:105]
	v_mfma_f32_16x16x32_bf16 v[98:101], v[180:183], v[196:199], v[98:101]
	v_mfma_f32_16x16x32_bf16 v[86:89], v[172:175], v[216:219], v[86:89]
	v_mfma_f32_16x16x32_bf16 v[82:85], v[180:183], v[216:219], v[82:85]
	v_mfma_f32_16x16x32_bf16 v[70:73], v[172:175], v[224:227], v[70:73]
	v_mfma_f32_16x16x32_bf16 v[66:69], v[180:183], v[224:227], v[66:69]
	s_setprio 0
	s_barrier
	s_mov_b32 m0, s42
	s_add_u32 s78, s28, s40
	ds_read_b128 v[184:187], v157 offset:16384
	ds_read_b128 v[188:191], v157 offset:17408
	ds_read_b128 v[192:195], v157 offset:18432
	ds_read_b128 v[196:199], v157 offset:19456
	ds_read_b128 v[212:215], v157 offset:20480
	ds_read_b128 v[216:219], v157 offset:21504
	ds_read_b128 v[220:223], v157 offset:22528
	ds_read_b128 v[224:227], v157 offset:23552
	global_load_lds_dwordx4 v0, s[28:29]
	s_mov_b32 m0, s43
	s_addc_u32 s79, s29, 0
	global_load_lds_dwordx4 v134, s[28:29]
	s_mov_b32 m0, s45
	s_nop 0
	global_load_lds_dwordx4 v0, s[78:79]
	s_mov_b32 m0, s46
	s_nop 0
	global_load_lds_dwordx4 v134, s[78:79]
	s_mov_b32 m0, s47
	s_nop 0
	global_load_lds_dwordx4 v130, s[30:31]
	s_mov_b32 m0, s48
	s_nop 0
	global_load_lds_dwordx4 v132, s[30:31]
	s_waitcnt vmcnt(8)
	s_waitcnt lgkmcnt(0)
	s_barrier
	s_setprio 1
	s_waitcnt lgkmcnt(0)
	v_mfma_f32_16x16x32_bf16 v[62:65], v[136:139], v[184:187], v[62:65]
	v_mfma_f32_16x16x32_bf16 v[58:61], v[144:147], v[184:187], v[58:61]
	v_mfma_f32_16x16x32_bf16 v[46:49], v[136:139], v[192:195], v[46:49]
	v_mfma_f32_16x16x32_bf16 v[42:45], v[144:147], v[192:195], v[42:45]
	v_mfma_f32_16x16x32_bf16 v[30:33], v[136:139], v[212:215], v[30:33]
	v_mfma_f32_16x16x32_bf16 v[26:29], v[144:147], v[212:215], v[26:29]
	v_mfma_f32_16x16x32_bf16 v[14:17], v[136:139], v[220:223], v[14:17]
	v_mfma_f32_16x16x32_bf16 v[10:13], v[144:147], v[220:223], v[10:13]
	v_mfma_f32_16x16x32_bf16 v[62:65], v[140:143], v[188:191], v[62:65]
	v_mfma_f32_16x16x32_bf16 v[58:61], v[148:151], v[188:191], v[58:61]
	v_mfma_f32_16x16x32_bf16 v[46:49], v[140:143], v[196:199], v[46:49]
	v_mfma_f32_16x16x32_bf16 v[42:45], v[148:151], v[196:199], v[42:45]
	v_mfma_f32_16x16x32_bf16 v[30:33], v[140:143], v[216:219], v[30:33]
	v_mfma_f32_16x16x32_bf16 v[26:29], v[148:151], v[216:219], v[26:29]
	v_mfma_f32_16x16x32_bf16 v[14:17], v[140:143], v[224:227], v[14:17]
	v_mfma_f32_16x16x32_bf16 v[10:13], v[148:151], v[224:227], v[10:13]
	s_setprio 0
	s_setprio 1
	v_mfma_f32_16x16x32_bf16 v[54:57], v[158:161], v[184:187], v[54:57]
	v_mfma_f32_16x16x32_bf16 v[50:53], v[176:179], v[184:187], v[50:53]
	v_mfma_f32_16x16x32_bf16 v[38:41], v[158:161], v[192:195], v[38:41]
	v_mfma_f32_16x16x32_bf16 v[34:37], v[176:179], v[192:195], v[34:37]
	v_mfma_f32_16x16x32_bf16 v[22:25], v[158:161], v[212:215], v[22:25]
	v_mfma_f32_16x16x32_bf16 v[18:21], v[176:179], v[212:215], v[18:21]
	v_mfma_f32_16x16x32_bf16 v[6:9], v[158:161], v[220:223], v[6:9]
	v_mfma_f32_16x16x32_bf16 v[2:5], v[176:179], v[220:223], v[2:5]
	v_mfma_f32_16x16x32_bf16 v[54:57], v[172:175], v[188:191], v[54:57]
	v_mfma_f32_16x16x32_bf16 v[50:53], v[180:183], v[188:191], v[50:53]
	v_mfma_f32_16x16x32_bf16 v[38:41], v[172:175], v[196:199], v[38:41]
	v_mfma_f32_16x16x32_bf16 v[34:37], v[180:183], v[196:199], v[34:37]
	v_mfma_f32_16x16x32_bf16 v[22:25], v[172:175], v[216:219], v[22:25]
	v_mfma_f32_16x16x32_bf16 v[18:21], v[180:183], v[216:219], v[18:21]
	v_mfma_f32_16x16x32_bf16 v[6:9], v[172:175], v[224:227], v[6:9]
	v_mfma_f32_16x16x32_bf16 v[2:5], v[180:183], v[224:227], v[2:5]
	s_setprio 0
	s_barrier
	v_add_u32_e32 v148, s55, v155
	v_add_u32_e32 v152, s60, v155
	ds_read_b128 v[136:139], v148
	ds_read_b128 v[140:143], v148 offset:1024
	ds_read_b128 v[144:147], v148 offset:2048
	ds_read_b128 v[148:151], v148 offset:3072
	ds_read_b128 v[158:161], v152
	ds_read_b128 v[172:175], v152 offset:1024
	ds_read_b128 v[176:179], v152 offset:2048
	ds_read_b128 v[180:183], v152 offset:3072
	s_add_u32 s30, s30, s40
	s_addc_u32 s31, s31, 0
	s_mov_b32 m0, s49
	ds_read_b128 v[184:187], v157 offset:32768
	ds_read_b128 v[188:191], v157 offset:33792
	ds_read_b128 v[192:195], v157 offset:34816
	ds_read_b128 v[196:199], v157 offset:35840
	ds_read_b128 v[212:215], v157 offset:36864
	ds_read_b128 v[216:219], v157 offset:37888
	ds_read_b128 v[220:223], v157 offset:38912
	ds_read_b128 v[224:227], v157 offset:39936
	global_load_lds_dwordx4 v130, s[30:31]
	s_mov_b32 m0, s50
	s_nop 0
	global_load_lds_dwordx4 v132, s[30:31]
	s_waitcnt vmcnt(8)
	s_waitcnt lgkmcnt(0)
	s_barrier
	s_setprio 1
	s_waitcnt lgkmcnt(0)
	v_mfma_f32_16x16x32_bf16 v[126:129], v[136:139], v[184:187], v[126:129]
	v_mfma_f32_16x16x32_bf16 v[122:125], v[144:147], v[184:187], v[122:125]
	v_mfma_f32_16x16x32_bf16 v[110:113], v[136:139], v[192:195], v[110:113]
	v_mfma_f32_16x16x32_bf16 v[106:109], v[144:147], v[192:195], v[106:109]
	v_mfma_f32_16x16x32_bf16 v[94:97], v[136:139], v[212:215], v[94:97]
	v_mfma_f32_16x16x32_bf16 v[90:93], v[144:147], v[212:215], v[90:93]
	v_mfma_f32_16x16x32_bf16 v[78:81], v[136:139], v[220:223], v[78:81]
	v_mfma_f32_16x16x32_bf16 v[74:77], v[144:147], v[220:223], v[74:77]
	v_mfma_f32_16x16x32_bf16 v[126:129], v[140:143], v[188:191], v[126:129]
	v_mfma_f32_16x16x32_bf16 v[122:125], v[148:151], v[188:191], v[122:125]
	v_mfma_f32_16x16x32_bf16 v[110:113], v[140:143], v[196:199], v[110:113]
	v_mfma_f32_16x16x32_bf16 v[106:109], v[148:151], v[196:199], v[106:109]
	v_mfma_f32_16x16x32_bf16 v[94:97], v[140:143], v[216:219], v[94:97]
	v_mfma_f32_16x16x32_bf16 v[90:93], v[148:151], v[216:219], v[90:93]
	v_mfma_f32_16x16x32_bf16 v[78:81], v[140:143], v[224:227], v[78:81]
	v_mfma_f32_16x16x32_bf16 v[74:77], v[148:151], v[224:227], v[74:77]
	s_setprio 0
	s_setprio 1
	v_mfma_f32_16x16x32_bf16 v[118:121], v[158:161], v[184:187], v[118:121]
	v_mfma_f32_16x16x32_bf16 v[114:117], v[176:179], v[184:187], v[114:117]
	v_mfma_f32_16x16x32_bf16 v[102:105], v[158:161], v[192:195], v[102:105]
	v_mfma_f32_16x16x32_bf16 v[98:101], v[176:179], v[192:195], v[98:101]
	v_mfma_f32_16x16x32_bf16 v[86:89], v[158:161], v[212:215], v[86:89]
	v_mfma_f32_16x16x32_bf16 v[82:85], v[176:179], v[212:215], v[82:85]
	v_mfma_f32_16x16x32_bf16 v[70:73], v[158:161], v[220:223], v[70:73]
	v_mfma_f32_16x16x32_bf16 v[66:69], v[176:179], v[220:223], v[66:69]
	v_mfma_f32_16x16x32_bf16 v[118:121], v[172:175], v[188:191], v[118:121]
	v_mfma_f32_16x16x32_bf16 v[114:117], v[180:183], v[188:191], v[114:117]
	v_mfma_f32_16x16x32_bf16 v[102:105], v[172:175], v[196:199], v[102:105]
	v_mfma_f32_16x16x32_bf16 v[98:101], v[180:183], v[196:199], v[98:101]
	v_mfma_f32_16x16x32_bf16 v[86:89], v[172:175], v[216:219], v[86:89]
	v_mfma_f32_16x16x32_bf16 v[82:85], v[180:183], v[216:219], v[82:85]
	v_mfma_f32_16x16x32_bf16 v[70:73], v[172:175], v[224:227], v[70:73]
	v_mfma_f32_16x16x32_bf16 v[66:69], v[180:183], v[224:227], v[66:69]
	s_setprio 0
	s_barrier
	s_add_u32 s28, s28, s54
	s_addc_u32 s29, s29, 0
	s_mov_b32 m0, s56
	ds_read_b128 v[184:187], v157 offset:49152
	ds_read_b128 v[188:191], v157 offset:50176
	ds_read_b128 v[192:195], v157 offset:51200
	ds_read_b128 v[196:199], v157 offset:52224
	ds_read_b128 v[212:215], v157 offset:53248
	ds_read_b128 v[216:219], v157 offset:54272
	ds_read_b128 v[220:223], v157 offset:55296
	ds_read_b128 v[224:227], v157 offset:56320
	global_load_lds_dwordx4 v0, s[28:29]
	v_lshl_add_u64 v[152:153], s[28:29], 0, v[134:135]
	s_add_u32 s28, s28, s40
	s_mov_b32 m0, s57
	s_addc_u32 s29, s29, 0
	global_load_lds_dwordx4 v[152:153], off
	s_mov_b32 m0, s62
	s_nop 0
	global_load_lds_dwordx4 v0, s[28:29]
	s_mov_b32 m0, s63
	s_nop 0
	global_load_lds_dwordx4 v134, s[28:29]
	s_mov_b32 m0, s58
	s_nop 0
	global_load_lds_dwordx4 v130, s[26:27]
	s_mov_b32 m0, s59
	s_nop 0
	global_load_lds_dwordx4 v132, s[26:27]
	s_waitcnt vmcnt(8)
	s_waitcnt lgkmcnt(0)
	s_barrier
	s_setprio 1
	s_waitcnt lgkmcnt(0)
	v_mfma_f32_16x16x32_bf16 v[62:65], v[136:139], v[184:187], v[62:65]
	v_mfma_f32_16x16x32_bf16 v[58:61], v[144:147], v[184:187], v[58:61]
	v_mfma_f32_16x16x32_bf16 v[46:49], v[136:139], v[192:195], v[46:49]
	v_mfma_f32_16x16x32_bf16 v[42:45], v[144:147], v[192:195], v[42:45]
	v_mfma_f32_16x16x32_bf16 v[30:33], v[136:139], v[212:215], v[30:33]
	v_mfma_f32_16x16x32_bf16 v[26:29], v[144:147], v[212:215], v[26:29]
	v_mfma_f32_16x16x32_bf16 v[14:17], v[136:139], v[220:223], v[14:17]
	v_mfma_f32_16x16x32_bf16 v[10:13], v[144:147], v[220:223], v[10:13]
	v_mfma_f32_16x16x32_bf16 v[62:65], v[140:143], v[188:191], v[62:65]
	v_mfma_f32_16x16x32_bf16 v[58:61], v[148:151], v[188:191], v[58:61]
	v_mfma_f32_16x16x32_bf16 v[46:49], v[140:143], v[196:199], v[46:49]
	v_mfma_f32_16x16x32_bf16 v[42:45], v[148:151], v[196:199], v[42:45]
	v_mfma_f32_16x16x32_bf16 v[30:33], v[140:143], v[216:219], v[30:33]
	v_mfma_f32_16x16x32_bf16 v[26:29], v[148:151], v[216:219], v[26:29]
	v_mfma_f32_16x16x32_bf16 v[14:17], v[140:143], v[224:227], v[14:17]
	v_mfma_f32_16x16x32_bf16 v[10:13], v[148:151], v[224:227], v[10:13]
	s_setprio 0
	s_setprio 1
	v_mfma_f32_16x16x32_bf16 v[54:57], v[158:161], v[184:187], v[54:57]
	v_mfma_f32_16x16x32_bf16 v[50:53], v[176:179], v[184:187], v[50:53]
	v_mfma_f32_16x16x32_bf16 v[38:41], v[158:161], v[192:195], v[38:41]
	v_mfma_f32_16x16x32_bf16 v[34:37], v[176:179], v[192:195], v[34:37]
	v_mfma_f32_16x16x32_bf16 v[22:25], v[158:161], v[212:215], v[22:25]
	v_mfma_f32_16x16x32_bf16 v[18:21], v[176:179], v[212:215], v[18:21]
	v_mfma_f32_16x16x32_bf16 v[6:9], v[158:161], v[220:223], v[6:9]
	v_mfma_f32_16x16x32_bf16 v[2:5], v[176:179], v[220:223], v[2:5]
	v_mfma_f32_16x16x32_bf16 v[54:57], v[172:175], v[188:191], v[54:57]
	v_mfma_f32_16x16x32_bf16 v[50:53], v[180:183], v[188:191], v[50:53]
	v_mfma_f32_16x16x32_bf16 v[38:41], v[172:175], v[196:199], v[38:41]
	v_mfma_f32_16x16x32_bf16 v[34:37], v[180:183], v[196:199], v[34:37]
	v_mfma_f32_16x16x32_bf16 v[22:25], v[172:175], v[216:219], v[22:25]
	v_mfma_f32_16x16x32_bf16 v[18:21], v[180:183], v[216:219], v[18:21]
	v_mfma_f32_16x16x32_bf16 v[6:9], v[172:175], v[224:227], v[6:9]
	v_mfma_f32_16x16x32_bf16 v[2:5], v[180:183], v[224:227], v[2:5]
	s_setprio 0
	s_barrier
	s_add_i32 s77, s77, 2
	s_cmp_ge_i32 s77, s52
	s_cbranch_scc0 .LBB0_575

.LBB0_837:
	s_add_u32 s10, s42, 0x2f200000
	s_addc_u32 s11, s43, 0
	s_add_i32 s26, s44, 0x400
	s_ashr_i32 s27, s26, 31
	s_lshr_b32 s27, s27, 26
	s_add_i32 s26, s26, s27
	s_ashr_i32 s53, s26, 6
	s_add_i32 s55, s53, -2
	s_and_b64 s[2:3], s[2:3], exec
	s_movk_i32 s2, 0x80
	s_cselect_b32 s56, s2, 0x8000
	s_lshl_b32 s2, s25, 5
	s_and_b32 s25, s2, 0x60
	s_lshl_b32 s26, s19, 13
	s_lshl_b32 s27, s25, 7
	s_add_u32 s2, s16, s56
	s_addc_u32 s3, s17, 0
	s_add_i32 s57, s74, 0x18000
	s_add_i32 s58, s57, s24
	v_mov_b32_e32 v133, v1
	s_mov_b32 m0, s58
	s_add_i32 s59, s58, 0x2000
	s_waitcnt vmcnt(2)
	s_barrier
	global_load_lds_dwordx4 v0, s[2:3]
	v_lshl_add_u64 v[2:3], s[2:3], 0, v[132:133]
	s_add_u32 s2, s12, s56
	s_mov_b32 m0, s59
	s_addc_u32 s3, s13, 0
	s_add_i32 s60, s49, 0x8000
	global_load_lds_dwordx4 v[2:3], off
	s_mov_b32 m0, s60
	s_add_i32 s62, s49, 0xa000
	global_load_lds_dwordx4 v0, s[2:3]
	v_lshl_add_u64 v[2:3], s[2:3], 0, v[132:133]
	s_add_u32 s2, s14, s56
	s_addc_u32 s3, s15, 0
	s_add_i32 s63, s74, 0x1c000
	s_mov_b32 m0, s62
	s_add_i32 s64, s63, s24
	global_load_lds_dwordx4 v[2:3], off
	s_mov_b32 m0, s64
	s_add_i32 s65, s64, 0x2000
	global_load_lds_dwordx4 v0, s[2:3]
	s_mov_b32 m0, s65
	s_cmpk_gt_i32 s44, 0xfc3f
	global_load_lds_dwordx4 v132, s[2:3]
	v_bfe_u32 v2, v130, 4, 2
	v_and_b32_e32 v3, 15, v130
	v_lshlrev_b32_e32 v4, 4, v2
	v_lshl_or_b32 v131, s19, 6, v3
	v_lshl_or_b32 v3, v3, 6, v4
	v_lshlrev_b32_e32 v4, 2, v130
	v_and_b32_e32 v4, 32, v4
	s_waitcnt vmcnt(6)
	v_bitop3_b32 v5, v3, s26, v4 bitop3:0xde
	s_cselect_b64 s[12:13], -1, 0
	s_cmpk_lt_u32 s18, 0x100
	s_mov_b32 s66, 0
	v_bitop3_b32 v134, s27, v3, v4 bitop3:0xf6
	s_cselect_b64 s[14:15], -1, 0
	s_ashr_i32 s67, s36, 31
	v_lshl_or_b32 v135, v2, 2, s25
	v_add_u32_e32 v136, s74, v5
	s_barrier
	s_waitcnt vmcnt(0)
	s_branch .LBB0_840

.LBB0_852:
	s_add_i32 s26, s0, s79
	s_add_i32 s24, s26, 1
	s_cmp_ge_i32 s24, s53
	s_cselect_b32 s25, s53, 0
	s_sub_i32 s24, s24, s25
	s_ashr_i32 s25, s24, 31
	s_lshl_b64 s[82:83], s[24:25], s39
	s_add_i32 s26, s26, 2
	s_cmp_ge_i32 s26, s53
	s_cselect_b32 s24, s53, 0
	s_sub_i32 s24, s26, s24
	s_ashr_i32 s25, s24, 31
	v_add_u32_e32 v137, s1, v134
	s_lshl_b64 s[24:25], s[24:25], s39
	ds_read_b128 v[138:141], v137
	ds_read_b128 v[142:145], v137 offset:1024
	ds_read_b128 v[146:149], v137 offset:2048
	ds_read_b128 v[150:153], v137 offset:3072
	v_add_u32_e32 v137, s46, v134
	s_add_u32 s26, s20, s24
	ds_read_b128 v[156:159], v137
	ds_read_b128 v[160:163], v137 offset:1024
	ds_read_b128 v[172:175], v137 offset:2048
	ds_read_b128 v[176:179], v137 offset:3072
	s_addc_u32 s27, s21, s25
	s_add_u32 s24, s22, s24
	s_addc_u32 s25, s23, s25
	s_cmp_eq_u32 s55, s79
	s_cselect_b32 s28, s75, s26
	s_cselect_b32 s29, s76, s27
	s_cselect_b32 s27, s78, s25
	s_cselect_b32 s26, s77, s24
	s_add_u32 s24, s28, s56
	s_addc_u32 s25, s29, 0
	s_add_u32 s82, s72, s82
	s_addc_u32 s83, s73, s83
	s_add_i32 m0, s49, 0xc000
	ds_read_b128 v[180:183], v136
	ds_read_b128 v[184:187], v136 offset:1024
	ds_read_b128 v[188:191], v136 offset:2048
	ds_read_b128 v[192:195], v136 offset:3072
	ds_read_b128 v[196:199], v136 offset:4096
	ds_read_b128 v[212:215], v136 offset:5120
	ds_read_b128 v[216:219], v136 offset:6144
	ds_read_b128 v[220:223], v136 offset:7168
	global_load_lds_dwordx4 v0, s[82:83]
	s_add_i32 m0, s49, 0xe000
	s_nop 0
	global_load_lds_dwordx4 v132, s[82:83]
	s_waitcnt vmcnt(8)
	s_waitcnt lgkmcnt(0)
	s_barrier
	s_setprio 1
	s_waitcnt lgkmcnt(0)
	v_mfma_f32_16x16x32_bf16 v[126:129], v[138:141], v[180:183], v[126:129]
	v_mfma_f32_16x16x32_bf16 v[122:125], v[146:149], v[180:183], v[122:125]
	v_mfma_f32_16x16x32_bf16 v[110:113], v[138:141], v[188:191], v[110:113]
	v_mfma_f32_16x16x32_bf16 v[106:109], v[146:149], v[188:191], v[106:109]
	v_mfma_f32_16x16x32_bf16 v[94:97], v[138:141], v[196:199], v[94:97]
	v_mfma_f32_16x16x32_bf16 v[90:93], v[146:149], v[196:199], v[90:93]
	v_mfma_f32_16x16x32_bf16 v[78:81], v[138:141], v[216:219], v[78:81]
	v_mfma_f32_16x16x32_bf16 v[74:77], v[146:149], v[216:219], v[74:77]
	v_mfma_f32_16x16x32_bf16 v[126:129], v[142:145], v[184:187], v[126:129]
	v_mfma_f32_16x16x32_bf16 v[122:125], v[150:153], v[184:187], v[122:125]
	v_mfma_f32_16x16x32_bf16 v[110:113], v[142:145], v[192:195], v[110:113]
	v_mfma_f32_16x16x32_bf16 v[106:109], v[150:153], v[192:195], v[106:109]
	v_mfma_f32_16x16x32_bf16 v[94:97], v[142:145], v[212:215], v[94:97]
	v_mfma_f32_16x16x32_bf16 v[90:93], v[150:153], v[212:215], v[90:93]
	v_mfma_f32_16x16x32_bf16 v[78:81], v[142:145], v[220:223], v[78:81]
	v_mfma_f32_16x16x32_bf16 v[74:77], v[150:153], v[220:223], v[74:77]
	s_setprio 0
	s_setprio 1
	v_mfma_f32_16x16x32_bf16 v[118:121], v[156:159], v[180:183], v[118:121]
	v_mfma_f32_16x16x32_bf16 v[114:117], v[172:175], v[180:183], v[114:117]
	v_mfma_f32_16x16x32_bf16 v[102:105], v[156:159], v[188:191], v[102:105]
	v_mfma_f32_16x16x32_bf16 v[98:101], v[172:175], v[188:191], v[98:101]
	v_mfma_f32_16x16x32_bf16 v[86:89], v[156:159], v[196:199], v[86:89]
	v_mfma_f32_16x16x32_bf16 v[82:85], v[172:175], v[196:199], v[82:85]
	v_mfma_f32_16x16x32_bf16 v[70:73], v[156:159], v[216:219], v[70:73]
	v_mfma_f32_16x16x32_bf16 v[66:69], v[172:175], v[216:219], v[66:69]
	v_mfma_f32_16x16x32_bf16 v[118:121], v[160:163], v[184:187], v[118:121]
	v_mfma_f32_16x16x32_bf16 v[114:117], v[176:179], v[184:187], v[114:117]
	v_mfma_f32_16x16x32_bf16 v[102:105], v[160:163], v[192:195], v[102:105]
	v_mfma_f32_16x16x32_bf16 v[98:101], v[176:179], v[192:195], v[98:101]
	v_mfma_f32_16x16x32_bf16 v[86:89], v[160:163], v[212:215], v[86:89]
	v_mfma_f32_16x16x32_bf16 v[82:85], v[176:179], v[212:215], v[82:85]
	v_mfma_f32_16x16x32_bf16 v[70:73], v[160:163], v[220:223], v[70:73]
	v_mfma_f32_16x16x32_bf16 v[66:69], v[176:179], v[220:223], v[66:69]
	s_setprio 0
	s_barrier
	s_mov_b32 m0, s40
	s_add_u32 s82, s26, s38
	ds_read_b128 v[180:183], v136 offset:16384
	ds_read_b128 v[184:187], v136 offset:17408
	ds_read_b128 v[188:191], v136 offset:18432
	ds_read_b128 v[192:195], v136 offset:19456
	ds_read_b128 v[196:199], v136 offset:20480
	ds_read_b128 v[212:215], v136 offset:21504
	ds_read_b128 v[216:219], v136 offset:22528
	ds_read_b128 v[220:223], v136 offset:23552
	global_load_lds_dwordx4 v0, s[26:27]
	s_mov_b32 m0, s41
	s_addc_u32 s83, s27, 0
	global_load_lds_dwordx4 v132, s[26:27]
	s_mov_b32 m0, s47
	s_nop 0
	global_load_lds_dwordx4 v0, s[82:83]
	s_mov_b32 m0, s48
	s_nop 0
	global_load_lds_dwordx4 v132, s[82:83]
	s_mov_b32 m0, s49
	s_nop 0
	global_load_lds_dwordx4 v0, s[28:29]
	s_mov_b32 m0, s50
	s_nop 0
	global_load_lds_dwordx4 v132, s[28:29]
	s_waitcnt vmcnt(8)
	s_waitcnt lgkmcnt(0)
	s_barrier
	s_setprio 1
	s_waitcnt lgkmcnt(0)
	v_mfma_f32_16x16x32_bf16 v[62:65], v[138:141], v[180:183], v[62:65]
	v_mfma_f32_16x16x32_bf16 v[58:61], v[146:149], v[180:183], v[58:61]
	v_mfma_f32_16x16x32_bf16 v[46:49], v[138:141], v[188:191], v[46:49]
	v_mfma_f32_16x16x32_bf16 v[42:45], v[146:149], v[188:191], v[42:45]
	v_mfma_f32_16x16x32_bf16 v[30:33], v[138:141], v[196:199], v[30:33]
	v_mfma_f32_16x16x32_bf16 v[26:29], v[146:149], v[196:199], v[26:29]
	v_mfma_f32_16x16x32_bf16 v[14:17], v[138:141], v[216:219], v[14:17]
	v_mfma_f32_16x16x32_bf16 v[10:13], v[146:149], v[216:219], v[10:13]
	v_mfma_f32_16x16x32_bf16 v[62:65], v[142:145], v[184:187], v[62:65]
	v_mfma_f32_16x16x32_bf16 v[58:61], v[150:153], v[184:187], v[58:61]
	v_mfma_f32_16x16x32_bf16 v[46:49], v[142:145], v[192:195], v[46:49]
	v_mfma_f32_16x16x32_bf16 v[42:45], v[150:153], v[192:195], v[42:45]
	v_mfma_f32_16x16x32_bf16 v[30:33], v[142:145], v[212:215], v[30:33]
	v_mfma_f32_16x16x32_bf16 v[26:29], v[150:153], v[212:215], v[26:29]
	v_mfma_f32_16x16x32_bf16 v[14:17], v[142:145], v[220:223], v[14:17]
	v_mfma_f32_16x16x32_bf16 v[10:13], v[150:153], v[220:223], v[10:13]
	s_setprio 0
	s_setprio 1
	v_mfma_f32_16x16x32_bf16 v[54:57], v[156:159], v[180:183], v[54:57]
	v_mfma_f32_16x16x32_bf16 v[50:53], v[172:175], v[180:183], v[50:53]
	v_mfma_f32_16x16x32_bf16 v[38:41], v[156:159], v[188:191], v[38:41]
	v_mfma_f32_16x16x32_bf16 v[34:37], v[172:175], v[188:191], v[34:37]
	v_mfma_f32_16x16x32_bf16 v[22:25], v[156:159], v[196:199], v[22:25]
	v_mfma_f32_16x16x32_bf16 v[18:21], v[172:175], v[196:199], v[18:21]
	v_mfma_f32_16x16x32_bf16 v[6:9], v[156:159], v[216:219], v[6:9]
	v_mfma_f32_16x16x32_bf16 v[2:5], v[172:175], v[216:219], v[2:5]
	v_mfma_f32_16x16x32_bf16 v[54:57], v[160:163], v[184:187], v[54:57]
	v_mfma_f32_16x16x32_bf16 v[50:53], v[176:179], v[184:187], v[50:53]
	v_mfma_f32_16x16x32_bf16 v[38:41], v[160:163], v[192:195], v[38:41]
	v_mfma_f32_16x16x32_bf16 v[34:37], v[176:179], v[192:195], v[34:37]
	v_mfma_f32_16x16x32_bf16 v[22:25], v[160:163], v[212:215], v[22:25]
	v_mfma_f32_16x16x32_bf16 v[18:21], v[176:179], v[212:215], v[18:21]
	v_mfma_f32_16x16x32_bf16 v[6:9], v[160:163], v[220:223], v[6:9]
	v_mfma_f32_16x16x32_bf16 v[2:5], v[176:179], v[220:223], v[2:5]
	s_setprio 0
	s_barrier
	v_add_u32_e32 v137, s57, v134
	ds_read_b128 v[138:141], v137
	ds_read_b128 v[142:145], v137 offset:1024
	ds_read_b128 v[146:149], v137 offset:2048
	ds_read_b128 v[150:153], v137 offset:3072
	v_add_u32_e32 v137, s63, v134
	ds_read_b128 v[156:159], v137
	ds_read_b128 v[160:163], v137 offset:1024
	ds_read_b128 v[172:175], v137 offset:2048
	ds_read_b128 v[176:179], v137 offset:3072
	s_add_u32 s28, s28, s38
	s_addc_u32 s29, s29, 0
	s_mov_b32 m0, s51
	ds_read_b128 v[180:183], v136 offset:32768
	ds_read_b128 v[184:187], v136 offset:33792
	ds_read_b128 v[188:191], v136 offset:34816
	ds_read_b128 v[192:195], v136 offset:35840
	ds_read_b128 v[196:199], v136 offset:36864
	ds_read_b128 v[212:215], v136 offset:37888
	ds_read_b128 v[216:219], v136 offset:38912
	ds_read_b128 v[220:223], v136 offset:39936
	global_load_lds_dwordx4 v0, s[28:29]
	s_mov_b32 m0, s52
	s_nop 0
	global_load_lds_dwordx4 v132, s[28:29]
	s_waitcnt vmcnt(8)
	s_waitcnt lgkmcnt(0)
	s_barrier
	s_setprio 1
	s_waitcnt lgkmcnt(0)
	v_mfma_f32_16x16x32_bf16 v[126:129], v[138:141], v[180:183], v[126:129]
	v_mfma_f32_16x16x32_bf16 v[122:125], v[146:149], v[180:183], v[122:125]
	v_mfma_f32_16x16x32_bf16 v[110:113], v[138:141], v[188:191], v[110:113]
	v_mfma_f32_16x16x32_bf16 v[106:109], v[146:149], v[188:191], v[106:109]
	v_mfma_f32_16x16x32_bf16 v[94:97], v[138:141], v[196:199], v[94:97]
	v_mfma_f32_16x16x32_bf16 v[90:93], v[146:149], v[196:199], v[90:93]
	v_mfma_f32_16x16x32_bf16 v[78:81], v[138:141], v[216:219], v[78:81]
	v_mfma_f32_16x16x32_bf16 v[74:77], v[146:149], v[216:219], v[74:77]
	v_mfma_f32_16x16x32_bf16 v[126:129], v[142:145], v[184:187], v[126:129]
	v_mfma_f32_16x16x32_bf16 v[122:125], v[150:153], v[184:187], v[122:125]
	v_mfma_f32_16x16x32_bf16 v[110:113], v[142:145], v[192:195], v[110:113]
	v_mfma_f32_16x16x32_bf16 v[106:109], v[150:153], v[192:195], v[106:109]
	v_mfma_f32_16x16x32_bf16 v[94:97], v[142:145], v[212:215], v[94:97]
	v_mfma_f32_16x16x32_bf16 v[90:93], v[150:153], v[212:215], v[90:93]
	v_mfma_f32_16x16x32_bf16 v[78:81], v[142:145], v[220:223], v[78:81]
	v_mfma_f32_16x16x32_bf16 v[74:77], v[150:153], v[220:223], v[74:77]
	s_setprio 0
	s_setprio 1
	v_mfma_f32_16x16x32_bf16 v[118:121], v[156:159], v[180:183], v[118:121]
	v_mfma_f32_16x16x32_bf16 v[114:117], v[172:175], v[180:183], v[114:117]
	v_mfma_f32_16x16x32_bf16 v[102:105], v[156:159], v[188:191], v[102:105]
	v_mfma_f32_16x16x32_bf16 v[98:101], v[172:175], v[188:191], v[98:101]
	v_mfma_f32_16x16x32_bf16 v[86:89], v[156:159], v[196:199], v[86:89]
	v_mfma_f32_16x16x32_bf16 v[82:85], v[172:175], v[196:199], v[82:85]
	v_mfma_f32_16x16x32_bf16 v[70:73], v[156:159], v[216:219], v[70:73]
	v_mfma_f32_16x16x32_bf16 v[66:69], v[172:175], v[216:219], v[66:69]
	v_mfma_f32_16x16x32_bf16 v[118:121], v[160:163], v[184:187], v[118:121]
	v_mfma_f32_16x16x32_bf16 v[114:117], v[176:179], v[184:187], v[114:117]
	v_mfma_f32_16x16x32_bf16 v[102:105], v[160:163], v[192:195], v[102:105]
	v_mfma_f32_16x16x32_bf16 v[98:101], v[176:179], v[192:195], v[98:101]
	v_mfma_f32_16x16x32_bf16 v[86:89], v[160:163], v[212:215], v[86:89]
	v_mfma_f32_16x16x32_bf16 v[82:85], v[176:179], v[212:215], v[82:85]
	v_mfma_f32_16x16x32_bf16 v[70:73], v[160:163], v[220:223], v[70:73]
	v_mfma_f32_16x16x32_bf16 v[66:69], v[176:179], v[220:223], v[66:69]
	s_setprio 0
	s_barrier
	s_add_u32 s26, s26, s56
	s_addc_u32 s27, s27, 0
	s_mov_b32 m0, s58
	ds_read_b128 v[180:183], v136 offset:49152
	ds_read_b128 v[184:187], v136 offset:50176
	ds_read_b128 v[188:191], v136 offset:51200
	ds_read_b128 v[192:195], v136 offset:52224
	ds_read_b128 v[196:199], v136 offset:53248
	ds_read_b128 v[212:215], v136 offset:54272
	ds_read_b128 v[216:219], v136 offset:55296
	ds_read_b128 v[220:223], v136 offset:56320
	global_load_lds_dwordx4 v0, s[26:27]
	v_lshl_add_u64 v[168:169], s[26:27], 0, v[132:133]
	s_add_u32 s26, s26, s38
	s_mov_b32 m0, s59
	s_addc_u32 s27, s27, 0
	global_load_lds_dwordx4 v[168:169], off
	s_mov_b32 m0, s64
	s_nop 0
	global_load_lds_dwordx4 v0, s[26:27]
	s_mov_b32 m0, s65
	s_nop 0
	global_load_lds_dwordx4 v132, s[26:27]
	s_mov_b32 m0, s60
	s_nop 0
	global_load_lds_dwordx4 v0, s[24:25]
	s_mov_b32 m0, s62
	s_nop 0
	global_load_lds_dwordx4 v132, s[24:25]
	s_waitcnt vmcnt(8)
	s_waitcnt lgkmcnt(0)
	s_barrier
	s_setprio 1
	s_waitcnt lgkmcnt(0)
	v_mfma_f32_16x16x32_bf16 v[62:65], v[138:141], v[180:183], v[62:65]
	v_mfma_f32_16x16x32_bf16 v[58:61], v[146:149], v[180:183], v[58:61]
	v_mfma_f32_16x16x32_bf16 v[46:49], v[138:141], v[188:191], v[46:49]
	v_mfma_f32_16x16x32_bf16 v[42:45], v[146:149], v[188:191], v[42:45]
	v_mfma_f32_16x16x32_bf16 v[30:33], v[138:141], v[196:199], v[30:33]
	v_mfma_f32_16x16x32_bf16 v[26:29], v[146:149], v[196:199], v[26:29]
	v_mfma_f32_16x16x32_bf16 v[14:17], v[138:141], v[216:219], v[14:17]
	v_mfma_f32_16x16x32_bf16 v[10:13], v[146:149], v[216:219], v[10:13]
	v_mfma_f32_16x16x32_bf16 v[62:65], v[142:145], v[184:187], v[62:65]
	v_mfma_f32_16x16x32_bf16 v[58:61], v[150:153], v[184:187], v[58:61]
	v_mfma_f32_16x16x32_bf16 v[46:49], v[142:145], v[192:195], v[46:49]
	v_mfma_f32_16x16x32_bf16 v[42:45], v[150:153], v[192:195], v[42:45]
	v_mfma_f32_16x16x32_bf16 v[30:33], v[142:145], v[212:215], v[30:33]
	v_mfma_f32_16x16x32_bf16 v[26:29], v[150:153], v[212:215], v[26:29]
	v_mfma_f32_16x16x32_bf16 v[14:17], v[142:145], v[220:223], v[14:17]
	v_mfma_f32_16x16x32_bf16 v[10:13], v[150:153], v[220:223], v[10:13]
	s_setprio 0
	s_setprio 1
	v_mfma_f32_16x16x32_bf16 v[54:57], v[156:159], v[180:183], v[54:57]
	v_mfma_f32_16x16x32_bf16 v[50:53], v[172:175], v[180:183], v[50:53]
	v_mfma_f32_16x16x32_bf16 v[38:41], v[156:159], v[188:191], v[38:41]
	v_mfma_f32_16x16x32_bf16 v[34:37], v[172:175], v[188:191], v[34:37]
	v_mfma_f32_16x16x32_bf16 v[22:25], v[156:159], v[196:199], v[22:25]
	v_mfma_f32_16x16x32_bf16 v[18:21], v[172:175], v[196:199], v[18:21]
	v_mfma_f32_16x16x32_bf16 v[6:9], v[156:159], v[216:219], v[6:9]
	v_mfma_f32_16x16x32_bf16 v[2:5], v[172:175], v[216:219], v[2:5]
	v_mfma_f32_16x16x32_bf16 v[54:57], v[160:163], v[184:187], v[54:57]
	v_mfma_f32_16x16x32_bf16 v[50:53], v[176:179], v[184:187], v[50:53]
	v_mfma_f32_16x16x32_bf16 v[38:41], v[160:163], v[192:195], v[38:41]
	v_mfma_f32_16x16x32_bf16 v[34:37], v[176:179], v[192:195], v[34:37]
	v_mfma_f32_16x16x32_bf16 v[22:25], v[160:163], v[212:215], v[22:25]
	v_mfma_f32_16x16x32_bf16 v[18:21], v[176:179], v[212:215], v[18:21]
	v_mfma_f32_16x16x32_bf16 v[6:9], v[160:163], v[220:223], v[6:9]
	v_mfma_f32_16x16x32_bf16 v[2:5], v[176:179], v[220:223], v[2:5]
	s_setprio 0
	s_barrier
	s_add_i32 s79, s79, 2
	s_cmp_ge_i32 s79, s53
	s_cbranch_scc0 .LBB0_852

.LBB0_1201:
	s_load_dword s14, s[96:97], 0xc0
	v_lshrrev_b32_e32 v3, 1, v0
	v_and_b32_e32 v4, 24, v3
	v_and_b32_e32 v2, 15, v0
	v_lshlrev_b32_e32 v3, 1, v4
	s_waitcnt lgkmcnt(0)
	s_add_i32 s49, s22, s14
	s_add_u32 s14, s16, 0x1ba00000
	s_addc_u32 s15, s17, 0
	s_add_u32 s16, s16, 0x2aa00000
	s_addc_u32 s17, s17, 0
	s_add_i32 s30, s22, 0x100
	s_ashr_i32 s31, s30, 31
	s_lshr_b32 s31, s31, 26
	s_add_i32 s30, s30, s31
	s_ashr_i32 s50, s30, 6
	s_add_i32 s51, s50, -2
	s_and_b64 s[2:3], s[2:3], exec
	s_movk_i32 s2, 0x80
	v_lshlrev_b32_e32 v0, 2, v0
	s_cselect_b32 s52, s2, 0x8000
	v_lshl_or_b32 v165, s28, 6, v2
	v_lshl_or_b32 v2, v2, 6, v3
	s_lshl_b32 s2, s28, 13
	v_and_b32_e32 v0, 32, v0
	v_bitop3_b32 v5, v2, s2, v0 bitop3:0xde
	s_lshl_b32 s2, s25, 5
	s_and_b32 s25, s2, 0x60
	s_lshl_b32 s2, s25, 7
	v_bitop3_b32 v188, s2, v2, v0 bitop3:0xf6
	s_add_u32 s2, s20, s52
	s_addc_u32 s3, s21, 0
	s_add_i32 s54, s24, 0x18000
	v_mov_b32_e32 v175, v1
	s_add_i32 s55, s54, s29
	v_mov_b32_e32 v179, v1
	s_mov_b32 m0, s55
	s_add_i32 s56, s55, 0x2000
	s_waitcnt vmcnt(2)
	s_barrier
	global_load_lds_dwordx4 v174, s[2:3]
	v_lshl_add_u64 v[2:3], s[2:3], 0, v[178:179]
	s_add_u32 s2, s4, s52
	v_mov_b32_e32 v173, v1
	s_mov_b32 m0, s56
	s_addc_u32 s3, s5, 0
	s_add_i32 s57, s45, 0x8000
	v_mov_b32_e32 v177, v1
	global_load_lds_dwordx4 v[2:3], off
	s_mov_b32 m0, s57
	s_add_i32 s58, s45, 0xa000
	global_load_lds_dwordx4 v172, s[2:3]
	v_lshl_add_u64 v[2:3], s[2:3], 0, v[176:177]
	s_add_u32 s2, s18, s52
	s_addc_u32 s3, s19, 0
	s_add_i32 s59, s24, 0x1c000
	s_mov_b32 m0, s58
	s_add_i32 s60, s59, s29
	global_load_lds_dwordx4 v[2:3], off
	s_mov_b32 m0, s60
	s_add_i32 s62, s60, 0x2000
	global_load_lds_dwordx4 v174, s[2:3]
	s_mov_b32 m0, s62
	s_cmpk_gt_i32 s22, 0xff3f
	global_load_lds_dwordx4 v178, s[2:3]
	s_waitcnt vmcnt(6)
	v_mov_b32_e32 v2, v1
	v_mov_b32_e32 v3, v1
	s_cselect_b64 s[18:19], -1, 0
	s_cmpk_lt_u32 s23, 0x100
	v_or_b32_e32 v189, s25, v4
	v_mov_b32_e32 v0, v1
	v_add_u32_e32 v190, s24, v5
	v_mov_b64_e32 v[6:7], v[2:3]
	v_mov_b64_e32 v[10:11], v[2:3]
	v_mov_b64_e32 v[14:15], v[2:3]
	v_mov_b64_e32 v[18:19], v[2:3]
	v_mov_b64_e32 v[22:23], v[2:3]
	v_mov_b64_e32 v[26:27], v[2:3]
	v_mov_b64_e32 v[30:31], v[2:3]
	s_waitcnt vmcnt(0)
	v_mov_b64_e32 v[34:35], v[2:3]
	v_mov_b64_e32 v[38:39], v[2:3]
	v_mov_b64_e32 v[42:43], v[2:3]
	v_mov_b64_e32 v[46:47], v[2:3]
	v_mov_b64_e32 v[54:55], v[2:3]
	v_mov_b64_e32 v[50:51], v[2:3]
	v_mov_b64_e32 v[58:59], v[2:3]
	v_mov_b64_e32 v[62:63], v[2:3]
	v_mov_b64_e32 v[66:67], v[2:3]
	v_mov_b64_e32 v[70:71], v[2:3]
	v_mov_b64_e32 v[74:75], v[2:3]
	v_mov_b64_e32 v[78:79], v[2:3]
	v_mov_b64_e32 v[82:83], v[2:3]
	v_mov_b64_e32 v[86:87], v[2:3]
	v_mov_b64_e32 v[90:91], v[2:3]
	v_mov_b64_e32 v[94:95], v[2:3]
	v_mov_b64_e32 v[98:99], v[2:3]
	v_mov_b64_e32 v[102:103], v[2:3]
	v_mov_b64_e32 v[106:107], v[2:3]
	v_mov_b64_e32 v[110:111], v[2:3]
	v_mov_b64_e32 v[114:115], v[2:3]
	v_mov_b64_e32 v[118:119], v[2:3]
	v_mov_b64_e32 v[122:123], v[2:3]
	v_mov_b64_e32 v[126:127], v[2:3]
	v_mov_b64_e32 v[130:131], v[2:3]
	s_mov_b32 s53, 0
	s_cselect_b64 s[20:21], -1, 0
	s_ashr_i32 s64, s33, 31
	v_mov_b64_e32 v[4:5], v[0:1]
	v_mov_b64_e32 v[8:9], v[0:1]
	v_mov_b64_e32 v[12:13], v[0:1]
	v_mov_b64_e32 v[16:17], v[0:1]
	v_mov_b64_e32 v[20:21], v[0:1]
	v_mov_b64_e32 v[24:25], v[0:1]
	v_mov_b64_e32 v[28:29], v[0:1]
	v_mov_b64_e32 v[32:33], v[0:1]
	v_mov_b64_e32 v[36:37], v[0:1]
	v_mov_b64_e32 v[40:41], v[0:1]
	v_mov_b64_e32 v[44:45], v[0:1]
	v_mov_b64_e32 v[52:53], v[0:1]
	v_mov_b64_e32 v[48:49], v[0:1]
	v_mov_b64_e32 v[56:57], v[0:1]
	v_mov_b64_e32 v[60:61], v[0:1]
	v_mov_b64_e32 v[64:65], v[0:1]
	v_mov_b64_e32 v[68:69], v[0:1]
	v_mov_b64_e32 v[72:73], v[0:1]
	v_mov_b64_e32 v[76:77], v[0:1]
	v_mov_b64_e32 v[80:81], v[0:1]
	v_mov_b64_e32 v[84:85], v[0:1]
	v_mov_b64_e32 v[88:89], v[0:1]
	v_mov_b64_e32 v[92:93], v[0:1]
	v_mov_b64_e32 v[96:97], v[0:1]
	v_mov_b64_e32 v[100:101], v[0:1]
	v_mov_b64_e32 v[104:105], v[0:1]
	v_mov_b64_e32 v[108:109], v[0:1]
	v_mov_b64_e32 v[112:113], v[0:1]
	v_mov_b64_e32 v[116:117], v[0:1]
	v_mov_b64_e32 v[120:121], v[0:1]
	v_mov_b64_e32 v[124:125], v[0:1]
	v_mov_b64_e32 v[128:129], v[0:1]
	s_barrier
	s_branch .LBB0_1204

.LBB0_1216:
	s_add_i32 s28, s0, s74
	s_add_i32 s4, s28, 1
	s_cmp_ge_i32 s4, s50
	s_cselect_b32 s5, s50, 0
	s_sub_i32 s4, s4, s5
	s_ashr_i32 s5, s4, 31
	s_lshl_b64 s[76:77], s[4:5], s39
	s_add_i32 s28, s28, 2
	s_cmp_ge_i32 s28, s50
	s_cselect_b32 s4, s50, 0
	s_sub_i32 s4, s28, s4
	s_ashr_i32 s5, s4, 31
	v_add_u32_e32 v0, s1, v188
	s_lshl_b64 s[4:5], s[4:5], s39
	ds_read_b128 v[132:135], v0
	ds_read_b128 v[136:139], v0 offset:1024
	ds_read_b128 v[140:143], v0 offset:2048
	ds_read_b128 v[144:147], v0 offset:3072
	v_add_u32_e32 v0, s42, v188
	s_add_u32 s28, s6, s4
	ds_read_b128 v[148:151], v0
	ds_read_b128 v[152:155], v0 offset:1024
	ds_read_b128 v[156:159], v0 offset:2048
	ds_read_b128 v[160:163], v0 offset:3072
	s_addc_u32 s29, s7, s5
	s_add_u32 s4, s26, s4
	s_addc_u32 s5, s27, s5
	s_cmp_eq_u32 s51, s74
	s_cselect_b32 s30, s70, s28
	s_cselect_b32 s31, s71, s29
	s_cselect_b32 s29, s73, s5
	s_cselect_b32 s28, s72, s4
	s_add_u32 s4, s30, s52
	s_addc_u32 s5, s31, 0
	s_add_u32 s76, s68, s76
	s_addc_u32 s77, s69, s77
	s_add_i32 m0, s45, 0xc000
	ds_read_b128 v[180:183], v190
	ds_read_b128 v[184:187], v190 offset:1024
	ds_read_b128 v[192:195], v190 offset:2048
	ds_read_b128 v[196:199], v190 offset:3072
	ds_read_b128 v[212:215], v190 offset:4096
	ds_read_b128 v[216:219], v190 offset:5120
	ds_read_b128 v[220:223], v190 offset:6144
	ds_read_b128 v[224:227], v190 offset:7168
	global_load_lds_dwordx4 v172, s[76:77]
	s_add_i32 m0, s45, 0xe000
	s_nop 0
	global_load_lds_dwordx4 v176, s[76:77]
	s_waitcnt vmcnt(8)
	s_waitcnt lgkmcnt(0)
	s_barrier
	s_setprio 1
	s_waitcnt lgkmcnt(0)
	v_mfma_f32_16x16x32_bf16 v[112:115], v[132:135], v[180:183], v[112:115]
	v_mfma_f32_16x16x32_bf16 v[108:111], v[140:143], v[180:183], v[108:111]
	v_mfma_f32_16x16x32_bf16 v[104:107], v[132:135], v[192:195], v[104:107]
	v_mfma_f32_16x16x32_bf16 v[100:103], v[140:143], v[192:195], v[100:103]
	v_mfma_f32_16x16x32_bf16 v[96:99], v[132:135], v[212:215], v[96:99]
	v_mfma_f32_16x16x32_bf16 v[92:95], v[140:143], v[212:215], v[92:95]
	v_mfma_f32_16x16x32_bf16 v[88:91], v[132:135], v[220:223], v[88:91]
	v_mfma_f32_16x16x32_bf16 v[84:87], v[140:143], v[220:223], v[84:87]
	v_mfma_f32_16x16x32_bf16 v[112:115], v[136:139], v[184:187], v[112:115]
	v_mfma_f32_16x16x32_bf16 v[108:111], v[144:147], v[184:187], v[108:111]
	v_mfma_f32_16x16x32_bf16 v[104:107], v[136:139], v[196:199], v[104:107]
	v_mfma_f32_16x16x32_bf16 v[100:103], v[144:147], v[196:199], v[100:103]
	v_mfma_f32_16x16x32_bf16 v[96:99], v[136:139], v[216:219], v[96:99]
	v_mfma_f32_16x16x32_bf16 v[92:95], v[144:147], v[216:219], v[92:95]
	v_mfma_f32_16x16x32_bf16 v[88:91], v[136:139], v[224:227], v[88:91]
	v_mfma_f32_16x16x32_bf16 v[84:87], v[144:147], v[224:227], v[84:87]
	s_setprio 0
	s_setprio 1
	v_mfma_f32_16x16x32_bf16 v[80:83], v[148:151], v[180:183], v[80:83]
	v_mfma_f32_16x16x32_bf16 v[76:79], v[156:159], v[180:183], v[76:79]
	v_mfma_f32_16x16x32_bf16 v[72:75], v[148:151], v[192:195], v[72:75]
	v_mfma_f32_16x16x32_bf16 v[68:71], v[156:159], v[192:195], v[68:71]
	v_mfma_f32_16x16x32_bf16 v[64:67], v[148:151], v[212:215], v[64:67]
	v_mfma_f32_16x16x32_bf16 v[60:63], v[156:159], v[212:215], v[60:63]
	v_mfma_f32_16x16x32_bf16 v[56:59], v[148:151], v[220:223], v[56:59]
	v_mfma_f32_16x16x32_bf16 v[48:51], v[156:159], v[220:223], v[48:51]
	v_mfma_f32_16x16x32_bf16 v[80:83], v[152:155], v[184:187], v[80:83]
	v_mfma_f32_16x16x32_bf16 v[76:79], v[160:163], v[184:187], v[76:79]
	v_mfma_f32_16x16x32_bf16 v[72:75], v[152:155], v[196:199], v[72:75]
	v_mfma_f32_16x16x32_bf16 v[68:71], v[160:163], v[196:199], v[68:71]
	v_mfma_f32_16x16x32_bf16 v[64:67], v[152:155], v[216:219], v[64:67]
	v_mfma_f32_16x16x32_bf16 v[60:63], v[160:163], v[216:219], v[60:63]
	v_mfma_f32_16x16x32_bf16 v[56:59], v[152:155], v[224:227], v[56:59]
	v_mfma_f32_16x16x32_bf16 v[48:51], v[160:163], v[224:227], v[48:51]
	s_setprio 0
	s_barrier
	s_mov_b32 m0, s40
	s_add_u32 s76, s28, s38
	ds_read_b128 v[180:183], v190 offset:16384
	ds_read_b128 v[184:187], v190 offset:17408
	ds_read_b128 v[192:195], v190 offset:18432
	ds_read_b128 v[196:199], v190 offset:19456
	ds_read_b128 v[212:215], v190 offset:20480
	ds_read_b128 v[216:219], v190 offset:21504
	ds_read_b128 v[220:223], v190 offset:22528
	ds_read_b128 v[224:227], v190 offset:23552
	global_load_lds_dwordx4 v174, s[28:29]
	s_mov_b32 m0, s41
	s_addc_u32 s77, s29, 0
	global_load_lds_dwordx4 v178, s[28:29]
	s_mov_b32 m0, s43
	s_nop 0
	global_load_lds_dwordx4 v174, s[76:77]
	s_mov_b32 m0, s44
	s_nop 0
	global_load_lds_dwordx4 v178, s[76:77]
	s_mov_b32 m0, s45
	s_nop 0
	global_load_lds_dwordx4 v172, s[30:31]
	s_mov_b32 m0, s46
	s_nop 0
	global_load_lds_dwordx4 v176, s[30:31]
	s_waitcnt vmcnt(8)
	s_waitcnt lgkmcnt(0)
	s_barrier
	s_setprio 1
	s_waitcnt lgkmcnt(0)
	v_mfma_f32_16x16x32_bf16 v[52:55], v[132:135], v[180:183], v[52:55]
	v_mfma_f32_16x16x32_bf16 v[44:47], v[140:143], v[180:183], v[44:47]
	v_mfma_f32_16x16x32_bf16 v[40:43], v[132:135], v[192:195], v[40:43]
	v_mfma_f32_16x16x32_bf16 v[36:39], v[140:143], v[192:195], v[36:39]
	v_mfma_f32_16x16x32_bf16 v[32:35], v[132:135], v[212:215], v[32:35]
	v_mfma_f32_16x16x32_bf16 v[28:31], v[140:143], v[212:215], v[28:31]
	v_mfma_f32_16x16x32_bf16 v[24:27], v[132:135], v[220:223], v[24:27]
	v_mfma_f32_16x16x32_bf16 v[20:23], v[140:143], v[220:223], v[20:23]
	v_mfma_f32_16x16x32_bf16 v[52:55], v[136:139], v[184:187], v[52:55]
	v_mfma_f32_16x16x32_bf16 v[44:47], v[144:147], v[184:187], v[44:47]
	v_mfma_f32_16x16x32_bf16 v[40:43], v[136:139], v[196:199], v[40:43]
	v_mfma_f32_16x16x32_bf16 v[36:39], v[144:147], v[196:199], v[36:39]
	v_mfma_f32_16x16x32_bf16 v[32:35], v[136:139], v[216:219], v[32:35]
	v_mfma_f32_16x16x32_bf16 v[28:31], v[144:147], v[216:219], v[28:31]
	v_mfma_f32_16x16x32_bf16 v[24:27], v[136:139], v[224:227], v[24:27]
	v_mfma_f32_16x16x32_bf16 v[20:23], v[144:147], v[224:227], v[20:23]
	s_setprio 0
	s_setprio 1
	v_mfma_f32_16x16x32_bf16 v[16:19], v[148:151], v[180:183], v[16:19]
	v_mfma_f32_16x16x32_bf16 v[12:15], v[156:159], v[180:183], v[12:15]
	v_mfma_f32_16x16x32_bf16 v[8:11], v[148:151], v[192:195], v[8:11]
	v_mfma_f32_16x16x32_bf16 v[2:5], v[156:159], v[192:195], v[4:7]
	v_mfma_f32_16x16x32_bf16 v[116:119], v[148:151], v[212:215], v[116:119]
	v_mfma_f32_16x16x32_bf16 v[120:123], v[156:159], v[212:215], v[120:123]
	v_mfma_f32_16x16x32_bf16 v[124:127], v[148:151], v[220:223], v[124:127]
	v_mfma_f32_16x16x32_bf16 v[128:131], v[156:159], v[220:223], v[128:131]
	v_mfma_f32_16x16x32_bf16 v[16:19], v[152:155], v[184:187], v[16:19]
	v_mfma_f32_16x16x32_bf16 v[12:15], v[160:163], v[184:187], v[12:15]
	v_mfma_f32_16x16x32_bf16 v[8:11], v[152:155], v[196:199], v[8:11]
	v_mfma_f32_16x16x32_bf16 v[2:5], v[160:163], v[196:199], v[2:5]
	v_mfma_f32_16x16x32_bf16 v[116:119], v[152:155], v[216:219], v[116:119]
	v_mfma_f32_16x16x32_bf16 v[120:123], v[160:163], v[216:219], v[120:123]
	v_mfma_f32_16x16x32_bf16 v[124:127], v[152:155], v[224:227], v[124:127]
	v_mfma_f32_16x16x32_bf16 v[128:131], v[160:163], v[224:227], v[128:131]
	s_setprio 0
	s_barrier
	v_add_u32_e32 v0, s54, v188
	ds_read_b128 v[132:135], v0
	ds_read_b128 v[136:139], v0 offset:1024
	ds_read_b128 v[140:143], v0 offset:2048
	ds_read_b128 v[144:147], v0 offset:3072
	v_add_u32_e32 v0, s59, v188
	ds_read_b128 v[148:151], v0
	ds_read_b128 v[152:155], v0 offset:1024
	ds_read_b128 v[156:159], v0 offset:2048
	ds_read_b128 v[160:163], v0 offset:3072
	s_add_u32 s30, s30, s38
	s_addc_u32 s31, s31, 0
	s_mov_b32 m0, s47
	ds_read_b128 v[180:183], v190 offset:32768
	ds_read_b128 v[184:187], v190 offset:33792
	ds_read_b128 v[192:195], v190 offset:34816
	ds_read_b128 v[196:199], v190 offset:35840
	ds_read_b128 v[212:215], v190 offset:36864
	ds_read_b128 v[216:219], v190 offset:37888
	ds_read_b128 v[220:223], v190 offset:38912
	ds_read_b128 v[224:227], v190 offset:39936
	global_load_lds_dwordx4 v172, s[30:31]
	s_mov_b32 m0, s48
	s_nop 0
	global_load_lds_dwordx4 v176, s[30:31]
	s_waitcnt vmcnt(8)
	s_waitcnt lgkmcnt(0)
	s_barrier
	s_setprio 1
	s_waitcnt lgkmcnt(0)
	v_mfma_f32_16x16x32_bf16 v[112:115], v[132:135], v[180:183], v[112:115]
	v_mfma_f32_16x16x32_bf16 v[108:111], v[140:143], v[180:183], v[108:111]
	v_mfma_f32_16x16x32_bf16 v[104:107], v[132:135], v[192:195], v[104:107]
	v_mfma_f32_16x16x32_bf16 v[100:103], v[140:143], v[192:195], v[100:103]
	v_mfma_f32_16x16x32_bf16 v[96:99], v[132:135], v[212:215], v[96:99]
	v_mfma_f32_16x16x32_bf16 v[92:95], v[140:143], v[212:215], v[92:95]
	v_mfma_f32_16x16x32_bf16 v[88:91], v[132:135], v[220:223], v[88:91]
	v_mfma_f32_16x16x32_bf16 v[84:87], v[140:143], v[220:223], v[84:87]
	v_mfma_f32_16x16x32_bf16 v[112:115], v[136:139], v[184:187], v[112:115]
	v_mfma_f32_16x16x32_bf16 v[108:111], v[144:147], v[184:187], v[108:111]
	v_mfma_f32_16x16x32_bf16 v[104:107], v[136:139], v[196:199], v[104:107]
	v_mfma_f32_16x16x32_bf16 v[100:103], v[144:147], v[196:199], v[100:103]
	v_mfma_f32_16x16x32_bf16 v[96:99], v[136:139], v[216:219], v[96:99]
	v_mfma_f32_16x16x32_bf16 v[92:95], v[144:147], v[216:219], v[92:95]
	v_mfma_f32_16x16x32_bf16 v[88:91], v[136:139], v[224:227], v[88:91]
	v_mfma_f32_16x16x32_bf16 v[84:87], v[144:147], v[224:227], v[84:87]
	s_setprio 0
	s_setprio 1
	v_mfma_f32_16x16x32_bf16 v[80:83], v[148:151], v[180:183], v[80:83]
	v_mfma_f32_16x16x32_bf16 v[76:79], v[156:159], v[180:183], v[76:79]
	v_mfma_f32_16x16x32_bf16 v[72:75], v[148:151], v[192:195], v[72:75]
	v_mfma_f32_16x16x32_bf16 v[68:71], v[156:159], v[192:195], v[68:71]
	v_mfma_f32_16x16x32_bf16 v[64:67], v[148:151], v[212:215], v[64:67]
	v_mfma_f32_16x16x32_bf16 v[60:63], v[156:159], v[212:215], v[60:63]
	v_mfma_f32_16x16x32_bf16 v[56:59], v[148:151], v[220:223], v[56:59]
	v_mfma_f32_16x16x32_bf16 v[48:51], v[156:159], v[220:223], v[48:51]
	v_mfma_f32_16x16x32_bf16 v[80:83], v[152:155], v[184:187], v[80:83]
	v_mfma_f32_16x16x32_bf16 v[76:79], v[160:163], v[184:187], v[76:79]
	v_mfma_f32_16x16x32_bf16 v[72:75], v[152:155], v[196:199], v[72:75]
	v_mfma_f32_16x16x32_bf16 v[68:71], v[160:163], v[196:199], v[68:71]
	v_mfma_f32_16x16x32_bf16 v[64:67], v[152:155], v[216:219], v[64:67]
	v_mfma_f32_16x16x32_bf16 v[60:63], v[160:163], v[216:219], v[60:63]
	v_mfma_f32_16x16x32_bf16 v[56:59], v[152:155], v[224:227], v[56:59]
	v_mfma_f32_16x16x32_bf16 v[48:51], v[160:163], v[224:227], v[48:51]
	s_setprio 0
	s_barrier
	s_add_u32 s28, s28, s52
	s_addc_u32 s29, s29, 0
	s_mov_b32 m0, s55
	ds_read_b128 v[180:183], v190 offset:49152
	ds_read_b128 v[184:187], v190 offset:50176
	ds_read_b128 v[192:195], v190 offset:51200
	ds_read_b128 v[196:199], v190 offset:52224
	ds_read_b128 v[212:215], v190 offset:53248
	ds_read_b128 v[216:219], v190 offset:54272
	ds_read_b128 v[220:223], v190 offset:55296
	ds_read_b128 v[224:227], v190 offset:56320
	global_load_lds_dwordx4 v174, s[28:29]
	v_lshl_add_u64 v[6:7], s[28:29], 0, v[178:179]
	s_add_u32 s28, s28, s38
	s_mov_b32 m0, s56
	s_addc_u32 s29, s29, 0
	global_load_lds_dwordx4 v[6:7], off
	s_mov_b32 m0, s60
	s_nop 0
	global_load_lds_dwordx4 v174, s[28:29]
	s_mov_b32 m0, s62
	s_nop 0
	global_load_lds_dwordx4 v178, s[28:29]
	s_mov_b32 m0, s57
	s_nop 0
	global_load_lds_dwordx4 v172, s[4:5]
	s_mov_b32 m0, s58
	s_nop 0
	global_load_lds_dwordx4 v176, s[4:5]
	s_waitcnt vmcnt(8)
	s_waitcnt lgkmcnt(0)
	s_barrier
	s_setprio 1
	s_waitcnt lgkmcnt(0)
	v_mfma_f32_16x16x32_bf16 v[52:55], v[132:135], v[180:183], v[52:55]
	v_mfma_f32_16x16x32_bf16 v[44:47], v[140:143], v[180:183], v[44:47]
	v_mfma_f32_16x16x32_bf16 v[40:43], v[132:135], v[192:195], v[40:43]
	v_mfma_f32_16x16x32_bf16 v[36:39], v[140:143], v[192:195], v[36:39]
	v_mfma_f32_16x16x32_bf16 v[32:35], v[132:135], v[212:215], v[32:35]
	v_mfma_f32_16x16x32_bf16 v[28:31], v[140:143], v[212:215], v[28:31]
	v_mfma_f32_16x16x32_bf16 v[24:27], v[132:135], v[220:223], v[24:27]
	v_mfma_f32_16x16x32_bf16 v[20:23], v[140:143], v[220:223], v[20:23]
	v_mfma_f32_16x16x32_bf16 v[52:55], v[136:139], v[184:187], v[52:55]
	v_mfma_f32_16x16x32_bf16 v[44:47], v[144:147], v[184:187], v[44:47]
	v_mfma_f32_16x16x32_bf16 v[40:43], v[136:139], v[196:199], v[40:43]
	v_mfma_f32_16x16x32_bf16 v[36:39], v[144:147], v[196:199], v[36:39]
	v_mfma_f32_16x16x32_bf16 v[32:35], v[136:139], v[216:219], v[32:35]
	v_mfma_f32_16x16x32_bf16 v[28:31], v[144:147], v[216:219], v[28:31]
	v_mfma_f32_16x16x32_bf16 v[24:27], v[136:139], v[224:227], v[24:27]
	v_mfma_f32_16x16x32_bf16 v[20:23], v[144:147], v[224:227], v[20:23]
	s_setprio 0
	s_setprio 1
	v_mfma_f32_16x16x32_bf16 v[16:19], v[148:151], v[180:183], v[16:19]
	v_mfma_f32_16x16x32_bf16 v[12:15], v[156:159], v[180:183], v[12:15]
	v_mfma_f32_16x16x32_bf16 v[6:9], v[148:151], v[192:195], v[8:11]
	v_mfma_f32_16x16x32_bf16 v[2:5], v[156:159], v[192:195], v[2:5]
	v_mfma_f32_16x16x32_bf16 v[116:119], v[148:151], v[212:215], v[116:119]
	v_mfma_f32_16x16x32_bf16 v[120:123], v[156:159], v[212:215], v[120:123]
	v_mfma_f32_16x16x32_bf16 v[124:127], v[148:151], v[220:223], v[124:127]
	v_mfma_f32_16x16x32_bf16 v[128:131], v[156:159], v[220:223], v[128:131]
	v_mfma_f32_16x16x32_bf16 v[16:19], v[152:155], v[184:187], v[16:19]
	v_mfma_f32_16x16x32_bf16 v[12:15], v[160:163], v[184:187], v[12:15]
	v_mfma_f32_16x16x32_bf16 v[8:11], v[152:155], v[196:199], v[6:9]
	v_mfma_f32_16x16x32_bf16 v[4:7], v[160:163], v[196:199], v[2:5]
	v_mfma_f32_16x16x32_bf16 v[116:119], v[152:155], v[216:219], v[116:119]
	v_mfma_f32_16x16x32_bf16 v[120:123], v[160:163], v[216:219], v[120:123]
	v_mfma_f32_16x16x32_bf16 v[124:127], v[152:155], v[224:227], v[124:127]
	v_mfma_f32_16x16x32_bf16 v[128:131], v[160:163], v[224:227], v[128:131]
	s_setprio 0
	s_barrier
	s_add_i32 s74, s74, 2
	s_cmp_ge_i32 s74, s50
	s_cbranch_scc0 .LBB0_1216

.LBB0_1449:
	s_lshl_b32 s16, s60, 1
	s_add_u32 s14, s14, s16
	s_addc_u32 s15, s15, 0
	s_add_u32 s14, s14, 0x32000000
	v_readlane_b32 s16, v254, 6
	s_addc_u32 s15, s15, 0
	v_readlane_b32 s17, v254, 7
	s_and_b64 s[16:17], s[16:17], exec
	s_cselect_b32 s17, s3, 0
	s_cselect_b32 s16, s2, 0
	s_add_i32 s2, s0, 0x400
	s_ashr_i32 s3, s2, 31
	s_lshr_b32 s3, s3, 26
	s_add_i32 s2, s2, s3
	s_ashr_i32 s52, s2, 6
	s_add_i32 s53, s52, -2
	s_and_b64 s[2:3], s[18:19], exec
	s_movk_i32 s2, 0x80
	s_cselect_b32 s54, s2, 0x8000
	s_lshl_b32 s2, s31, 5
	s_and_b32 s31, s2, 0x60
	s_load_dword s2, s[96:97], 0xc0
	s_lshl_b32 s18, s1, 13
	s_lshl_b32 s19, s31, 7
	v_mov_b32_e32 v163, v1
	s_waitcnt vmcnt(2)
	s_waitcnt lgkmcnt(0)
	s_add_i32 s55, s0, s2
	s_add_u32 s2, s24, s54
	s_addc_u32 s3, s25, 0
	s_add_i32 s56, s29, 0x18000
	s_add_i32 s57, s56, s30
	s_mov_b32 m0, s57
	s_add_i32 s58, s57, 0x2000
	s_barrier
	global_load_lds_dwordx4 v0, s[2:3]
	v_lshl_add_u64 v[4:5], s[2:3], 0, v[162:163]
	s_add_u32 s2, s20, s54
	s_mov_b32 m0, s58
	s_addc_u32 s3, s21, 0
	s_add_i32 s59, s48, 0x8000
	global_load_lds_dwordx4 v[4:5], off
	s_mov_b32 m0, s59
	s_add_i32 s60, s48, 0xa000
	global_load_lds_dwordx4 v0, s[2:3]
	v_lshl_add_u64 v[4:5], s[2:3], 0, v[162:163]
	s_add_u32 s2, s22, s54
	s_addc_u32 s3, s23, 0
	s_add_i32 s62, s29, 0x1c000
	s_mov_b32 m0, s60
	s_add_i32 s63, s62, s30
	global_load_lds_dwordx4 v[4:5], off
	s_mov_b32 m0, s63
	s_add_i32 s64, s63, 0x2000
	global_load_lds_dwordx4 v0, s[2:3]
	s_mov_b32 m0, s64
	v_bfe_u32 v3, v2, 4, 2
	global_load_lds_dwordx4 v162, s[2:3]
	v_and_b32_e32 v4, 15, v2
	v_lshlrev_b32_e32 v5, 4, v3
	v_lshlrev_b32_e32 v2, 2, v2
	v_lshl_or_b32 v186, s1, 6, v4
	v_lshl_or_b32 v4, v4, 6, v5
	v_and_b32_e32 v2, 32, v2
	s_cmpk_gt_i32 s0, 0xfc3f
	v_bitop3_b32 v5, v4, s18, v2 bitop3:0xde
	v_bitop3_b32 v187, s19, v4, v2 bitop3:0xf6
	s_waitcnt vmcnt(6)
	s_cselect_b64 s[18:19], -1, 0
	s_cmpk_lt_u32 s28, 0x100
	s_cselect_b64 s[20:21], -1, 0
	s_cmp_lg_u64 s[16:17], 0
	s_mov_b32 s65, 0
	s_cselect_b64 s[22:23], -1, 0
	s_ashr_i32 s66, s55, 31
	s_ashr_i32 s67, s36, 31
	v_lshl_or_b32 v188, v3, 2, s31
	v_add_u32_e32 v189, s29, v5
	s_barrier
	s_branch .LBB0_1452

.LBB0_1464:
	s_add_i32 s30, s6, s78
	s_add_i32 s28, s30, 1
	s_cmp_ge_i32 s28, s52
	s_cselect_b32 s29, s52, 0
	s_sub_i32 s28, s28, s29
	s_ashr_i32 s29, s28, 31
	s_lshl_b64 s[80:81], s[28:29], s42
	s_add_i32 s30, s30, 2
	s_cmp_ge_i32 s30, s52
	s_cselect_b32 s28, s52, 0
	s_sub_i32 s28, s30, s28
	s_ashr_i32 s29, s28, 31
	s_lshl_b64 s[28:29], s[28:29], s42
	v_add_u32_e32 v142, s7, v187
	v_add_u32_e32 v158, s45, v187
	s_add_u32 s30, s4, s28
	ds_read_b128 v[130:133], v142
	ds_read_b128 v[134:137], v142 offset:1024
	ds_read_b128 v[138:141], v142 offset:2048
	ds_read_b128 v[142:145], v142 offset:3072
	ds_read_b128 v[146:149], v158
	ds_read_b128 v[150:153], v158 offset:1024
	ds_read_b128 v[154:157], v158 offset:2048
	ds_read_b128 v[158:161], v158 offset:3072
	s_addc_u32 s31, s5, s29
	s_add_u32 s28, s26, s28
	s_addc_u32 s29, s27, s29
	s_cmp_eq_u32 s53, s78
	s_cselect_b32 s34, s74, s30
	s_cselect_b32 s35, s75, s31
	s_cselect_b32 s31, s77, s29
	s_cselect_b32 s30, s76, s28
	s_add_u32 s28, s34, s54
	s_addc_u32 s29, s35, 0
	s_add_u32 s80, s72, s80
	s_addc_u32 s81, s73, s81
	s_add_i32 m0, s48, 0xc000
	ds_read_b128 v[172:175], v189
	ds_read_b128 v[176:179], v189 offset:1024
	ds_read_b128 v[180:183], v189 offset:2048
	ds_read_b128 v[190:193], v189 offset:3072
	ds_read_b128 v[194:197], v189 offset:4096
	ds_read_b128 v[212:215], v189 offset:5120
	ds_read_b128 v[216:219], v189 offset:6144
	ds_read_b128 v[220:223], v189 offset:7168
	global_load_lds_dwordx4 v0, s[80:81]
	s_add_i32 m0, s48, 0xe000
	s_nop 0
	global_load_lds_dwordx4 v162, s[80:81]
	s_waitcnt vmcnt(8)
	s_waitcnt lgkmcnt(0)
	s_barrier
	s_setprio 1
	s_waitcnt lgkmcnt(0)
	v_mfma_f32_16x16x32_bf16 v[126:129], v[130:133], v[172:175], v[126:129]
	v_mfma_f32_16x16x32_bf16 v[122:125], v[138:141], v[172:175], v[122:125]
	v_mfma_f32_16x16x32_bf16 v[110:113], v[130:133], v[180:183], v[110:113]
	v_mfma_f32_16x16x32_bf16 v[106:109], v[138:141], v[180:183], v[106:109]
	v_mfma_f32_16x16x32_bf16 v[94:97], v[130:133], v[194:197], v[94:97]
	v_mfma_f32_16x16x32_bf16 v[90:93], v[138:141], v[194:197], v[90:93]
	v_mfma_f32_16x16x32_bf16 v[78:81], v[130:133], v[216:219], v[78:81]
	v_mfma_f32_16x16x32_bf16 v[74:77], v[138:141], v[216:219], v[74:77]
	v_mfma_f32_16x16x32_bf16 v[126:129], v[134:137], v[176:179], v[126:129]
	v_mfma_f32_16x16x32_bf16 v[122:125], v[142:145], v[176:179], v[122:125]
	v_mfma_f32_16x16x32_bf16 v[110:113], v[134:137], v[190:193], v[110:113]
	v_mfma_f32_16x16x32_bf16 v[106:109], v[142:145], v[190:193], v[106:109]
	v_mfma_f32_16x16x32_bf16 v[94:97], v[134:137], v[212:215], v[94:97]
	v_mfma_f32_16x16x32_bf16 v[90:93], v[142:145], v[212:215], v[90:93]
	v_mfma_f32_16x16x32_bf16 v[78:81], v[134:137], v[220:223], v[78:81]
	v_mfma_f32_16x16x32_bf16 v[74:77], v[142:145], v[220:223], v[74:77]
	s_setprio 0
	s_setprio 1
	v_mfma_f32_16x16x32_bf16 v[118:121], v[146:149], v[172:175], v[118:121]
	v_mfma_f32_16x16x32_bf16 v[114:117], v[154:157], v[172:175], v[114:117]
	v_mfma_f32_16x16x32_bf16 v[102:105], v[146:149], v[180:183], v[102:105]
	v_mfma_f32_16x16x32_bf16 v[98:101], v[154:157], v[180:183], v[98:101]
	v_mfma_f32_16x16x32_bf16 v[86:89], v[146:149], v[194:197], v[86:89]
	v_mfma_f32_16x16x32_bf16 v[82:85], v[154:157], v[194:197], v[82:85]
	v_mfma_f32_16x16x32_bf16 v[70:73], v[146:149], v[216:219], v[70:73]
	v_mfma_f32_16x16x32_bf16 v[66:69], v[154:157], v[216:219], v[66:69]
	v_mfma_f32_16x16x32_bf16 v[118:121], v[150:153], v[176:179], v[118:121]
	v_mfma_f32_16x16x32_bf16 v[114:117], v[158:161], v[176:179], v[114:117]
	v_mfma_f32_16x16x32_bf16 v[102:105], v[150:153], v[190:193], v[102:105]
	v_mfma_f32_16x16x32_bf16 v[98:101], v[158:161], v[190:193], v[98:101]
	v_mfma_f32_16x16x32_bf16 v[86:89], v[150:153], v[212:215], v[86:89]
	v_mfma_f32_16x16x32_bf16 v[82:85], v[158:161], v[212:215], v[82:85]
	v_mfma_f32_16x16x32_bf16 v[70:73], v[150:153], v[220:223], v[70:73]
	v_mfma_f32_16x16x32_bf16 v[66:69], v[158:161], v[220:223], v[66:69]
	s_setprio 0
	s_barrier
	s_mov_b32 m0, s43
	s_add_u32 s80, s30, s41
	ds_read_b128 v[172:175], v189 offset:16384
	ds_read_b128 v[176:179], v189 offset:17408
	ds_read_b128 v[180:183], v189 offset:18432
	ds_read_b128 v[190:193], v189 offset:19456
	ds_read_b128 v[194:197], v189 offset:20480
	ds_read_b128 v[212:215], v189 offset:21504
	ds_read_b128 v[216:219], v189 offset:22528
	ds_read_b128 v[220:223], v189 offset:23552
	global_load_lds_dwordx4 v0, s[30:31]
	s_mov_b32 m0, s44
	s_addc_u32 s81, s31, 0
	global_load_lds_dwordx4 v162, s[30:31]
	s_mov_b32 m0, s46
	s_nop 0
	global_load_lds_dwordx4 v0, s[80:81]
	s_mov_b32 m0, s47
	s_nop 0
	global_load_lds_dwordx4 v162, s[80:81]
	s_mov_b32 m0, s48
	s_nop 0
	global_load_lds_dwordx4 v0, s[34:35]
	s_mov_b32 m0, s49
	s_nop 0
	global_load_lds_dwordx4 v162, s[34:35]
	s_waitcnt vmcnt(8)
	s_waitcnt lgkmcnt(0)
	s_barrier
	s_setprio 1
	s_waitcnt lgkmcnt(0)
	v_mfma_f32_16x16x32_bf16 v[62:65], v[130:133], v[172:175], v[62:65]
	v_mfma_f32_16x16x32_bf16 v[58:61], v[138:141], v[172:175], v[58:61]
	v_mfma_f32_16x16x32_bf16 v[46:49], v[130:133], v[180:183], v[46:49]
	v_mfma_f32_16x16x32_bf16 v[42:45], v[138:141], v[180:183], v[42:45]
	v_mfma_f32_16x16x32_bf16 v[30:33], v[130:133], v[194:197], v[30:33]
	v_mfma_f32_16x16x32_bf16 v[26:29], v[138:141], v[194:197], v[26:29]
	v_mfma_f32_16x16x32_bf16 v[14:17], v[130:133], v[216:219], v[14:17]
	v_mfma_f32_16x16x32_bf16 v[10:13], v[138:141], v[216:219], v[10:13]
	v_mfma_f32_16x16x32_bf16 v[62:65], v[134:137], v[176:179], v[62:65]
	v_mfma_f32_16x16x32_bf16 v[58:61], v[142:145], v[176:179], v[58:61]
	v_mfma_f32_16x16x32_bf16 v[46:49], v[134:137], v[190:193], v[46:49]
	v_mfma_f32_16x16x32_bf16 v[42:45], v[142:145], v[190:193], v[42:45]
	v_mfma_f32_16x16x32_bf16 v[30:33], v[134:137], v[212:215], v[30:33]
	v_mfma_f32_16x16x32_bf16 v[26:29], v[142:145], v[212:215], v[26:29]
	v_mfma_f32_16x16x32_bf16 v[14:17], v[134:137], v[220:223], v[14:17]
	v_mfma_f32_16x16x32_bf16 v[10:13], v[142:145], v[220:223], v[10:13]
	s_setprio 0
	s_setprio 1
	v_mfma_f32_16x16x32_bf16 v[54:57], v[146:149], v[172:175], v[54:57]
	v_mfma_f32_16x16x32_bf16 v[50:53], v[154:157], v[172:175], v[50:53]
	v_mfma_f32_16x16x32_bf16 v[38:41], v[146:149], v[180:183], v[38:41]
	v_mfma_f32_16x16x32_bf16 v[34:37], v[154:157], v[180:183], v[34:37]
	v_mfma_f32_16x16x32_bf16 v[22:25], v[146:149], v[194:197], v[22:25]
	v_mfma_f32_16x16x32_bf16 v[18:21], v[154:157], v[194:197], v[18:21]
	v_mfma_f32_16x16x32_bf16 v[6:9], v[146:149], v[216:219], v[6:9]
	v_mfma_f32_16x16x32_bf16 v[2:5], v[154:157], v[216:219], v[2:5]
	v_mfma_f32_16x16x32_bf16 v[54:57], v[150:153], v[176:179], v[54:57]
	v_mfma_f32_16x16x32_bf16 v[50:53], v[158:161], v[176:179], v[50:53]
	v_mfma_f32_16x16x32_bf16 v[38:41], v[150:153], v[190:193], v[38:41]
	v_mfma_f32_16x16x32_bf16 v[34:37], v[158:161], v[190:193], v[34:37]
	v_mfma_f32_16x16x32_bf16 v[22:25], v[150:153], v[212:215], v[22:25]
	v_mfma_f32_16x16x32_bf16 v[18:21], v[158:161], v[212:215], v[18:21]
	v_mfma_f32_16x16x32_bf16 v[6:9], v[150:153], v[220:223], v[6:9]
	v_mfma_f32_16x16x32_bf16 v[2:5], v[158:161], v[220:223], v[2:5]
	s_setprio 0
	s_barrier
	v_add_u32_e32 v142, s56, v187
	v_add_u32_e32 v158, s62, v187
	ds_read_b128 v[130:133], v142
	ds_read_b128 v[134:137], v142 offset:1024
	ds_read_b128 v[138:141], v142 offset:2048
	ds_read_b128 v[142:145], v142 offset:3072
	ds_read_b128 v[146:149], v158
	ds_read_b128 v[150:153], v158 offset:1024
	ds_read_b128 v[154:157], v158 offset:2048
	ds_read_b128 v[158:161], v158 offset:3072
	s_add_u32 s34, s34, s41
	s_addc_u32 s35, s35, 0
	s_mov_b32 m0, s50
	ds_read_b128 v[172:175], v189 offset:32768
	ds_read_b128 v[176:179], v189 offset:33792
	ds_read_b128 v[180:183], v189 offset:34816
	ds_read_b128 v[190:193], v189 offset:35840
	ds_read_b128 v[194:197], v189 offset:36864
	ds_read_b128 v[212:215], v189 offset:37888
	ds_read_b128 v[216:219], v189 offset:38912
	ds_read_b128 v[220:223], v189 offset:39936
	global_load_lds_dwordx4 v0, s[34:35]
	s_mov_b32 m0, s51
	s_nop 0
	global_load_lds_dwordx4 v162, s[34:35]
	s_waitcnt vmcnt(8)
	s_waitcnt lgkmcnt(0)
	s_barrier
	s_setprio 1
	s_waitcnt lgkmcnt(0)
	v_mfma_f32_16x16x32_bf16 v[126:129], v[130:133], v[172:175], v[126:129]
	v_mfma_f32_16x16x32_bf16 v[122:125], v[138:141], v[172:175], v[122:125]
	v_mfma_f32_16x16x32_bf16 v[110:113], v[130:133], v[180:183], v[110:113]
	v_mfma_f32_16x16x32_bf16 v[106:109], v[138:141], v[180:183], v[106:109]
	v_mfma_f32_16x16x32_bf16 v[94:97], v[130:133], v[194:197], v[94:97]
	v_mfma_f32_16x16x32_bf16 v[90:93], v[138:141], v[194:197], v[90:93]
	v_mfma_f32_16x16x32_bf16 v[78:81], v[130:133], v[216:219], v[78:81]
	v_mfma_f32_16x16x32_bf16 v[74:77], v[138:141], v[216:219], v[74:77]
	v_mfma_f32_16x16x32_bf16 v[126:129], v[134:137], v[176:179], v[126:129]
	v_mfma_f32_16x16x32_bf16 v[122:125], v[142:145], v[176:179], v[122:125]
	v_mfma_f32_16x16x32_bf16 v[110:113], v[134:137], v[190:193], v[110:113]
	v_mfma_f32_16x16x32_bf16 v[106:109], v[142:145], v[190:193], v[106:109]
	v_mfma_f32_16x16x32_bf16 v[94:97], v[134:137], v[212:215], v[94:97]
	v_mfma_f32_16x16x32_bf16 v[90:93], v[142:145], v[212:215], v[90:93]
	v_mfma_f32_16x16x32_bf16 v[78:81], v[134:137], v[220:223], v[78:81]
	v_mfma_f32_16x16x32_bf16 v[74:77], v[142:145], v[220:223], v[74:77]
	s_setprio 0
	s_setprio 1
	v_mfma_f32_16x16x32_bf16 v[118:121], v[146:149], v[172:175], v[118:121]
	v_mfma_f32_16x16x32_bf16 v[114:117], v[154:157], v[172:175], v[114:117]
	v_mfma_f32_16x16x32_bf16 v[102:105], v[146:149], v[180:183], v[102:105]
	v_mfma_f32_16x16x32_bf16 v[98:101], v[154:157], v[180:183], v[98:101]
	v_mfma_f32_16x16x32_bf16 v[86:89], v[146:149], v[194:197], v[86:89]
	v_mfma_f32_16x16x32_bf16 v[82:85], v[154:157], v[194:197], v[82:85]
	v_mfma_f32_16x16x32_bf16 v[70:73], v[146:149], v[216:219], v[70:73]
	v_mfma_f32_16x16x32_bf16 v[66:69], v[154:157], v[216:219], v[66:69]
	v_mfma_f32_16x16x32_bf16 v[118:121], v[150:153], v[176:179], v[118:121]
	v_mfma_f32_16x16x32_bf16 v[114:117], v[158:161], v[176:179], v[114:117]
	v_mfma_f32_16x16x32_bf16 v[102:105], v[150:153], v[190:193], v[102:105]
	v_mfma_f32_16x16x32_bf16 v[98:101], v[158:161], v[190:193], v[98:101]
	v_mfma_f32_16x16x32_bf16 v[86:89], v[150:153], v[212:215], v[86:89]
	v_mfma_f32_16x16x32_bf16 v[82:85], v[158:161], v[212:215], v[82:85]
	v_mfma_f32_16x16x32_bf16 v[70:73], v[150:153], v[220:223], v[70:73]
	v_mfma_f32_16x16x32_bf16 v[66:69], v[158:161], v[220:223], v[66:69]
	s_setprio 0
	s_barrier
	s_add_u32 s30, s30, s54
	s_addc_u32 s31, s31, 0
	s_mov_b32 m0, s57
	ds_read_b128 v[172:175], v189 offset:49152
	ds_read_b128 v[176:179], v189 offset:50176
	ds_read_b128 v[180:183], v189 offset:51200
	ds_read_b128 v[190:193], v189 offset:52224
	ds_read_b128 v[194:197], v189 offset:53248
	ds_read_b128 v[212:215], v189 offset:54272
	ds_read_b128 v[216:219], v189 offset:55296
	ds_read_b128 v[220:223], v189 offset:56320
	global_load_lds_dwordx4 v0, s[30:31]
	v_lshl_add_u64 v[168:169], s[30:31], 0, v[162:163]
	s_add_u32 s30, s30, s41
	s_mov_b32 m0, s58
	s_addc_u32 s31, s31, 0
	global_load_lds_dwordx4 v[168:169], off
	s_mov_b32 m0, s63
	s_nop 0
	global_load_lds_dwordx4 v0, s[30:31]
	s_mov_b32 m0, s64
	s_nop 0
	global_load_lds_dwordx4 v162, s[30:31]
	s_mov_b32 m0, s59
	s_nop 0
	global_load_lds_dwordx4 v0, s[28:29]
	s_mov_b32 m0, s60
	s_nop 0
	global_load_lds_dwordx4 v162, s[28:29]
	s_waitcnt vmcnt(8)
	s_waitcnt lgkmcnt(0)
	s_barrier
	s_setprio 1
	s_waitcnt lgkmcnt(0)
	v_mfma_f32_16x16x32_bf16 v[62:65], v[130:133], v[172:175], v[62:65]
	v_mfma_f32_16x16x32_bf16 v[58:61], v[138:141], v[172:175], v[58:61]
	v_mfma_f32_16x16x32_bf16 v[46:49], v[130:133], v[180:183], v[46:49]
	v_mfma_f32_16x16x32_bf16 v[42:45], v[138:141], v[180:183], v[42:45]
	v_mfma_f32_16x16x32_bf16 v[30:33], v[130:133], v[194:197], v[30:33]
	v_mfma_f32_16x16x32_bf16 v[26:29], v[138:141], v[194:197], v[26:29]
	v_mfma_f32_16x16x32_bf16 v[14:17], v[130:133], v[216:219], v[14:17]
	v_mfma_f32_16x16x32_bf16 v[10:13], v[138:141], v[216:219], v[10:13]
	v_mfma_f32_16x16x32_bf16 v[62:65], v[134:137], v[176:179], v[62:65]
	v_mfma_f32_16x16x32_bf16 v[58:61], v[142:145], v[176:179], v[58:61]
	v_mfma_f32_16x16x32_bf16 v[46:49], v[134:137], v[190:193], v[46:49]
	v_mfma_f32_16x16x32_bf16 v[42:45], v[142:145], v[190:193], v[42:45]
	v_mfma_f32_16x16x32_bf16 v[30:33], v[134:137], v[212:215], v[30:33]
	v_mfma_f32_16x16x32_bf16 v[26:29], v[142:145], v[212:215], v[26:29]
	v_mfma_f32_16x16x32_bf16 v[14:17], v[134:137], v[220:223], v[14:17]
	v_mfma_f32_16x16x32_bf16 v[10:13], v[142:145], v[220:223], v[10:13]
	s_setprio 0
	s_setprio 1
	v_mfma_f32_16x16x32_bf16 v[54:57], v[146:149], v[172:175], v[54:57]
	v_mfma_f32_16x16x32_bf16 v[50:53], v[154:157], v[172:175], v[50:53]
	v_mfma_f32_16x16x32_bf16 v[38:41], v[146:149], v[180:183], v[38:41]
	v_mfma_f32_16x16x32_bf16 v[34:37], v[154:157], v[180:183], v[34:37]
	v_mfma_f32_16x16x32_bf16 v[22:25], v[146:149], v[194:197], v[22:25]
	v_mfma_f32_16x16x32_bf16 v[18:21], v[154:157], v[194:197], v[18:21]
	v_mfma_f32_16x16x32_bf16 v[6:9], v[146:149], v[216:219], v[6:9]
	v_mfma_f32_16x16x32_bf16 v[2:5], v[154:157], v[216:219], v[2:5]
	v_mfma_f32_16x16x32_bf16 v[54:57], v[150:153], v[176:179], v[54:57]
	v_mfma_f32_16x16x32_bf16 v[50:53], v[158:161], v[176:179], v[50:53]
	v_mfma_f32_16x16x32_bf16 v[38:41], v[150:153], v[190:193], v[38:41]
	v_mfma_f32_16x16x32_bf16 v[34:37], v[158:161], v[190:193], v[34:37]
	v_mfma_f32_16x16x32_bf16 v[22:25], v[150:153], v[212:215], v[22:25]
	v_mfma_f32_16x16x32_bf16 v[18:21], v[158:161], v[212:215], v[18:21]
	v_mfma_f32_16x16x32_bf16 v[6:9], v[150:153], v[220:223], v[6:9]
	v_mfma_f32_16x16x32_bf16 v[2:5], v[158:161], v[220:223], v[2:5]
	s_setprio 0
	s_barrier
	s_add_i32 s78, s78, 2
	s_cmp_ge_i32 s78, s52
	s_cbranch_scc0 .LBB0_1464

.LBB0_1966:
	v_readlane_b32 s7, v252, 18
	s_or_b32 s8, s34, s7
	s_mul_i32 s60, s8, 0x8800
	s_lshl_b64 s[8:9], s[60:61], 2
	v_readlane_b32 s7, v252, 28
	s_add_u32 s28, s7, s8
	v_readlane_b32 s7, v252, 30
	s_addc_u32 s29, s7, s9
	s_add_i32 s10, s3, s11
	s_mul_hi_i32 s3, s10, 0x92492493
	s_add_i32 s3, s3, s10
	s_lshr_b32 s11, s3, 31
	s_ashr_i32 s3, s3, 6
	s_add_i32 s11, s3, s11
	s_lshl_b32 s13, s11, 2
	s_sub_i32 s3, s58, s13
	s_min_i32 s30, s3, 4
	s_abs_i32 s31, s30
	v_cvt_f32_u32_e32 v0, s31
	s_sub_i32 s36, 0, s31
	s_mulk_i32 s11, 0x70
	s_sub_i32 s10, s10, s11
	v_rcp_iflag_f32_e32 v0, v0
	s_abs_i32 s35, s10
	s_ashr_i32 s48, s2, 6
	s_xor_b32 s11, s10, s30
	v_mul_f32_e32 v0, 0x4f7ffffe, v0
	v_cvt_u32_f32_e32 v0, v0
	s_ashr_i32 s49, s2, 8
	s_lshl_b32 s3, s48, 10
	s_ashr_i32 s11, s11, 31
	v_readfirstlane_b32 s37, v0
	s_mul_i32 s36, s36, s37
	s_mul_hi_u32 s36, s37, s36
	s_add_i32 s37, s37, s36
	s_mul_hi_u32 s36, s35, s37
	s_mul_i32 s37, s36, s31
	s_sub_i32 s35, s35, s37
	s_add_i32 s37, s36, 1
	s_sub_i32 s40, s35, s31
	s_cmp_ge_u32 s35, s31
	s_cselect_b32 s36, s37, s36
	s_cselect_b32 s35, s40, s35
	s_add_i32 s37, s36, 1
	s_cmp_ge_u32 s35, s31
	s_cselect_b32 s31, s37, s36
	s_xor_b32 s31, s31, s11
	s_sub_i32 s11, s31, s11
	s_mul_i32 s30, s11, s30
	s_sub_i32 s10, s10, s30
	s_add_i32 s85, s13, s10
	v_lshl_add_u32 v2, s85, 8, v159
	v_ashrrev_i32_e32 v3, 31, v2
	v_lshl_add_u64 v[2:3], v[2:3], 2, s[28:29]
	global_load_dword v0, v[2:3], off
	global_load_dword v6, v[2:3], off offset:256
	global_load_dword v7, v[2:3], off offset:512
	global_load_dword v8, v[2:3], off offset:768
	s_lshl_b32 s10, s85, 2
	s_add_i32 s10, s46, s10
	v_mov_b32_e32 v2, s10
	ds_read_b32 v2, v2
	s_waitcnt lgkmcnt(0)
	v_readfirstlane_b32 s10, v2
	s_mul_i32 s10, s10, 28
	s_add_i32 s86, s10, s11
	s_ashr_i32 s10, s86, 31
	s_mul_hi_u32 s11, s14, s86
	s_mul_i32 s10, s14, s10
	s_mul_i32 s13, s15, s86
	s_add_i32 s10, s11, s10
	s_mul_i32 s30, s14, s86
	s_add_i32 s10, s10, s13
	s_add_u32 s44, s69, s30
	s_addc_u32 s45, s70, s10
	s_add_u32 s42, s44, s16
	s_addc_u32 s43, s45, s17
	s_add_i32 s13, s1, s3
	s_add_i32 s76, s13, 0x2000
	s_mov_b32 m0, s13
	s_add_u32 s10, s42, s74
	global_load_lds_dwordx4 v130, s[42:43]
	s_mov_b32 m0, s76
	s_addc_u32 s11, s43, 0
	s_add_i32 s79, s93, s3
	global_load_lds_dwordx4 v132, s[42:43]
	s_add_i32 s77, s79, 0x2000
	s_mov_b32 m0, s79
	s_add_i32 s78, s39, s3
	global_load_lds_dwordx4 v130, s[10:11]
	s_mov_b32 m0, s77
	s_add_i32 s80, s78, 0x2000
	global_load_lds_dwordx4 v132, s[10:11]
	s_mov_b32 m0, s78
	s_add_i32 s81, s78, 0x4000
	s_add_i32 s82, s78, 0x6000
	s_cmp_eq_u32 s49, 1
	s_cselect_b64 s[30:31], -1, 0
	s_cmp_lg_u32 s49, 1
	s_waitcnt vmcnt(0)
	v_max_i32_e32 v0, 0, v0
	v_max_i32_e32 v2, 0, v6
	v_mul_lo_u32 v0, v0, s12
	v_max_i32_e32 v3, 0, v7
	v_mul_lo_u32 v2, v2, s12
	v_add_lshl_u32 v148, v0, v165, 1
	v_max_i32_e32 v4, 0, v8
	v_mul_lo_u32 v3, v3, s12
	v_add_lshl_u32 v146, v2, v165, 1
	global_load_lds_dwordx4 v148, s[18:19]
	s_mov_b32 m0, s80
	v_mul_lo_u32 v4, v4, s12
	v_add_lshl_u32 v0, v3, v165, 1
	global_load_lds_dwordx4 v146, s[18:19]
	s_mov_b32 m0, s81
	v_add_lshl_u32 v144, v4, v165, 1
	global_load_lds_dwordx4 v0, s[18:19]
	s_mov_b32 m0, s82
	s_nop 0
	global_load_lds_dwordx4 v144, s[18:19]
	s_cbranch_scc1 .LBB0_1968
	s_barrier
.LBB0_1968:
	s_mul_i32 s60, s34, 0x7700000
	s_lshl_b64 s[34:35], s[60:61], 1
	v_readlane_b32 s7, v252, 8
	s_add_u32 s34, s7, s34
	v_readlane_b32 s7, v252, 10
	s_addc_u32 s35, s7, s35
	v_readlane_b32 s7, v252, 12
	s_add_u32 s36, s7, s8
	v_readlane_b32 s7, v252, 20
	s_addc_u32 s37, s7, s9
	v_readlane_b32 s7, v252, 22
	s_add_u32 s40, s7, s8
	v_readlane_b32 s7, v252, 24
	v_lshlrev_b32_e32 v3, 2, v155
	s_addc_u32 s41, s7, s9
	v_lshl_or_b32 v2, v155, 6, v187
	s_lshl_b32 s8, s49, 13
	v_and_b32_e32 v3, 32, v3
	v_bitop3_b32 v4, v2, s8, v3 bitop3:0xde
	s_lshl_b32 s8, s48, 5
	s_and_b32 s48, s8, 0x60
	s_add_u32 s8, s42, s73
	s_addc_u32 s9, s43, 0
	s_add_i32 s60, s94, s3
	s_mov_b32 m0, s60
	s_waitcnt vmcnt(2)
	s_barrier
	global_load_lds_dwordx4 v130, s[8:9]
	v_lshl_add_u64 v[2:3], s[8:9], 0, v[132:133]
	s_add_i32 s83, s60, 0x2000
	v_readlane_b32 s8, v252, 1
	v_mov_b32_e32 v149, v1
	s_mov_b32 m0, s83
	v_readlane_b32 s9, v252, 2
	s_add_i32 s84, s78, 0x8000
	v_mov_b32_e32 v147, v1
	global_load_lds_dwordx4 v[2:3], off
	s_mov_b32 m0, s84
	s_add_i32 s87, s78, 0xa000
	global_load_lds_dwordx4 v148, s[8:9]
	v_lshl_add_u64 v[2:3], s[8:9], 0, v[146:147]
	s_add_u32 s8, s10, s73
	s_mov_b32 m0, s87
	s_addc_u32 s9, s11, 0
	s_add_i32 s88, s95, s3
	global_load_lds_dwordx4 v[2:3], off
	s_mov_b32 m0, s88
	s_add_i32 s89, s88, 0x2000
	global_load_lds_dwordx4 v130, s[8:9]
	s_mov_b32 m0, s89
	s_cmpk_lt_u32 s2, 0x100
	global_load_lds_dwordx4 v132, s[8:9]
	s_waitcnt vmcnt(6)
	v_lshl_or_b32 v189, s49, 6, v155
	v_lshl_or_b32 v190, s48, 7, v188
	s_cselect_b64 s[42:43], -1, 0
	v_or_b32_e32 v191, s48, v186
	s_mov_b32 s90, 0
	v_add_u32_e32 v192, s39, v4
	s_barrier
	s_branch .LBB0_1971

.LBB0_1983:
	s_add_i32 s3, s3, 1
	s_cmp_ge_i32 s3, s71
	s_cselect_b32 vcc_lo, s71, 0
	s_sub_i32 vcc_lo, s3, vcc_lo
	s_ashr_i32 vcc_hi, vcc_lo, 31
	v_add_u32_e32 v154, s1, v190
	s_lshl_b64 vcc, vcc, s75
	ds_read_b128 v[160:163], v154
	ds_read_b128 v[172:175], v154 offset:1024
	ds_read_b128 v[176:179], v154 offset:2048
	ds_read_b128 v[180:183], v154 offset:3072
	v_add_u32_e32 v154, s93, v190
	s_add_u32 vcc_lo, s65, vcc_lo
	ds_read_b128 v[196:199], v154
	ds_read_b128 v[212:215], v154 offset:1024
	ds_read_b128 v[216:219], v154 offset:2048
	ds_read_b128 v[220:223], v154 offset:3072
	s_addc_u32 vcc_hi, s66, vcc_hi
	s_and_b64 s[52:53], exec, s[52:53]
	s_cselect_b32 s52, s16, s54
	s_cselect_b32 s3, s17, s55
	s_add_u32 s54, s65, s52
	s_addc_u32 s55, s66, s3
	s_add_u32 s52, s54, s73
	s_addc_u32 s53, s55, 0
	s_add_i32 m0, s78, 0xc000
	ds_read_b128 v[224:227], v192
	ds_read_b128 v[228:231], v192 offset:1024
	ds_read_b128 v[232:235], v192 offset:2048
	ds_read_b128 v[236:239], v192 offset:3072
	ds_read_b128 v[240:243], v192 offset:4096
	ds_read_b128 v[244:247], v192 offset:5120
	ds_read_b128 v[248:251], v192 offset:6144
	ds_read_b128 v[168:171], v192 offset:7168
	global_load_lds_dwordx4 v0, vcc
	s_add_i32 m0, s78, 0xe000
	s_nop 0
	global_load_lds_dwordx4 v144, vcc
	s_waitcnt vmcnt(8)
	s_waitcnt lgkmcnt(0)
	s_barrier
	s_setprio 1
	s_waitcnt lgkmcnt(0)
	v_mfma_f32_16x16x32_bf16 v[122:125], v[160:163], v[224:227], v[122:125]
	v_mfma_f32_16x16x32_bf16 v[114:117], v[176:179], v[224:227], v[114:117]
	v_mfma_f32_16x16x32_bf16 v[106:109], v[160:163], v[232:235], v[106:109]
	v_mfma_f32_16x16x32_bf16 v[98:101], v[176:179], v[232:235], v[98:101]
	v_mfma_f32_16x16x32_bf16 v[90:93], v[160:163], v[240:243], v[90:93]
	v_mfma_f32_16x16x32_bf16 v[82:85], v[176:179], v[240:243], v[82:85]
	v_mfma_f32_16x16x32_bf16 v[74:77], v[160:163], v[248:251], v[74:77]
	v_mfma_f32_16x16x32_bf16 v[66:69], v[176:179], v[248:251], v[66:69]
	v_mfma_f32_16x16x32_bf16 v[122:125], v[172:175], v[228:231], v[122:125]
	v_mfma_f32_16x16x32_bf16 v[114:117], v[180:183], v[228:231], v[114:117]
	v_mfma_f32_16x16x32_bf16 v[106:109], v[172:175], v[236:239], v[106:109]
	v_mfma_f32_16x16x32_bf16 v[98:101], v[180:183], v[236:239], v[98:101]
	v_mfma_f32_16x16x32_bf16 v[90:93], v[172:175], v[244:247], v[90:93]
	v_mfma_f32_16x16x32_bf16 v[82:85], v[180:183], v[244:247], v[82:85]
	v_mfma_f32_16x16x32_bf16 v[74:77], v[172:175], v[168:171], v[74:77]
	v_mfma_f32_16x16x32_bf16 v[66:69], v[180:183], v[168:171], v[66:69]
	s_setprio 0
	s_setprio 1
	v_mfma_f32_16x16x32_bf16 v[126:129], v[196:199], v[224:227], v[126:129]
	v_mfma_f32_16x16x32_bf16 v[118:121], v[216:219], v[224:227], v[118:121]
	v_mfma_f32_16x16x32_bf16 v[110:113], v[196:199], v[232:235], v[110:113]
	v_mfma_f32_16x16x32_bf16 v[102:105], v[216:219], v[232:235], v[102:105]
	v_mfma_f32_16x16x32_bf16 v[94:97], v[196:199], v[240:243], v[94:97]
	v_mfma_f32_16x16x32_bf16 v[86:89], v[216:219], v[240:243], v[86:89]
	v_mfma_f32_16x16x32_bf16 v[78:81], v[196:199], v[248:251], v[78:81]
	v_mfma_f32_16x16x32_bf16 v[70:73], v[216:219], v[248:251], v[70:73]
	v_mfma_f32_16x16x32_bf16 v[126:129], v[212:215], v[228:231], v[126:129]
	v_mfma_f32_16x16x32_bf16 v[118:121], v[220:223], v[228:231], v[118:121]
	v_mfma_f32_16x16x32_bf16 v[110:113], v[212:215], v[236:239], v[110:113]
	v_mfma_f32_16x16x32_bf16 v[102:105], v[220:223], v[236:239], v[102:105]
	v_mfma_f32_16x16x32_bf16 v[94:97], v[212:215], v[244:247], v[94:97]
	v_mfma_f32_16x16x32_bf16 v[86:89], v[220:223], v[244:247], v[86:89]
	v_mfma_f32_16x16x32_bf16 v[78:81], v[212:215], v[168:171], v[78:81]
	v_mfma_f32_16x16x32_bf16 v[70:73], v[220:223], v[168:171], v[70:73]
	s_setprio 0
	s_barrier
	s_mov_b32 m0, s13
	s_add_u32 vcc_lo, s50, s74
	ds_read_b128 v[168:171], v192 offset:16384
	ds_read_b128 v[224:227], v192 offset:17408
	ds_read_b128 v[228:231], v192 offset:18432
	ds_read_b128 v[232:235], v192 offset:19456
	ds_read_b128 v[236:239], v192 offset:20480
	ds_read_b128 v[240:243], v192 offset:21504
	ds_read_b128 v[244:247], v192 offset:22528
	ds_read_b128 v[248:251], v192 offset:23552
	global_load_lds_dwordx4 v130, s[50:51]
	s_mov_b32 m0, s76
	s_addc_u32 vcc_hi, s51, 0
	global_load_lds_dwordx4 v132, s[50:51]
	s_mov_b32 m0, s79
	s_nop 0
	global_load_lds_dwordx4 v130, vcc
	s_mov_b32 m0, s77
	s_nop 0
	global_load_lds_dwordx4 v132, vcc
	s_mov_b32 m0, s78
	s_nop 0
	global_load_lds_dwordx4 v149, s[54:55]
	s_mov_b32 m0, s80
	s_nop 0
	global_load_lds_dwordx4 v147, s[54:55]
	s_waitcnt vmcnt(8)
	s_waitcnt lgkmcnt(0)
	s_barrier
	s_setprio 1
	s_waitcnt lgkmcnt(0)
	v_mfma_f32_16x16x32_bf16 v[58:61], v[160:163], v[168:171], v[58:61]
	v_mfma_f32_16x16x32_bf16 v[50:53], v[176:179], v[168:171], v[50:53]
	v_mfma_f32_16x16x32_bf16 v[42:45], v[160:163], v[228:231], v[42:45]
	v_mfma_f32_16x16x32_bf16 v[38:41], v[176:179], v[228:231], v[38:41]
	v_mfma_f32_16x16x32_bf16 v[26:29], v[160:163], v[236:239], v[26:29]
	v_mfma_f32_16x16x32_bf16 v[18:21], v[176:179], v[236:239], v[18:21]
	v_mfma_f32_16x16x32_bf16 v[10:13], v[160:163], v[244:247], v[10:13]
	v_mfma_f32_16x16x32_bf16 v[6:9], v[176:179], v[244:247], v[6:9]
	v_mfma_f32_16x16x32_bf16 v[58:61], v[172:175], v[224:227], v[58:61]
	v_mfma_f32_16x16x32_bf16 v[50:53], v[180:183], v[224:227], v[50:53]
	v_mfma_f32_16x16x32_bf16 v[42:45], v[172:175], v[232:235], v[42:45]
	v_mfma_f32_16x16x32_bf16 v[38:41], v[180:183], v[232:235], v[38:41]
	v_mfma_f32_16x16x32_bf16 v[26:29], v[172:175], v[240:243], v[26:29]
	v_mfma_f32_16x16x32_bf16 v[18:21], v[180:183], v[240:243], v[18:21]
	v_mfma_f32_16x16x32_bf16 v[10:13], v[172:175], v[248:251], v[10:13]
	v_mfma_f32_16x16x32_bf16 v[6:9], v[180:183], v[248:251], v[6:9]
	s_setprio 0
	s_setprio 1
	v_mfma_f32_16x16x32_bf16 v[62:65], v[196:199], v[168:171], v[62:65]
	v_mfma_f32_16x16x32_bf16 v[54:57], v[216:219], v[168:171], v[54:57]
	v_mfma_f32_16x16x32_bf16 v[46:49], v[196:199], v[228:231], v[46:49]
	v_mfma_f32_16x16x32_bf16 v[34:37], v[216:219], v[228:231], v[34:37]
	v_mfma_f32_16x16x32_bf16 v[30:33], v[196:199], v[236:239], v[30:33]
	v_mfma_f32_16x16x32_bf16 v[22:25], v[216:219], v[236:239], v[22:25]
	v_mfma_f32_16x16x32_bf16 v[14:17], v[196:199], v[244:247], v[14:17]
	v_mfma_f32_16x16x32_bf16 v[2:5], v[216:219], v[244:247], v[2:5]
	v_mfma_f32_16x16x32_bf16 v[62:65], v[212:215], v[224:227], v[62:65]
	v_mfma_f32_16x16x32_bf16 v[54:57], v[220:223], v[224:227], v[54:57]
	v_mfma_f32_16x16x32_bf16 v[46:49], v[212:215], v[232:235], v[46:49]
	v_mfma_f32_16x16x32_bf16 v[34:37], v[220:223], v[232:235], v[34:37]
	v_mfma_f32_16x16x32_bf16 v[30:33], v[212:215], v[240:243], v[30:33]
	v_mfma_f32_16x16x32_bf16 v[22:25], v[220:223], v[240:243], v[22:25]
	v_mfma_f32_16x16x32_bf16 v[14:17], v[212:215], v[248:251], v[14:17]
	v_mfma_f32_16x16x32_bf16 v[2:5], v[220:223], v[248:251], v[2:5]
	s_setprio 0
	s_barrier
	v_add_u32_e32 v154, s94, v190
	ds_read_b128 v[160:163], v154
	ds_read_b128 v[168:171], v154 offset:1024
	ds_read_b128 v[172:175], v154 offset:2048
	ds_read_b128 v[176:179], v154 offset:3072
	v_add_u32_e32 v154, s95, v190
	ds_read_b128 v[180:183], v154
	ds_read_b128 v[196:199], v154 offset:1024
	ds_read_b128 v[212:215], v154 offset:2048
	ds_read_b128 v[216:219], v154 offset:3072
	s_mov_b32 m0, s81
	ds_read_b128 v[220:223], v192 offset:32768
	ds_read_b128 v[224:227], v192 offset:33792
	ds_read_b128 v[228:231], v192 offset:34816
	ds_read_b128 v[232:235], v192 offset:35840
	ds_read_b128 v[236:239], v192 offset:36864
	ds_read_b128 v[240:243], v192 offset:37888
	ds_read_b128 v[244:247], v192 offset:38912
	ds_read_b128 v[248:251], v192 offset:39936
	global_load_lds_dwordx4 v152, s[54:55]
	s_mov_b32 m0, s82
	s_nop 0
	global_load_lds_dwordx4 v150, s[54:55]
	s_waitcnt vmcnt(8)
	s_waitcnt lgkmcnt(0)
	s_barrier
	s_setprio 1
	s_waitcnt lgkmcnt(0)
	v_mfma_f32_16x16x32_bf16 v[122:125], v[160:163], v[220:223], v[122:125]
	v_mfma_f32_16x16x32_bf16 v[114:117], v[172:175], v[220:223], v[114:117]
	v_mfma_f32_16x16x32_bf16 v[106:109], v[160:163], v[228:231], v[106:109]
	v_mfma_f32_16x16x32_bf16 v[98:101], v[172:175], v[228:231], v[98:101]
	v_mfma_f32_16x16x32_bf16 v[90:93], v[160:163], v[236:239], v[90:93]
	v_mfma_f32_16x16x32_bf16 v[82:85], v[172:175], v[236:239], v[82:85]
	v_mfma_f32_16x16x32_bf16 v[74:77], v[160:163], v[244:247], v[74:77]
	v_mfma_f32_16x16x32_bf16 v[66:69], v[172:175], v[244:247], v[66:69]
	v_mfma_f32_16x16x32_bf16 v[122:125], v[168:171], v[224:227], v[122:125]
	v_mfma_f32_16x16x32_bf16 v[114:117], v[176:179], v[224:227], v[114:117]
	v_mfma_f32_16x16x32_bf16 v[106:109], v[168:171], v[232:235], v[106:109]
	v_mfma_f32_16x16x32_bf16 v[98:101], v[176:179], v[232:235], v[98:101]
	v_mfma_f32_16x16x32_bf16 v[90:93], v[168:171], v[240:243], v[90:93]
	v_mfma_f32_16x16x32_bf16 v[82:85], v[176:179], v[240:243], v[82:85]
	v_mfma_f32_16x16x32_bf16 v[74:77], v[168:171], v[248:251], v[74:77]
	v_mfma_f32_16x16x32_bf16 v[66:69], v[176:179], v[248:251], v[66:69]
	s_setprio 0
	s_setprio 1
	v_mfma_f32_16x16x32_bf16 v[126:129], v[180:183], v[220:223], v[126:129]
	v_mfma_f32_16x16x32_bf16 v[118:121], v[212:215], v[220:223], v[118:121]
	v_mfma_f32_16x16x32_bf16 v[110:113], v[180:183], v[228:231], v[110:113]
	v_mfma_f32_16x16x32_bf16 v[102:105], v[212:215], v[228:231], v[102:105]
	v_mfma_f32_16x16x32_bf16 v[94:97], v[180:183], v[236:239], v[94:97]
	v_mfma_f32_16x16x32_bf16 v[86:89], v[212:215], v[236:239], v[86:89]
	v_mfma_f32_16x16x32_bf16 v[78:81], v[180:183], v[244:247], v[78:81]
	v_mfma_f32_16x16x32_bf16 v[70:73], v[212:215], v[244:247], v[70:73]
	v_mfma_f32_16x16x32_bf16 v[126:129], v[196:199], v[224:227], v[126:129]
	v_mfma_f32_16x16x32_bf16 v[118:121], v[216:219], v[224:227], v[118:121]
	v_mfma_f32_16x16x32_bf16 v[110:113], v[196:199], v[232:235], v[110:113]
	v_mfma_f32_16x16x32_bf16 v[102:105], v[216:219], v[232:235], v[102:105]
	v_mfma_f32_16x16x32_bf16 v[94:97], v[196:199], v[240:243], v[94:97]
	v_mfma_f32_16x16x32_bf16 v[86:89], v[216:219], v[240:243], v[86:89]
	v_mfma_f32_16x16x32_bf16 v[78:81], v[196:199], v[248:251], v[78:81]
	v_mfma_f32_16x16x32_bf16 v[70:73], v[216:219], v[248:251], v[70:73]
	s_setprio 0
	s_barrier
	s_add_u32 s50, s50, s73
	s_addc_u32 s51, s51, 0
	s_mov_b32 m0, s60
	ds_read_b128 v[150:153], v192 offset:49152
	ds_read_b128 v[220:223], v192 offset:50176
	ds_read_b128 v[224:227], v192 offset:51200
	ds_read_b128 v[228:231], v192 offset:52224
	ds_read_b128 v[232:235], v192 offset:53248
	ds_read_b128 v[236:239], v192 offset:54272
	ds_read_b128 v[240:243], v192 offset:55296
	ds_read_b128 v[244:247], v192 offset:56320
	global_load_lds_dwordx4 v130, s[50:51]
	v_lshl_add_u64 v[156:157], s[50:51], 0, v[132:133]
	s_add_u32 s50, s50, s74
	s_mov_b32 m0, s83
	s_addc_u32 s51, s51, 0
	global_load_lds_dwordx4 v[156:157], off
	s_mov_b32 m0, s88
	s_nop 0
	global_load_lds_dwordx4 v130, s[50:51]
	s_mov_b32 m0, s89
	s_nop 0
	global_load_lds_dwordx4 v132, s[50:51]
	s_mov_b32 m0, s84
	s_nop 0
	global_load_lds_dwordx4 v149, s[52:53]
	s_mov_b32 m0, s87
	s_nop 0
	global_load_lds_dwordx4 v147, s[52:53]
	s_waitcnt vmcnt(8)
	s_waitcnt lgkmcnt(0)
	s_barrier
	s_setprio 1
	s_waitcnt lgkmcnt(0)
	v_mfma_f32_16x16x32_bf16 v[58:61], v[160:163], v[150:153], v[58:61]
	v_mfma_f32_16x16x32_bf16 v[50:53], v[172:175], v[150:153], v[50:53]
	v_mfma_f32_16x16x32_bf16 v[42:45], v[160:163], v[224:227], v[42:45]
	v_mfma_f32_16x16x32_bf16 v[38:41], v[172:175], v[224:227], v[38:41]
	v_mfma_f32_16x16x32_bf16 v[26:29], v[160:163], v[232:235], v[26:29]
	v_mfma_f32_16x16x32_bf16 v[18:21], v[172:175], v[232:235], v[18:21]
	v_mfma_f32_16x16x32_bf16 v[10:13], v[160:163], v[240:243], v[10:13]
	v_mfma_f32_16x16x32_bf16 v[6:9], v[172:175], v[240:243], v[6:9]
	v_mfma_f32_16x16x32_bf16 v[58:61], v[168:171], v[220:223], v[58:61]
	v_mfma_f32_16x16x32_bf16 v[50:53], v[176:179], v[220:223], v[50:53]
	v_mfma_f32_16x16x32_bf16 v[42:45], v[168:171], v[228:231], v[42:45]
	v_mfma_f32_16x16x32_bf16 v[38:41], v[176:179], v[228:231], v[38:41]
	v_mfma_f32_16x16x32_bf16 v[26:29], v[168:171], v[236:239], v[26:29]
	v_mfma_f32_16x16x32_bf16 v[18:21], v[176:179], v[236:239], v[18:21]
	v_mfma_f32_16x16x32_bf16 v[10:13], v[168:171], v[244:247], v[10:13]
	v_mfma_f32_16x16x32_bf16 v[6:9], v[176:179], v[244:247], v[6:9]
	s_setprio 0
	s_setprio 1
	v_mfma_f32_16x16x32_bf16 v[62:65], v[180:183], v[150:153], v[62:65]
	v_mfma_f32_16x16x32_bf16 v[54:57], v[212:215], v[150:153], v[54:57]
	v_mfma_f32_16x16x32_bf16 v[46:49], v[180:183], v[224:227], v[46:49]
	v_mfma_f32_16x16x32_bf16 v[34:37], v[212:215], v[224:227], v[34:37]
	v_mfma_f32_16x16x32_bf16 v[30:33], v[180:183], v[232:235], v[30:33]
	v_mfma_f32_16x16x32_bf16 v[22:25], v[212:215], v[232:235], v[22:25]
	v_mfma_f32_16x16x32_bf16 v[14:17], v[180:183], v[240:243], v[14:17]
	v_mfma_f32_16x16x32_bf16 v[2:5], v[212:215], v[240:243], v[2:5]
	v_mfma_f32_16x16x32_bf16 v[62:65], v[196:199], v[220:223], v[62:65]
	v_mfma_f32_16x16x32_bf16 v[54:57], v[216:219], v[220:223], v[54:57]
	v_mfma_f32_16x16x32_bf16 v[46:49], v[196:199], v[228:231], v[46:49]
	v_mfma_f32_16x16x32_bf16 v[34:37], v[216:219], v[228:231], v[34:37]
	v_mfma_f32_16x16x32_bf16 v[30:33], v[196:199], v[236:239], v[30:33]
	v_mfma_f32_16x16x32_bf16 v[22:25], v[216:219], v[236:239], v[22:25]
	v_mfma_f32_16x16x32_bf16 v[14:17], v[196:199], v[244:247], v[14:17]
	v_mfma_f32_16x16x32_bf16 v[2:5], v[216:219], v[244:247], v[2:5]
	s_setprio 0
	s_barrier
	s_add_i32 s2, s2, 2
	s_cmp_ge_i32 s2, s71
	s_cbranch_scc1 .LBB0_1986

.LBB0_2131:
	v_readlane_b32 s22, v252, 39
	s_ashr_i32 s21, s22, 31
	s_lshr_b32 s21, s21, 26
	s_add_i32 s21, s22, s21
	s_ashr_i32 s75, s21, 6
	s_lshl_b32 s20, s20, 5
	s_add_i32 s76, s75, -2
	s_lshl_b32 s21, s7, 13
	s_and_b32 s22, s20, 0x60
	s_add_u32 s18, s18, s47
	s_addc_u32 s19, s19, 0
	s_add_i32 s77, s49, 0x18000
	s_add_i32 s78, s77, s9
	v_mov_b32_e32 v135, v1
	s_add_i32 s79, s78, 0x2000
	v_mov_b32_e32 v137, v1
	s_mov_b32 m0, s78
	s_add_u32 s0, s0, s47
	s_waitcnt vmcnt(2)
	s_barrier
	global_load_lds_dwordx4 v134, s[18:19]
	s_mov_b32 m0, s79
	s_addc_u32 s1, s1, 0
	s_add_i32 s80, s71, 0x8000
	global_load_lds_dwordx4 v136, s[18:19]
	s_mov_b32 m0, s80
	s_add_i32 s81, s71, 0xa000
	global_load_lds_dwordx4 v134, s[0:1]
	v_lshl_add_u64 v[2:3], s[0:1], 0, v[136:137]
	s_add_u32 s0, s2, s47
	s_addc_u32 s1, s3, 0
	s_add_i32 s82, s49, 0x1c000
	s_mov_b32 m0, s81
	s_add_i32 s83, s82, s9
	global_load_lds_dwordx4 v[2:3], off
	s_mov_b32 m0, s83
	s_add_i32 s92, s83, 0x2000
	global_load_lds_dwordx4 v134, s[0:1]
	s_mov_b32 m0, s92
	s_cmpk_gt_i32 s52, 0xf23f
	global_load_lds_dwordx4 v136, s[0:1]
	v_lshlrev_b32_e32 v2, 2, v131
	v_lshl_or_b32 v0, v131, 6, v138
	v_and_b32_e32 v2, 32, v2
	s_cselect_b64 s[18:19], -1, 0
	s_cmpk_lt_u32 s8, 0x100
	v_bitop3_b32 v0, v0, s21, v2 bitop3:0xde
	s_cselect_b64 s[20:21], -1, 0
	s_lshr_b32 s0, s95, 31
	s_add_i32 s0, s95, s0
	s_ashr_i32 s90, s0, 1
	v_readlane_b32 s0, v252, 20
	s_mov_b32 s2, s0
	s_ashr_i32 s0, s0, 31
	s_lshr_b32 s0, s0, 29
	s_waitcnt vmcnt(6)
	s_add_i32 s0, s2, s0
	s_and_b32 s0, s0, -8
	v_lshl_or_b32 v139, s7, 6, v131
	v_lshl_or_b32 v180, s22, 7, v179
	s_ashr_i32 s84, s93, 31
	s_ashr_i32 s55, s46, 31
	s_ashr_i32 s7, s6, 31
	s_sub_i32 s68, s2, s0
	s_add_i32 s69, s90, 1
	v_lshl_or_b32 v181, v178, 2, s22
	s_mov_b32 s50, 0
	v_add_u32_e32 v182, s49, v0
	s_barrier
	v_readlane_b32 s1, v252, 21
	s_branch .LBB0_2134

.LBB0_2148:
	s_add_i32 s9, s10, s8
	s_add_i32 s28, s9, 1
	s_cmp_ge_i32 s28, s75
	s_cselect_b32 s29, s75, 0
	s_sub_i32 s28, s28, s29
	s_ashr_i32 s29, s28, 31
	s_lshl_b64 s[40:41], s[28:29], s36
	s_add_i32 s9, s9, 2
	s_cmp_ge_i32 s9, s75
	s_cselect_b32 s28, s75, 0
	s_sub_i32 s28, s9, s28
	s_ashr_i32 s29, s28, 31
	v_add_u32_e32 v0, s11, v180
	s_lshl_b64 s[28:29], s[28:29], s36
	ds_read_b128 v[140:143], v0
	ds_read_b128 v[144:147], v0 offset:1024
	ds_read_b128 v[148:151], v0 offset:2048
	ds_read_b128 v[152:155], v0 offset:3072
	v_add_u32_e32 v0, s66, v180
	s_add_u32 s9, s24, s28
	ds_read_b128 v[156:159], v0
	ds_read_b128 v[160:163], v0 offset:1024
	ds_read_b128 v[168:171], v0 offset:2048
	ds_read_b128 v[172:175], v0 offset:3072
	s_addc_u32 s30, s25, s29
	s_add_u32 s28, s26, s28
	s_addc_u32 s29, s27, s29
	s_cmp_eq_u32 s76, s8
	s_cselect_b32 s34, s91, s9
	s_cselect_b32 s35, s97, s30
	s_cselect_b32 s31, vcc_hi, s29
	s_cselect_b32 s30, vcc_lo, s28
	s_add_u32 s28, s34, s47
	s_addc_u32 s29, s35, 0
	s_add_u32 s40, s85, s40
	s_addc_u32 s41, s86, s41
	s_add_i32 m0, s71, 0xc000
	ds_read_b128 v[184:187], v182
	ds_read_b128 v[188:191], v182 offset:1024
	ds_read_b128 v[192:195], v182 offset:2048
	ds_read_b128 v[196:199], v182 offset:3072
	ds_read_b128 v[212:215], v182 offset:4096
	ds_read_b128 v[216:219], v182 offset:5120
	ds_read_b128 v[220:223], v182 offset:6144
	ds_read_b128 v[224:227], v182 offset:7168
	global_load_lds_dwordx4 v134, s[40:41]
	s_add_i32 m0, s71, 0xe000
	s_nop 0
	global_load_lds_dwordx4 v136, s[40:41]
	s_waitcnt vmcnt(8)
	s_waitcnt lgkmcnt(0)
	s_barrier
	s_setprio 1
	s_waitcnt lgkmcnt(0)
	v_mfma_f32_16x16x32_bf16 v[126:129], v[140:143], v[184:187], v[126:129]
	v_mfma_f32_16x16x32_bf16 v[122:125], v[148:151], v[184:187], v[122:125]
	v_mfma_f32_16x16x32_bf16 v[110:113], v[140:143], v[192:195], v[110:113]
	v_mfma_f32_16x16x32_bf16 v[106:109], v[148:151], v[192:195], v[106:109]
	v_mfma_f32_16x16x32_bf16 v[94:97], v[140:143], v[212:215], v[94:97]
	v_mfma_f32_16x16x32_bf16 v[90:93], v[148:151], v[212:215], v[90:93]
	v_mfma_f32_16x16x32_bf16 v[78:81], v[140:143], v[220:223], v[78:81]
	v_mfma_f32_16x16x32_bf16 v[74:77], v[148:151], v[220:223], v[74:77]
	v_mfma_f32_16x16x32_bf16 v[126:129], v[144:147], v[188:191], v[126:129]
	v_mfma_f32_16x16x32_bf16 v[122:125], v[152:155], v[188:191], v[122:125]
	v_mfma_f32_16x16x32_bf16 v[110:113], v[144:147], v[196:199], v[110:113]
	v_mfma_f32_16x16x32_bf16 v[106:109], v[152:155], v[196:199], v[106:109]
	v_mfma_f32_16x16x32_bf16 v[94:97], v[144:147], v[216:219], v[94:97]
	v_mfma_f32_16x16x32_bf16 v[90:93], v[152:155], v[216:219], v[90:93]
	v_mfma_f32_16x16x32_bf16 v[78:81], v[144:147], v[224:227], v[78:81]
	v_mfma_f32_16x16x32_bf16 v[74:77], v[152:155], v[224:227], v[74:77]
	s_setprio 0
	s_setprio 1
	v_mfma_f32_16x16x32_bf16 v[118:121], v[156:159], v[184:187], v[118:121]
	v_mfma_f32_16x16x32_bf16 v[114:117], v[168:171], v[184:187], v[114:117]
	v_mfma_f32_16x16x32_bf16 v[102:105], v[156:159], v[192:195], v[102:105]
	v_mfma_f32_16x16x32_bf16 v[98:101], v[168:171], v[192:195], v[98:101]
	v_mfma_f32_16x16x32_bf16 v[86:89], v[156:159], v[212:215], v[86:89]
	v_mfma_f32_16x16x32_bf16 v[82:85], v[168:171], v[212:215], v[82:85]
	v_mfma_f32_16x16x32_bf16 v[70:73], v[156:159], v[220:223], v[70:73]
	v_mfma_f32_16x16x32_bf16 v[66:69], v[168:171], v[220:223], v[66:69]
	v_mfma_f32_16x16x32_bf16 v[118:121], v[160:163], v[188:191], v[118:121]
	v_mfma_f32_16x16x32_bf16 v[114:117], v[172:175], v[188:191], v[114:117]
	v_mfma_f32_16x16x32_bf16 v[102:105], v[160:163], v[196:199], v[102:105]
	v_mfma_f32_16x16x32_bf16 v[98:101], v[172:175], v[196:199], v[98:101]
	v_mfma_f32_16x16x32_bf16 v[86:89], v[160:163], v[216:219], v[86:89]
	v_mfma_f32_16x16x32_bf16 v[82:85], v[172:175], v[216:219], v[82:85]
	v_mfma_f32_16x16x32_bf16 v[70:73], v[160:163], v[224:227], v[70:73]
	v_mfma_f32_16x16x32_bf16 v[66:69], v[172:175], v[224:227], v[66:69]
	s_setprio 0
	s_barrier
	s_mov_b32 m0, s37
	s_add_u32 s40, s30, s33
	ds_read_b128 v[184:187], v182 offset:16384
	ds_read_b128 v[188:191], v182 offset:17408
	ds_read_b128 v[192:195], v182 offset:18432
	ds_read_b128 v[196:199], v182 offset:19456
	ds_read_b128 v[212:215], v182 offset:20480
	ds_read_b128 v[216:219], v182 offset:21504
	ds_read_b128 v[220:223], v182 offset:22528
	ds_read_b128 v[224:227], v182 offset:23552
	global_load_lds_dwordx4 v134, s[30:31]
	s_mov_b32 m0, s60
	s_addc_u32 s41, s31, 0
	global_load_lds_dwordx4 v136, s[30:31]
	s_mov_b32 m0, s67
	s_nop 0
	global_load_lds_dwordx4 v134, s[40:41]
	s_mov_b32 m0, s70
	s_nop 0
	global_load_lds_dwordx4 v136, s[40:41]
	s_mov_b32 m0, s71
	s_nop 0
	global_load_lds_dwordx4 v134, s[34:35]
	s_mov_b32 m0, s72
	s_nop 0
	global_load_lds_dwordx4 v136, s[34:35]
	s_waitcnt vmcnt(8)
	s_waitcnt lgkmcnt(0)
	s_barrier
	s_setprio 1
	s_waitcnt lgkmcnt(0)
	v_mfma_f32_16x16x32_bf16 v[62:65], v[140:143], v[184:187], v[62:65]
	v_mfma_f32_16x16x32_bf16 v[58:61], v[148:151], v[184:187], v[58:61]
	v_mfma_f32_16x16x32_bf16 v[46:49], v[140:143], v[192:195], v[46:49]
	v_mfma_f32_16x16x32_bf16 v[42:45], v[148:151], v[192:195], v[42:45]
	v_mfma_f32_16x16x32_bf16 v[30:33], v[140:143], v[212:215], v[30:33]
	v_mfma_f32_16x16x32_bf16 v[26:29], v[148:151], v[212:215], v[26:29]
	v_mfma_f32_16x16x32_bf16 v[14:17], v[140:143], v[220:223], v[14:17]
	v_mfma_f32_16x16x32_bf16 v[10:13], v[148:151], v[220:223], v[10:13]
	v_mfma_f32_16x16x32_bf16 v[62:65], v[144:147], v[188:191], v[62:65]
	v_mfma_f32_16x16x32_bf16 v[58:61], v[152:155], v[188:191], v[58:61]
	v_mfma_f32_16x16x32_bf16 v[46:49], v[144:147], v[196:199], v[46:49]
	v_mfma_f32_16x16x32_bf16 v[42:45], v[152:155], v[196:199], v[42:45]
	v_mfma_f32_16x16x32_bf16 v[30:33], v[144:147], v[216:219], v[30:33]
	v_mfma_f32_16x16x32_bf16 v[26:29], v[152:155], v[216:219], v[26:29]
	v_mfma_f32_16x16x32_bf16 v[14:17], v[144:147], v[224:227], v[14:17]
	v_mfma_f32_16x16x32_bf16 v[10:13], v[152:155], v[224:227], v[10:13]
	s_setprio 0
	s_setprio 1
	v_mfma_f32_16x16x32_bf16 v[54:57], v[156:159], v[184:187], v[54:57]
	v_mfma_f32_16x16x32_bf16 v[50:53], v[168:171], v[184:187], v[50:53]
	v_mfma_f32_16x16x32_bf16 v[38:41], v[156:159], v[192:195], v[38:41]
	v_mfma_f32_16x16x32_bf16 v[34:37], v[168:171], v[192:195], v[34:37]
	v_mfma_f32_16x16x32_bf16 v[22:25], v[156:159], v[212:215], v[22:25]
	v_mfma_f32_16x16x32_bf16 v[18:21], v[168:171], v[212:215], v[18:21]
	v_mfma_f32_16x16x32_bf16 v[6:9], v[156:159], v[220:223], v[6:9]
	v_mfma_f32_16x16x32_bf16 v[2:5], v[168:171], v[220:223], v[2:5]
	v_mfma_f32_16x16x32_bf16 v[54:57], v[160:163], v[188:191], v[54:57]
	v_mfma_f32_16x16x32_bf16 v[50:53], v[172:175], v[188:191], v[50:53]
	v_mfma_f32_16x16x32_bf16 v[38:41], v[160:163], v[196:199], v[38:41]
	v_mfma_f32_16x16x32_bf16 v[34:37], v[172:175], v[196:199], v[34:37]
	v_mfma_f32_16x16x32_bf16 v[22:25], v[160:163], v[216:219], v[22:25]
	v_mfma_f32_16x16x32_bf16 v[18:21], v[172:175], v[216:219], v[18:21]
	v_mfma_f32_16x16x32_bf16 v[6:9], v[160:163], v[224:227], v[6:9]
	v_mfma_f32_16x16x32_bf16 v[2:5], v[172:175], v[224:227], v[2:5]
	s_setprio 0
	s_barrier
	v_add_u32_e32 v0, s77, v180
	ds_read_b128 v[140:143], v0
	ds_read_b128 v[144:147], v0 offset:1024
	ds_read_b128 v[148:151], v0 offset:2048
	ds_read_b128 v[152:155], v0 offset:3072
	v_add_u32_e32 v0, s82, v180
	ds_read_b128 v[156:159], v0
	ds_read_b128 v[160:163], v0 offset:1024
	ds_read_b128 v[168:171], v0 offset:2048
	ds_read_b128 v[172:175], v0 offset:3072
	s_add_u32 s34, s34, s33
	s_addc_u32 s35, s35, 0
	s_mov_b32 m0, s73
	ds_read_b128 v[184:187], v182 offset:32768
	ds_read_b128 v[188:191], v182 offset:33792
	ds_read_b128 v[192:195], v182 offset:34816
	ds_read_b128 v[196:199], v182 offset:35840
	ds_read_b128 v[212:215], v182 offset:36864
	ds_read_b128 v[216:219], v182 offset:37888
	ds_read_b128 v[220:223], v182 offset:38912
	ds_read_b128 v[224:227], v182 offset:39936
	global_load_lds_dwordx4 v134, s[34:35]
	s_mov_b32 m0, s74
	s_nop 0
	global_load_lds_dwordx4 v136, s[34:35]
	s_waitcnt vmcnt(8)
	s_waitcnt lgkmcnt(0)
	s_barrier
	s_setprio 1
	s_waitcnt lgkmcnt(0)
	v_mfma_f32_16x16x32_bf16 v[126:129], v[140:143], v[184:187], v[126:129]
	v_mfma_f32_16x16x32_bf16 v[122:125], v[148:151], v[184:187], v[122:125]
	v_mfma_f32_16x16x32_bf16 v[110:113], v[140:143], v[192:195], v[110:113]
	v_mfma_f32_16x16x32_bf16 v[106:109], v[148:151], v[192:195], v[106:109]
	v_mfma_f32_16x16x32_bf16 v[94:97], v[140:143], v[212:215], v[94:97]
	v_mfma_f32_16x16x32_bf16 v[90:93], v[148:151], v[212:215], v[90:93]
	v_mfma_f32_16x16x32_bf16 v[78:81], v[140:143], v[220:223], v[78:81]
	v_mfma_f32_16x16x32_bf16 v[74:77], v[148:151], v[220:223], v[74:77]
	v_mfma_f32_16x16x32_bf16 v[126:129], v[144:147], v[188:191], v[126:129]
	v_mfma_f32_16x16x32_bf16 v[122:125], v[152:155], v[188:191], v[122:125]
	v_mfma_f32_16x16x32_bf16 v[110:113], v[144:147], v[196:199], v[110:113]
	v_mfma_f32_16x16x32_bf16 v[106:109], v[152:155], v[196:199], v[106:109]
	v_mfma_f32_16x16x32_bf16 v[94:97], v[144:147], v[216:219], v[94:97]
	v_mfma_f32_16x16x32_bf16 v[90:93], v[152:155], v[216:219], v[90:93]
	v_mfma_f32_16x16x32_bf16 v[78:81], v[144:147], v[224:227], v[78:81]
	v_mfma_f32_16x16x32_bf16 v[74:77], v[152:155], v[224:227], v[74:77]
	s_setprio 0
	s_setprio 1
	v_mfma_f32_16x16x32_bf16 v[118:121], v[156:159], v[184:187], v[118:121]
	v_mfma_f32_16x16x32_bf16 v[114:117], v[168:171], v[184:187], v[114:117]
	v_mfma_f32_16x16x32_bf16 v[102:105], v[156:159], v[192:195], v[102:105]
	v_mfma_f32_16x16x32_bf16 v[98:101], v[168:171], v[192:195], v[98:101]
	v_mfma_f32_16x16x32_bf16 v[86:89], v[156:159], v[212:215], v[86:89]
	v_mfma_f32_16x16x32_bf16 v[82:85], v[168:171], v[212:215], v[82:85]
	v_mfma_f32_16x16x32_bf16 v[70:73], v[156:159], v[220:223], v[70:73]
	v_mfma_f32_16x16x32_bf16 v[66:69], v[168:171], v[220:223], v[66:69]
	v_mfma_f32_16x16x32_bf16 v[118:121], v[160:163], v[188:191], v[118:121]
	v_mfma_f32_16x16x32_bf16 v[114:117], v[172:175], v[188:191], v[114:117]
	v_mfma_f32_16x16x32_bf16 v[102:105], v[160:163], v[196:199], v[102:105]
	v_mfma_f32_16x16x32_bf16 v[98:101], v[172:175], v[196:199], v[98:101]
	v_mfma_f32_16x16x32_bf16 v[86:89], v[160:163], v[216:219], v[86:89]
	v_mfma_f32_16x16x32_bf16 v[82:85], v[172:175], v[216:219], v[82:85]
	v_mfma_f32_16x16x32_bf16 v[70:73], v[160:163], v[224:227], v[70:73]
	v_mfma_f32_16x16x32_bf16 v[66:69], v[172:175], v[224:227], v[66:69]
	s_setprio 0
	s_barrier
	s_add_u32 s30, s30, s47
	s_addc_u32 s31, s31, 0
	s_mov_b32 m0, s78
	ds_read_b128 v[184:187], v182 offset:49152
	ds_read_b128 v[188:191], v182 offset:50176
	ds_read_b128 v[192:195], v182 offset:51200
	ds_read_b128 v[196:199], v182 offset:52224
	ds_read_b128 v[212:215], v182 offset:53248
	ds_read_b128 v[216:219], v182 offset:54272
	ds_read_b128 v[220:223], v182 offset:55296
	ds_read_b128 v[224:227], v182 offset:56320
	global_load_lds_dwordx4 v134, s[30:31]
	v_lshl_add_u64 v[228:229], s[30:31], 0, v[136:137]
	s_add_u32 s30, s30, s33
	s_mov_b32 m0, s79
	s_addc_u32 s31, s31, 0
	global_load_lds_dwordx4 v[228:229], off
	s_mov_b32 m0, s83
	s_nop 0
	global_load_lds_dwordx4 v134, s[30:31]
	s_mov_b32 m0, s92
	s_nop 0
	global_load_lds_dwordx4 v136, s[30:31]
	s_mov_b32 m0, s80
	s_nop 0
	global_load_lds_dwordx4 v134, s[28:29]
	s_mov_b32 m0, s81
	s_nop 0
	global_load_lds_dwordx4 v136, s[28:29]
	s_waitcnt vmcnt(8)
	s_waitcnt lgkmcnt(0)
	s_barrier
	s_setprio 1
	s_waitcnt lgkmcnt(0)
	v_mfma_f32_16x16x32_bf16 v[62:65], v[140:143], v[184:187], v[62:65]
	v_mfma_f32_16x16x32_bf16 v[58:61], v[148:151], v[184:187], v[58:61]
	v_mfma_f32_16x16x32_bf16 v[46:49], v[140:143], v[192:195], v[46:49]
	v_mfma_f32_16x16x32_bf16 v[42:45], v[148:151], v[192:195], v[42:45]
	v_mfma_f32_16x16x32_bf16 v[30:33], v[140:143], v[212:215], v[30:33]
	v_mfma_f32_16x16x32_bf16 v[26:29], v[148:151], v[212:215], v[26:29]
	v_mfma_f32_16x16x32_bf16 v[14:17], v[140:143], v[220:223], v[14:17]
	v_mfma_f32_16x16x32_bf16 v[10:13], v[148:151], v[220:223], v[10:13]
	v_mfma_f32_16x16x32_bf16 v[62:65], v[144:147], v[188:191], v[62:65]
	v_mfma_f32_16x16x32_bf16 v[58:61], v[152:155], v[188:191], v[58:61]
	v_mfma_f32_16x16x32_bf16 v[46:49], v[144:147], v[196:199], v[46:49]
	v_mfma_f32_16x16x32_bf16 v[42:45], v[152:155], v[196:199], v[42:45]
	v_mfma_f32_16x16x32_bf16 v[30:33], v[144:147], v[216:219], v[30:33]
	v_mfma_f32_16x16x32_bf16 v[26:29], v[152:155], v[216:219], v[26:29]
	v_mfma_f32_16x16x32_bf16 v[14:17], v[144:147], v[224:227], v[14:17]
	v_mfma_f32_16x16x32_bf16 v[10:13], v[152:155], v[224:227], v[10:13]
	s_setprio 0
	s_setprio 1
	v_mfma_f32_16x16x32_bf16 v[54:57], v[156:159], v[184:187], v[54:57]
	v_mfma_f32_16x16x32_bf16 v[50:53], v[168:171], v[184:187], v[50:53]
	v_mfma_f32_16x16x32_bf16 v[38:41], v[156:159], v[192:195], v[38:41]
	v_mfma_f32_16x16x32_bf16 v[34:37], v[168:171], v[192:195], v[34:37]
	v_mfma_f32_16x16x32_bf16 v[22:25], v[156:159], v[212:215], v[22:25]
	v_mfma_f32_16x16x32_bf16 v[18:21], v[168:171], v[212:215], v[18:21]
	v_mfma_f32_16x16x32_bf16 v[6:9], v[156:159], v[220:223], v[6:9]
	v_mfma_f32_16x16x32_bf16 v[2:5], v[168:171], v[220:223], v[2:5]
	v_mfma_f32_16x16x32_bf16 v[54:57], v[160:163], v[188:191], v[54:57]
	v_mfma_f32_16x16x32_bf16 v[50:53], v[172:175], v[188:191], v[50:53]
	v_mfma_f32_16x16x32_bf16 v[38:41], v[160:163], v[196:199], v[38:41]
	v_mfma_f32_16x16x32_bf16 v[34:37], v[172:175], v[196:199], v[34:37]
	v_mfma_f32_16x16x32_bf16 v[22:25], v[160:163], v[216:219], v[22:25]
	v_mfma_f32_16x16x32_bf16 v[18:21], v[172:175], v[216:219], v[18:21]
	v_mfma_f32_16x16x32_bf16 v[6:9], v[160:163], v[224:227], v[6:9]
	v_mfma_f32_16x16x32_bf16 v[2:5], v[172:175], v[224:227], v[2:5]
	s_setprio 0
	s_barrier
	s_add_i32 s8, s8, 2
	s_cmp_ge_i32 s8, s75
	s_cbranch_scc0 .LBB0_2148

.LBB0_2379:
	s_lshl_b32 s10, s10, 5
	s_and_b32 s16, s10, 0x60
	s_add_u32 s40, s4, s47
	s_addc_u32 s41, s5, 0
	s_add_i32 s35, s49, 0x18000
	v_mov_b32_e32 v135, v1
	s_add_i32 s36, s35, s11
	v_mov_b32_e32 v137, v1
	s_mov_b32 m0, s36
	s_add_i32 s37, s36, 0x2000
	s_waitcnt vmcnt(2)
	s_barrier
	global_load_lds_dwordx4 v134, s[40:41]
	v_lshl_add_u64 v[2:3], s[40:41], 0, v[136:137]
	s_add_u32 s40, s2, s47
	s_addc_u32 s41, s3, 0
	s_add_i32 s48, s30, 0x8000
	s_add_i32 s50, s30, 0xa000
	s_mov_b32 m0, s37
	s_add_u32 s6, s6, s47
	global_load_lds_dwordx4 v[2:3], off
	s_mov_b32 m0, s48
	s_addc_u32 s7, s7, 0
	s_add_i32 s51, s49, 0x1c000
	global_load_lds_dwordx4 v134, s[40:41]
	s_mov_b32 m0, s50
	s_add_i32 s55, s51, s11
	global_load_lds_dwordx4 v136, s[40:41]
	s_mov_b32 m0, s55
	s_add_i32 s60, s55, 0x2000
	global_load_lds_dwordx4 v134, s[6:7]
	s_mov_b32 m0, s60
	v_mov_b32_e32 v5, 0
	global_load_lds_dwordx4 v136, s[6:7]
	s_waitcnt vmcnt(6)
	v_lshl_or_b32 v140, s9, 6, v131
	s_cmp_lt_i32 s8, 64
	v_mov_b32_e32 v4, v5
	v_mov_b32_e32 v3, v5
	v_mov_b32_e32 v2, v5
	v_mov_b32_e32 v9, v5
	v_mov_b32_e32 v8, v5
	v_mov_b32_e32 v7, v5
	v_mov_b32_e32 v6, v5
	v_mov_b32_e32 v21, v5
	v_mov_b32_e32 v20, v5
	v_mov_b32_e32 v19, v5
	v_mov_b32_e32 v18, v5
	v_mov_b32_e32 v25, v5
	v_mov_b32_e32 v24, v5
	v_mov_b32_e32 v23, v5
	v_mov_b32_e32 v22, v5
	v_mov_b32_e32 v129, v5
	v_mov_b32_e32 v128, v5
	v_mov_b32_e32 v127, v5
	v_mov_b32_e32 v126, v5
	v_mov_b32_e32 v125, v5
	v_mov_b32_e32 v124, v5
	v_mov_b32_e32 v123, v5
	v_mov_b32_e32 v122, v5
	v_mov_b32_e32 v113, v5
	v_mov_b32_e32 v112, v5
	v_mov_b32_e32 v111, v5
	v_mov_b32_e32 v110, v5
	v_mov_b32_e32 v109, v5
	v_mov_b32_e32 v108, v5
	v_mov_b32_e32 v107, v5
	v_mov_b32_e32 v106, v5
	v_mov_b32_e32 v97, v5
	v_mov_b32_e32 v96, v5
	v_mov_b32_e32 v95, v5
	v_mov_b32_e32 v94, v5
	v_mov_b32_e32 v93, v5
	v_mov_b32_e32 v92, v5
	v_mov_b32_e32 v91, v5
	v_mov_b32_e32 v90, v5
	v_mov_b32_e32 v81, v5
	v_mov_b32_e32 v80, v5
	v_mov_b32_e32 v79, v5
	v_mov_b32_e32 v78, v5
	v_mov_b32_e32 v77, v5
	v_mov_b32_e32 v76, v5
	v_mov_b32_e32 v75, v5
	v_mov_b32_e32 v74, v5
	v_mov_b32_e32 v121, v5
	v_mov_b32_e32 v120, v5
	v_mov_b32_e32 v119, v5
	v_mov_b32_e32 v118, v5
	v_mov_b32_e32 v117, v5
	v_mov_b32_e32 v116, v5
	v_mov_b32_e32 v115, v5
	v_mov_b32_e32 v114, v5
	s_waitcnt vmcnt(0)
	v_mov_b32_e32 v105, v5
	v_mov_b32_e32 v104, v5
	v_mov_b32_e32 v103, v5
	v_mov_b32_e32 v102, v5
	v_mov_b32_e32 v101, v5
	v_mov_b32_e32 v100, v5
	v_mov_b32_e32 v99, v5
	v_mov_b32_e32 v98, v5
	v_mov_b32_e32 v89, v5
	v_mov_b32_e32 v88, v5
	v_mov_b32_e32 v87, v5
	v_mov_b32_e32 v86, v5
	v_mov_b32_e32 v85, v5
	v_mov_b32_e32 v84, v5
	v_mov_b32_e32 v83, v5
	v_mov_b32_e32 v82, v5
	v_mov_b32_e32 v73, v5
	v_mov_b32_e32 v72, v5
	v_mov_b32_e32 v71, v5
	v_mov_b32_e32 v70, v5
	v_mov_b32_e32 v69, v5
	v_mov_b32_e32 v68, v5
	v_mov_b32_e32 v67, v5
	v_mov_b32_e32 v66, v5
	v_mov_b32_e32 v65, v5
	v_mov_b32_e32 v64, v5
	v_mov_b32_e32 v63, v5
	v_mov_b32_e32 v62, v5
	v_mov_b32_e32 v61, v5
	v_mov_b32_e32 v60, v5
	v_mov_b32_e32 v59, v5
	v_mov_b32_e32 v58, v5
	v_mov_b32_e32 v49, v5
	v_mov_b32_e32 v48, v5
	v_mov_b32_e32 v47, v5
	v_mov_b32_e32 v46, v5
	v_mov_b32_e32 v45, v5
	v_mov_b32_e32 v44, v5
	v_mov_b32_e32 v43, v5
	v_mov_b32_e32 v42, v5
	v_mov_b32_e32 v33, v5
	v_mov_b32_e32 v32, v5
	v_mov_b32_e32 v31, v5
	v_mov_b32_e32 v30, v5
	v_mov_b32_e32 v29, v5
	v_mov_b32_e32 v28, v5
	v_mov_b32_e32 v27, v5
	v_mov_b32_e32 v26, v5
	v_mov_b32_e32 v17, v5
	v_mov_b32_e32 v16, v5
	v_mov_b32_e32 v15, v5
	v_mov_b32_e32 v14, v5
	v_mov_b32_e32 v13, v5
	v_mov_b32_e32 v12, v5
	v_mov_b32_e32 v11, v5
	v_mov_b32_e32 v10, v5
	v_mov_b32_e32 v57, v5
	v_mov_b32_e32 v56, v5
	v_mov_b32_e32 v55, v5
	v_mov_b32_e32 v54, v5
	v_mov_b32_e32 v53, v5
	v_mov_b32_e32 v52, v5
	v_mov_b32_e32 v51, v5
	v_mov_b32_e32 v50, v5
	v_mov_b32_e32 v41, v5
	v_mov_b32_e32 v40, v5
	v_mov_b32_e32 v39, v5
	v_mov_b32_e32 v38, v5
	v_mov_b32_e32 v37, v5
	v_mov_b32_e32 v36, v5
	v_mov_b32_e32 v35, v5
	v_mov_b32_e32 v34, v5
	s_barrier
	s_cbranch_scc1 .LBB0_2382
	s_add_u32 s64, s19, s18
	v_lshlrev_b32_e32 v0, 6, v140
	s_movk_i32 s6, 0x3c0
	s_addc_u32 s65, s20, s17
	v_and_or_b32 v0, v0, s6, v138
	s_ashr_i32 s6, s8, 31
	v_lshlrev_b32_e32 v2, 2, v140
	s_lshr_b32 s6, s6, 26
	v_and_b32_e32 v2, 32, v2
	s_add_i32 s8, s8, s6
	s_lshl_b32 s6, s9, 13
	v_bitop3_b32 v2, v0, s6, v2 bitop3:0xde
	v_mov_b32_e32 v34, 0
	s_mov_b32 s66, 2
	s_ashr_i32 s67, s8, 6
	v_lshl_or_b32 v0, s16, 7, v179
	v_add_u32_e32 v139, s49, v2
	v_mov_b32_e32 v35, v34
	v_mov_b32_e32 v36, v34
	v_mov_b32_e32 v37, v34
	v_mov_b32_e32 v38, v34
	v_mov_b32_e32 v39, v34
	v_mov_b32_e32 v40, v34
	v_mov_b32_e32 v41, v34
	v_mov_b32_e32 v50, v34
	v_mov_b32_e32 v51, v34
	v_mov_b32_e32 v52, v34
	v_mov_b32_e32 v53, v34
	v_mov_b32_e32 v54, v34
	v_mov_b32_e32 v55, v34
	v_mov_b32_e32 v56, v34
	v_mov_b32_e32 v57, v34
	v_mov_b32_e32 v10, v34
	v_mov_b32_e32 v11, v34
	v_mov_b32_e32 v12, v34
	v_mov_b32_e32 v13, v34
	v_mov_b32_e32 v14, v34
	v_mov_b32_e32 v15, v34
	v_mov_b32_e32 v16, v34
	v_mov_b32_e32 v17, v34
	v_mov_b32_e32 v26, v34
	v_mov_b32_e32 v27, v34
	v_mov_b32_e32 v28, v34
	v_mov_b32_e32 v29, v34
	v_mov_b32_e32 v30, v34
	v_mov_b32_e32 v31, v34
	v_mov_b32_e32 v32, v34
	v_mov_b32_e32 v33, v34
	v_mov_b32_e32 v42, v34
	v_mov_b32_e32 v43, v34
	v_mov_b32_e32 v44, v34
	v_mov_b32_e32 v45, v34
	v_mov_b32_e32 v46, v34
	v_mov_b32_e32 v47, v34
	v_mov_b32_e32 v48, v34
	v_mov_b32_e32 v49, v34
	v_mov_b32_e32 v58, v34
	v_mov_b32_e32 v59, v34
	v_mov_b32_e32 v60, v34
	v_mov_b32_e32 v61, v34
	v_mov_b32_e32 v62, v34
	v_mov_b32_e32 v63, v34
	v_mov_b32_e32 v64, v34
	v_mov_b32_e32 v65, v34
	v_mov_b32_e32 v66, v34
	v_mov_b32_e32 v67, v34
	v_mov_b32_e32 v68, v34
	v_mov_b32_e32 v69, v34
	v_mov_b32_e32 v70, v34
	v_mov_b32_e32 v71, v34
	v_mov_b32_e32 v72, v34
	v_mov_b32_e32 v73, v34
	v_mov_b32_e32 v82, v34
	v_mov_b32_e32 v83, v34
	v_mov_b32_e32 v84, v34
	v_mov_b32_e32 v85, v34
	v_mov_b32_e32 v86, v34
	v_mov_b32_e32 v87, v34
	v_mov_b32_e32 v88, v34
	v_mov_b32_e32 v89, v34
	v_mov_b32_e32 v98, v34
	v_mov_b32_e32 v99, v34
	v_mov_b32_e32 v100, v34
	v_mov_b32_e32 v101, v34
	v_mov_b32_e32 v102, v34
	v_mov_b32_e32 v103, v34
	v_mov_b32_e32 v104, v34
	v_mov_b32_e32 v105, v34
	v_mov_b32_e32 v114, v34
	v_mov_b32_e32 v115, v34
	v_mov_b32_e32 v116, v34
	v_mov_b32_e32 v117, v34
	v_mov_b32_e32 v118, v34
	v_mov_b32_e32 v119, v34
	v_mov_b32_e32 v120, v34
	v_mov_b32_e32 v121, v34
	v_mov_b32_e32 v74, v34
	v_mov_b32_e32 v75, v34
	v_mov_b32_e32 v76, v34
	v_mov_b32_e32 v77, v34
	v_mov_b32_e32 v78, v34
	v_mov_b32_e32 v79, v34
	v_mov_b32_e32 v80, v34
	v_mov_b32_e32 v81, v34
	v_mov_b32_e32 v90, v34
	v_mov_b32_e32 v91, v34
	v_mov_b32_e32 v92, v34
	v_mov_b32_e32 v93, v34
	v_mov_b32_e32 v94, v34
	v_mov_b32_e32 v95, v34
	v_mov_b32_e32 v96, v34
	v_mov_b32_e32 v97, v34
	v_mov_b32_e32 v106, v34
	v_mov_b32_e32 v107, v34
	v_mov_b32_e32 v108, v34
	v_mov_b32_e32 v109, v34
	v_mov_b32_e32 v110, v34
	v_mov_b32_e32 v111, v34
	v_mov_b32_e32 v112, v34
	v_mov_b32_e32 v113, v34
	v_mov_b32_e32 v122, v34
	v_mov_b32_e32 v123, v34
	v_mov_b32_e32 v124, v34
	v_mov_b32_e32 v125, v34
	v_mov_b32_e32 v126, v34
	v_mov_b32_e32 v127, v34
	v_mov_b32_e32 v128, v34
	v_mov_b32_e32 v129, v34
	v_mov_b32_e32 v22, v34
	v_mov_b32_e32 v23, v34
	v_mov_b32_e32 v24, v34
	v_mov_b32_e32 v25, v34
	v_mov_b32_e32 v18, v34
	v_mov_b32_e32 v19, v34
	v_mov_b32_e32 v20, v34
	v_mov_b32_e32 v21, v34
	v_mov_b32_e32 v6, v34
	v_mov_b32_e32 v7, v34
	v_mov_b32_e32 v8, v34
	v_mov_b32_e32 v9, v34
	v_mov_b32_e32 v2, v34
	v_mov_b32_e32 v3, v34
	v_mov_b32_e32 v4, v34
	v_mov_b32_e32 v5, v34
.LBB0_2381:
	s_add_i32 s8, s52, s66
	s_add_i32 s6, s8, -1
	s_cmp_ge_i32 s6, s67
	s_cselect_b32 s7, s67, 0
	s_sub_i32 s6, s6, s7
	s_ashr_i32 s7, s6, 31
	s_lshl_b64 s[40:41], s[6:7], s21
	s_cmp_ge_i32 s8, s67
	s_cselect_b32 s6, s67, 0
	s_sub_i32 s6, s8, s6
	s_ashr_i32 s7, s6, 31
	v_add_u32_e32 v141, s24, v0
	s_lshl_b64 s[6:7], s[6:7], s21
	ds_read_b128 v[142:145], v141
	ds_read_b128 v[146:149], v141 offset:1024
	ds_read_b128 v[150:153], v141 offset:2048
	ds_read_b128 v[154:157], v141 offset:3072
	v_add_u32_e32 v141, s27, v0
	s_add_u32 s8, s19, s6
	ds_read_b128 v[158:161], v141
	ds_read_b128 v[168:171], v141 offset:1024
	ds_read_b128 v[172:175], v141 offset:2048
	ds_read_b128 v[180:183], v141 offset:3072
	s_addc_u32 s9, s20, s7
	s_add_u32 s6, s22, s6
	s_addc_u32 s7, s23, s7
	s_cmp_eq_u32 s67, s66
	s_cselect_b32 s10, s2, s8
	s_cselect_b32 s11, s3, s9
	s_cselect_b32 s9, s5, s7
	s_cselect_b32 s8, s4, s6
	s_add_u32 s6, s10, s47
	s_addc_u32 s7, s11, 0
	s_add_u32 s40, s64, s40
	s_addc_u32 s41, s65, s41
	s_add_i32 m0, s30, 0xc000
	ds_read_b128 v[184:187], v139
	ds_read_b128 v[188:191], v139 offset:1024
	ds_read_b128 v[192:195], v139 offset:2048
	ds_read_b128 v[196:199], v139 offset:3072
	ds_read_b128 v[212:215], v139 offset:4096
	ds_read_b128 v[216:219], v139 offset:5120
	ds_read_b128 v[220:223], v139 offset:6144
	ds_read_b128 v[224:227], v139 offset:7168
	global_load_lds_dwordx4 v134, s[40:41]
	s_add_i32 m0, s30, 0xe000
	s_nop 0
	global_load_lds_dwordx4 v136, s[40:41]
	s_waitcnt vmcnt(8)
	s_waitcnt lgkmcnt(0)
	s_barrier
	s_setprio 1
	s_waitcnt lgkmcnt(0)
	v_mfma_f32_16x16x32_bf16 v[126:129], v[142:145], v[184:187], v[126:129]
	v_mfma_f32_16x16x32_bf16 v[122:125], v[150:153], v[184:187], v[122:125]
	v_mfma_f32_16x16x32_bf16 v[110:113], v[142:145], v[192:195], v[110:113]
	v_mfma_f32_16x16x32_bf16 v[106:109], v[150:153], v[192:195], v[106:109]
	v_mfma_f32_16x16x32_bf16 v[94:97], v[142:145], v[212:215], v[94:97]
	v_mfma_f32_16x16x32_bf16 v[90:93], v[150:153], v[212:215], v[90:93]
	v_mfma_f32_16x16x32_bf16 v[78:81], v[142:145], v[220:223], v[78:81]
	v_mfma_f32_16x16x32_bf16 v[74:77], v[150:153], v[220:223], v[74:77]
	v_mfma_f32_16x16x32_bf16 v[126:129], v[146:149], v[188:191], v[126:129]
	v_mfma_f32_16x16x32_bf16 v[122:125], v[154:157], v[188:191], v[122:125]
	v_mfma_f32_16x16x32_bf16 v[110:113], v[146:149], v[196:199], v[110:113]
	v_mfma_f32_16x16x32_bf16 v[106:109], v[154:157], v[196:199], v[106:109]
	v_mfma_f32_16x16x32_bf16 v[94:97], v[146:149], v[216:219], v[94:97]
	v_mfma_f32_16x16x32_bf16 v[90:93], v[154:157], v[216:219], v[90:93]
	v_mfma_f32_16x16x32_bf16 v[78:81], v[146:149], v[224:227], v[78:81]
	v_mfma_f32_16x16x32_bf16 v[74:77], v[154:157], v[224:227], v[74:77]
	s_setprio 0
	s_setprio 1
	v_mfma_f32_16x16x32_bf16 v[118:121], v[158:161], v[184:187], v[118:121]
	v_mfma_f32_16x16x32_bf16 v[114:117], v[172:175], v[184:187], v[114:117]
	v_mfma_f32_16x16x32_bf16 v[102:105], v[158:161], v[192:195], v[102:105]
	v_mfma_f32_16x16x32_bf16 v[98:101], v[172:175], v[192:195], v[98:101]
	v_mfma_f32_16x16x32_bf16 v[86:89], v[158:161], v[212:215], v[86:89]
	v_mfma_f32_16x16x32_bf16 v[82:85], v[172:175], v[212:215], v[82:85]
	v_mfma_f32_16x16x32_bf16 v[70:73], v[158:161], v[220:223], v[70:73]
	v_mfma_f32_16x16x32_bf16 v[66:69], v[172:175], v[220:223], v[66:69]
	v_mfma_f32_16x16x32_bf16 v[118:121], v[168:171], v[188:191], v[118:121]
	v_mfma_f32_16x16x32_bf16 v[114:117], v[180:183], v[188:191], v[114:117]
	v_mfma_f32_16x16x32_bf16 v[102:105], v[168:171], v[196:199], v[102:105]
	v_mfma_f32_16x16x32_bf16 v[98:101], v[180:183], v[196:199], v[98:101]
	v_mfma_f32_16x16x32_bf16 v[86:89], v[168:171], v[216:219], v[86:89]
	v_mfma_f32_16x16x32_bf16 v[82:85], v[180:183], v[216:219], v[82:85]
	v_mfma_f32_16x16x32_bf16 v[70:73], v[168:171], v[224:227], v[70:73]
	v_mfma_f32_16x16x32_bf16 v[66:69], v[180:183], v[224:227], v[66:69]
	s_setprio 0
	s_barrier
	s_mov_b32 m0, s25
	s_add_u32 s40, s8, s18
	ds_read_b128 v[184:187], v139 offset:16384
	ds_read_b128 v[188:191], v139 offset:17408
	ds_read_b128 v[192:195], v139 offset:18432
	ds_read_b128 v[196:199], v139 offset:19456
	ds_read_b128 v[212:215], v139 offset:20480
	ds_read_b128 v[216:219], v139 offset:21504
	ds_read_b128 v[220:223], v139 offset:22528
	ds_read_b128 v[224:227], v139 offset:23552
	global_load_lds_dwordx4 v134, s[8:9]
	s_mov_b32 m0, s26
	s_addc_u32 s41, s9, s17
	global_load_lds_dwordx4 v136, s[8:9]
	s_mov_b32 m0, s28
	s_nop 0
	global_load_lds_dwordx4 v134, s[40:41]
	s_mov_b32 m0, s29
	s_nop 0
	global_load_lds_dwordx4 v136, s[40:41]
	s_mov_b32 m0, s30
	s_nop 0
	global_load_lds_dwordx4 v134, s[10:11]
	s_mov_b32 m0, s31
	s_nop 0
	global_load_lds_dwordx4 v136, s[10:11]
	s_waitcnt vmcnt(8)
	s_waitcnt lgkmcnt(0)
	s_barrier
	s_setprio 1
	s_waitcnt lgkmcnt(0)
	v_mfma_f32_16x16x32_bf16 v[62:65], v[142:145], v[184:187], v[62:65]
	v_mfma_f32_16x16x32_bf16 v[58:61], v[150:153], v[184:187], v[58:61]
	v_mfma_f32_16x16x32_bf16 v[46:49], v[142:145], v[192:195], v[46:49]
	v_mfma_f32_16x16x32_bf16 v[42:45], v[150:153], v[192:195], v[42:45]
	v_mfma_f32_16x16x32_bf16 v[30:33], v[142:145], v[212:215], v[30:33]
	v_mfma_f32_16x16x32_bf16 v[26:29], v[150:153], v[212:215], v[26:29]
	v_mfma_f32_16x16x32_bf16 v[14:17], v[142:145], v[220:223], v[14:17]
	v_mfma_f32_16x16x32_bf16 v[10:13], v[150:153], v[220:223], v[10:13]
	v_mfma_f32_16x16x32_bf16 v[62:65], v[146:149], v[188:191], v[62:65]
	v_mfma_f32_16x16x32_bf16 v[58:61], v[154:157], v[188:191], v[58:61]
	v_mfma_f32_16x16x32_bf16 v[46:49], v[146:149], v[196:199], v[46:49]
	v_mfma_f32_16x16x32_bf16 v[42:45], v[154:157], v[196:199], v[42:45]
	v_mfma_f32_16x16x32_bf16 v[30:33], v[146:149], v[216:219], v[30:33]
	v_mfma_f32_16x16x32_bf16 v[26:29], v[154:157], v[216:219], v[26:29]
	v_mfma_f32_16x16x32_bf16 v[14:17], v[146:149], v[224:227], v[14:17]
	v_mfma_f32_16x16x32_bf16 v[10:13], v[154:157], v[224:227], v[10:13]
	s_setprio 0
	s_setprio 1
	v_mfma_f32_16x16x32_bf16 v[54:57], v[158:161], v[184:187], v[54:57]
	v_mfma_f32_16x16x32_bf16 v[50:53], v[172:175], v[184:187], v[50:53]
	v_mfma_f32_16x16x32_bf16 v[38:41], v[158:161], v[192:195], v[38:41]
	v_mfma_f32_16x16x32_bf16 v[34:37], v[172:175], v[192:195], v[34:37]
	v_mfma_f32_16x16x32_bf16 v[22:25], v[158:161], v[212:215], v[22:25]
	v_mfma_f32_16x16x32_bf16 v[18:21], v[172:175], v[212:215], v[18:21]
	v_mfma_f32_16x16x32_bf16 v[6:9], v[158:161], v[220:223], v[6:9]
	v_mfma_f32_16x16x32_bf16 v[2:5], v[172:175], v[220:223], v[2:5]
	v_mfma_f32_16x16x32_bf16 v[54:57], v[168:171], v[188:191], v[54:57]
	v_mfma_f32_16x16x32_bf16 v[50:53], v[180:183], v[188:191], v[50:53]
	v_mfma_f32_16x16x32_bf16 v[38:41], v[168:171], v[196:199], v[38:41]
	v_mfma_f32_16x16x32_bf16 v[34:37], v[180:183], v[196:199], v[34:37]
	v_mfma_f32_16x16x32_bf16 v[22:25], v[168:171], v[216:219], v[22:25]
	v_mfma_f32_16x16x32_bf16 v[18:21], v[180:183], v[216:219], v[18:21]
	v_mfma_f32_16x16x32_bf16 v[6:9], v[168:171], v[224:227], v[6:9]
	v_mfma_f32_16x16x32_bf16 v[2:5], v[180:183], v[224:227], v[2:5]
	s_setprio 0
	s_barrier
	v_add_u32_e32 v141, s35, v0
	ds_read_b128 v[142:145], v141
	ds_read_b128 v[146:149], v141 offset:1024
	ds_read_b128 v[150:153], v141 offset:2048
	ds_read_b128 v[154:157], v141 offset:3072
	v_add_u32_e32 v141, s51, v0
	ds_read_b128 v[158:161], v141
	ds_read_b128 v[168:171], v141 offset:1024
	ds_read_b128 v[172:175], v141 offset:2048
	ds_read_b128 v[180:183], v141 offset:3072
	s_add_u32 s10, s10, s18
	s_addc_u32 s11, s11, s17
	s_mov_b32 m0, s33
	ds_read_b128 v[184:187], v139 offset:32768
	ds_read_b128 v[188:191], v139 offset:33792
	ds_read_b128 v[192:195], v139 offset:34816
	ds_read_b128 v[196:199], v139 offset:35840
	ds_read_b128 v[212:215], v139 offset:36864
	ds_read_b128 v[216:219], v139 offset:37888
	ds_read_b128 v[220:223], v139 offset:38912
	ds_read_b128 v[224:227], v139 offset:39936
	global_load_lds_dwordx4 v134, s[10:11]
	s_mov_b32 m0, s34
	s_nop 0
	global_load_lds_dwordx4 v136, s[10:11]
	s_waitcnt vmcnt(8)
	s_waitcnt lgkmcnt(0)
	s_barrier
	s_setprio 1
	s_waitcnt lgkmcnt(0)
	v_mfma_f32_16x16x32_bf16 v[126:129], v[142:145], v[184:187], v[126:129]
	v_mfma_f32_16x16x32_bf16 v[122:125], v[150:153], v[184:187], v[122:125]
	v_mfma_f32_16x16x32_bf16 v[110:113], v[142:145], v[192:195], v[110:113]
	v_mfma_f32_16x16x32_bf16 v[106:109], v[150:153], v[192:195], v[106:109]
	v_mfma_f32_16x16x32_bf16 v[94:97], v[142:145], v[212:215], v[94:97]
	v_mfma_f32_16x16x32_bf16 v[90:93], v[150:153], v[212:215], v[90:93]
	v_mfma_f32_16x16x32_bf16 v[78:81], v[142:145], v[220:223], v[78:81]
	v_mfma_f32_16x16x32_bf16 v[74:77], v[150:153], v[220:223], v[74:77]
	v_mfma_f32_16x16x32_bf16 v[126:129], v[146:149], v[188:191], v[126:129]
	v_mfma_f32_16x16x32_bf16 v[122:125], v[154:157], v[188:191], v[122:125]
	v_mfma_f32_16x16x32_bf16 v[110:113], v[146:149], v[196:199], v[110:113]
	v_mfma_f32_16x16x32_bf16 v[106:109], v[154:157], v[196:199], v[106:109]
	v_mfma_f32_16x16x32_bf16 v[94:97], v[146:149], v[216:219], v[94:97]
	v_mfma_f32_16x16x32_bf16 v[90:93], v[154:157], v[216:219], v[90:93]
	v_mfma_f32_16x16x32_bf16 v[78:81], v[146:149], v[224:227], v[78:81]
	v_mfma_f32_16x16x32_bf16 v[74:77], v[154:157], v[224:227], v[74:77]
	s_setprio 0
	s_setprio 1
	v_mfma_f32_16x16x32_bf16 v[118:121], v[158:161], v[184:187], v[118:121]
	v_mfma_f32_16x16x32_bf16 v[114:117], v[172:175], v[184:187], v[114:117]
	v_mfma_f32_16x16x32_bf16 v[102:105], v[158:161], v[192:195], v[102:105]
	v_mfma_f32_16x16x32_bf16 v[98:101], v[172:175], v[192:195], v[98:101]
	v_mfma_f32_16x16x32_bf16 v[86:89], v[158:161], v[212:215], v[86:89]
	v_mfma_f32_16x16x32_bf16 v[82:85], v[172:175], v[212:215], v[82:85]
	v_mfma_f32_16x16x32_bf16 v[70:73], v[158:161], v[220:223], v[70:73]
	v_mfma_f32_16x16x32_bf16 v[66:69], v[172:175], v[220:223], v[66:69]
	v_mfma_f32_16x16x32_bf16 v[118:121], v[168:171], v[188:191], v[118:121]
	v_mfma_f32_16x16x32_bf16 v[114:117], v[180:183], v[188:191], v[114:117]
	v_mfma_f32_16x16x32_bf16 v[102:105], v[168:171], v[196:199], v[102:105]
	v_mfma_f32_16x16x32_bf16 v[98:101], v[180:183], v[196:199], v[98:101]
	v_mfma_f32_16x16x32_bf16 v[86:89], v[168:171], v[216:219], v[86:89]
	v_mfma_f32_16x16x32_bf16 v[82:85], v[180:183], v[216:219], v[82:85]
	v_mfma_f32_16x16x32_bf16 v[70:73], v[168:171], v[224:227], v[70:73]
	v_mfma_f32_16x16x32_bf16 v[66:69], v[180:183], v[224:227], v[66:69]
	s_setprio 0
	s_barrier
	s_add_u32 s8, s8, s47
	s_addc_u32 s9, s9, 0
	s_mov_b32 m0, s36
	ds_read_b128 v[184:187], v139 offset:49152
	ds_read_b128 v[188:191], v139 offset:50176
	ds_read_b128 v[192:195], v139 offset:51200
	ds_read_b128 v[196:199], v139 offset:52224
	ds_read_b128 v[212:215], v139 offset:53248
	ds_read_b128 v[216:219], v139 offset:54272
	ds_read_b128 v[220:223], v139 offset:55296
	ds_read_b128 v[224:227], v139 offset:56320
	global_load_lds_dwordx4 v134, s[8:9]
	v_lshl_add_u64 v[162:163], s[8:9], 0, v[136:137]
	s_add_u32 s8, s8, s18
	s_mov_b32 m0, s37
	s_addc_u32 s9, s9, s17
	global_load_lds_dwordx4 v[162:163], off
	s_mov_b32 m0, s55
	s_nop 0
	global_load_lds_dwordx4 v134, s[8:9]
	s_mov_b32 m0, s60
	s_nop 0
	global_load_lds_dwordx4 v136, s[8:9]
	s_mov_b32 m0, s48
	s_nop 0
	global_load_lds_dwordx4 v134, s[6:7]
	s_mov_b32 m0, s50
	s_nop 0
	global_load_lds_dwordx4 v136, s[6:7]
	s_waitcnt vmcnt(8)
	s_waitcnt lgkmcnt(0)
	s_barrier
	s_setprio 1
	s_waitcnt lgkmcnt(0)
	v_mfma_f32_16x16x32_bf16 v[62:65], v[142:145], v[184:187], v[62:65]
	v_mfma_f32_16x16x32_bf16 v[58:61], v[150:153], v[184:187], v[58:61]
	v_mfma_f32_16x16x32_bf16 v[46:49], v[142:145], v[192:195], v[46:49]
	v_mfma_f32_16x16x32_bf16 v[42:45], v[150:153], v[192:195], v[42:45]
	v_mfma_f32_16x16x32_bf16 v[30:33], v[142:145], v[212:215], v[30:33]
	v_mfma_f32_16x16x32_bf16 v[26:29], v[150:153], v[212:215], v[26:29]
	v_mfma_f32_16x16x32_bf16 v[14:17], v[142:145], v[220:223], v[14:17]
	v_mfma_f32_16x16x32_bf16 v[10:13], v[150:153], v[220:223], v[10:13]
	v_mfma_f32_16x16x32_bf16 v[62:65], v[146:149], v[188:191], v[62:65]
	v_mfma_f32_16x16x32_bf16 v[58:61], v[154:157], v[188:191], v[58:61]
	v_mfma_f32_16x16x32_bf16 v[46:49], v[146:149], v[196:199], v[46:49]
	v_mfma_f32_16x16x32_bf16 v[42:45], v[154:157], v[196:199], v[42:45]
	v_mfma_f32_16x16x32_bf16 v[30:33], v[146:149], v[216:219], v[30:33]
	v_mfma_f32_16x16x32_bf16 v[26:29], v[154:157], v[216:219], v[26:29]
	v_mfma_f32_16x16x32_bf16 v[14:17], v[146:149], v[224:227], v[14:17]
	v_mfma_f32_16x16x32_bf16 v[10:13], v[154:157], v[224:227], v[10:13]
	s_setprio 0
	s_setprio 1
	v_mfma_f32_16x16x32_bf16 v[54:57], v[158:161], v[184:187], v[54:57]
	v_mfma_f32_16x16x32_bf16 v[50:53], v[172:175], v[184:187], v[50:53]
	v_mfma_f32_16x16x32_bf16 v[38:41], v[158:161], v[192:195], v[38:41]
	v_mfma_f32_16x16x32_bf16 v[34:37], v[172:175], v[192:195], v[34:37]
	v_mfma_f32_16x16x32_bf16 v[22:25], v[158:161], v[212:215], v[22:25]
	v_mfma_f32_16x16x32_bf16 v[18:21], v[172:175], v[212:215], v[18:21]
	v_mfma_f32_16x16x32_bf16 v[6:9], v[158:161], v[220:223], v[6:9]
	v_mfma_f32_16x16x32_bf16 v[2:5], v[172:175], v[220:223], v[2:5]
	v_mfma_f32_16x16x32_bf16 v[54:57], v[168:171], v[188:191], v[54:57]
	v_mfma_f32_16x16x32_bf16 v[50:53], v[180:183], v[188:191], v[50:53]
	v_mfma_f32_16x16x32_bf16 v[38:41], v[168:171], v[196:199], v[38:41]
	v_mfma_f32_16x16x32_bf16 v[34:37], v[180:183], v[196:199], v[34:37]
	v_mfma_f32_16x16x32_bf16 v[22:25], v[168:171], v[216:219], v[22:25]
	v_mfma_f32_16x16x32_bf16 v[18:21], v[180:183], v[216:219], v[18:21]
	v_mfma_f32_16x16x32_bf16 v[6:9], v[168:171], v[224:227], v[6:9]
	v_mfma_f32_16x16x32_bf16 v[2:5], v[180:183], v[224:227], v[2:5]
	s_setprio 0
	s_barrier
	s_add_i32 s6, s66, 2
	s_cmp_ge_i32 s66, s67
	s_mov_b32 s66, s6
	s_cbranch_scc0 .LBB0_2381

.LBB0_2389:
	s_lshl_b32 s10, s10, 5
	s_and_b32 s14, s10, 0x60
	s_add_u32 s36, s4, s47
	s_addc_u32 s37, s5, 0
	s_add_i32 s33, s49, 0x18000
	s_add_i32 s34, s33, s11
	v_mov_b32_e32 v135, v1
	s_add_i32 s35, s34, 0x2000
	v_mov_b32_e32 v137, v1
	s_mov_b32 m0, s34
	s_add_u32 s40, s2, s47
	s_waitcnt vmcnt(2)
	s_barrier
	global_load_lds_dwordx4 v134, s[36:37]
	v_lshl_add_u64 v[2:3], s[36:37], 0, v[136:137]
	s_addc_u32 s41, s3, 0
	s_add_i32 s36, s28, 0x8000
	s_add_i32 s37, s28, 0xa000
	s_mov_b32 m0, s35
	s_add_u32 s6, s6, s47
	global_load_lds_dwordx4 v[2:3], off
	s_mov_b32 m0, s36
	s_addc_u32 s7, s7, 0
	s_add_i32 s38, s49, 0x1c000
	global_load_lds_dwordx4 v134, s[40:41]
	s_mov_b32 m0, s37
	s_add_i32 s48, s38, s11
	global_load_lds_dwordx4 v136, s[40:41]
	s_mov_b32 m0, s48
	s_add_i32 s50, s48, 0x2000
	global_load_lds_dwordx4 v134, s[6:7]
	s_mov_b32 m0, s50
	v_mov_b32_e32 v5, 0
	global_load_lds_dwordx4 v136, s[6:7]
	s_waitcnt vmcnt(6)
	v_lshl_or_b32 v0, s9, 6, v131
	s_cmp_lt_i32 s8, 64
	v_mov_b32_e32 v4, v5
	v_mov_b32_e32 v3, v5
	v_mov_b32_e32 v2, v5
	v_mov_b32_e32 v9, v5
	v_mov_b32_e32 v8, v5
	v_mov_b32_e32 v7, v5
	v_mov_b32_e32 v6, v5
	v_mov_b32_e32 v21, v5
	v_mov_b32_e32 v20, v5
	v_mov_b32_e32 v19, v5
	v_mov_b32_e32 v18, v5
	v_mov_b32_e32 v25, v5
	v_mov_b32_e32 v24, v5
	v_mov_b32_e32 v23, v5
	v_mov_b32_e32 v22, v5
	v_mov_b32_e32 v129, v5
	v_mov_b32_e32 v128, v5
	v_mov_b32_e32 v127, v5
	v_mov_b32_e32 v126, v5
	v_mov_b32_e32 v125, v5
	v_mov_b32_e32 v124, v5
	v_mov_b32_e32 v123, v5
	v_mov_b32_e32 v122, v5
	v_mov_b32_e32 v113, v5
	v_mov_b32_e32 v112, v5
	v_mov_b32_e32 v111, v5
	v_mov_b32_e32 v110, v5
	v_mov_b32_e32 v109, v5
	v_mov_b32_e32 v108, v5
	v_mov_b32_e32 v107, v5
	v_mov_b32_e32 v106, v5
	v_mov_b32_e32 v97, v5
	v_mov_b32_e32 v96, v5
	v_mov_b32_e32 v95, v5
	v_mov_b32_e32 v94, v5
	v_mov_b32_e32 v93, v5
	v_mov_b32_e32 v92, v5
	v_mov_b32_e32 v91, v5
	v_mov_b32_e32 v90, v5
	v_mov_b32_e32 v81, v5
	v_mov_b32_e32 v80, v5
	v_mov_b32_e32 v79, v5
	v_mov_b32_e32 v78, v5
	v_mov_b32_e32 v77, v5
	v_mov_b32_e32 v76, v5
	v_mov_b32_e32 v75, v5
	v_mov_b32_e32 v74, v5
	v_mov_b32_e32 v121, v5
	v_mov_b32_e32 v120, v5
	v_mov_b32_e32 v119, v5
	v_mov_b32_e32 v118, v5
	v_mov_b32_e32 v117, v5
	v_mov_b32_e32 v116, v5
	v_mov_b32_e32 v115, v5
	v_mov_b32_e32 v114, v5
	s_waitcnt vmcnt(0)
	v_mov_b32_e32 v105, v5
	v_mov_b32_e32 v104, v5
	v_mov_b32_e32 v103, v5
	v_mov_b32_e32 v102, v5
	v_mov_b32_e32 v101, v5
	v_mov_b32_e32 v100, v5
	v_mov_b32_e32 v99, v5
	v_mov_b32_e32 v98, v5
	v_mov_b32_e32 v89, v5
	v_mov_b32_e32 v88, v5
	v_mov_b32_e32 v87, v5
	v_mov_b32_e32 v86, v5
	v_mov_b32_e32 v85, v5
	v_mov_b32_e32 v84, v5
	v_mov_b32_e32 v83, v5
	v_mov_b32_e32 v82, v5
	v_mov_b32_e32 v73, v5
	v_mov_b32_e32 v72, v5
	v_mov_b32_e32 v71, v5
	v_mov_b32_e32 v70, v5
	v_mov_b32_e32 v69, v5
	v_mov_b32_e32 v68, v5
	v_mov_b32_e32 v67, v5
	v_mov_b32_e32 v66, v5
	v_mov_b32_e32 v65, v5
	v_mov_b32_e32 v64, v5
	v_mov_b32_e32 v63, v5
	v_mov_b32_e32 v62, v5
	v_mov_b32_e32 v61, v5
	v_mov_b32_e32 v60, v5
	v_mov_b32_e32 v59, v5
	v_mov_b32_e32 v58, v5
	v_mov_b32_e32 v49, v5
	v_mov_b32_e32 v48, v5
	v_mov_b32_e32 v47, v5
	v_mov_b32_e32 v46, v5
	v_mov_b32_e32 v45, v5
	v_mov_b32_e32 v44, v5
	v_mov_b32_e32 v43, v5
	v_mov_b32_e32 v42, v5
	v_mov_b32_e32 v33, v5
	v_mov_b32_e32 v32, v5
	v_mov_b32_e32 v31, v5
	v_mov_b32_e32 v30, v5
	v_mov_b32_e32 v29, v5
	v_mov_b32_e32 v28, v5
	v_mov_b32_e32 v27, v5
	v_mov_b32_e32 v26, v5
	v_mov_b32_e32 v17, v5
	v_mov_b32_e32 v16, v5
	v_mov_b32_e32 v15, v5
	v_mov_b32_e32 v14, v5
	v_mov_b32_e32 v13, v5
	v_mov_b32_e32 v12, v5
	v_mov_b32_e32 v11, v5
	v_mov_b32_e32 v10, v5
	v_mov_b32_e32 v57, v5
	v_mov_b32_e32 v56, v5
	v_mov_b32_e32 v55, v5
	v_mov_b32_e32 v54, v5
	v_mov_b32_e32 v53, v5
	v_mov_b32_e32 v52, v5
	v_mov_b32_e32 v51, v5
	v_mov_b32_e32 v50, v5
	v_mov_b32_e32 v41, v5
	v_mov_b32_e32 v40, v5
	v_mov_b32_e32 v39, v5
	v_mov_b32_e32 v38, v5
	v_mov_b32_e32 v37, v5
	v_mov_b32_e32 v36, v5
	v_mov_b32_e32 v35, v5
	v_mov_b32_e32 v34, v5
	s_barrier
	s_cbranch_scc1 .LBB0_2392
	s_add_u32 s51, s17, s16
	v_lshlrev_b32_e32 v2, 6, v0
	s_movk_i32 s6, 0x3c0
	s_addc_u32 s55, s18, s15
	v_and_or_b32 v2, v2, s6, v138
	s_ashr_i32 s6, s8, 31
	v_lshlrev_b32_e32 v3, 2, v0
	s_lshr_b32 s6, s6, 26
	v_and_b32_e32 v3, 32, v3
	s_add_i32 s8, s8, s6
	s_lshl_b32 s6, s9, 13
	v_bitop3_b32 v2, v2, s6, v3 bitop3:0xde
	s_mov_b32 s60, 2
	s_ashr_i32 s64, s8, 6
	v_lshl_or_b32 v138, s14, 7, v179
	v_add_u32_e32 v139, s49, v2
	v_mov_b32_e32 v2, 0
	v_mov_b32_e32 v3, 0
	v_mov_b32_e32 v4, 0
	v_mov_b32_e32 v5, 0
	s_nop 1
	v_mfma_f32_32x32x16_bf16 v[18:33], v[2:5], v[2:5], 0
	v_mfma_f32_32x32x16_bf16 v[34:49], v[2:5], v[2:5], 0
	v_mfma_f32_32x32x16_bf16 v[50:65], v[2:5], v[2:5], 0
	v_mfma_f32_32x32x16_bf16 v[66:81], v[2:5], v[2:5], 0
	v_mfma_f32_32x32x16_bf16 v[82:97], v[2:5], v[2:5], 0
	v_mfma_f32_32x32x16_bf16 v[98:113], v[2:5], v[2:5], 0
	v_mfma_f32_32x32x16_bf16 v[114:129], v[2:5], v[2:5], 0
	v_mfma_f32_16x16x32_bf16 v[6:9], v[2:5], v[2:5], 0
	v_mfma_f32_16x16x32_bf16 v[10:13], v[2:5], v[2:5], 0
	v_mfma_f32_16x16x32_bf16 v[14:17], v[2:5], v[2:5], 0
.LBB0_2391:
	s_add_i32 s8, s52, s60
	s_add_i32 s6, s8, -1
	s_cmp_ge_i32 s6, s64
	s_cselect_b32 s7, s64, 0
	s_sub_i32 s6, s6, s7
	s_ashr_i32 s7, s6, 31
	s_lshl_b64 s[40:41], s[6:7], s19
	s_cmp_ge_i32 s8, s64
	s_cselect_b32 s6, s64, 0
	s_sub_i32 s6, s8, s6
	s_ashr_i32 s7, s6, 31
	s_lshl_b64 s[6:7], s[6:7], s19
	v_add_u32_e32 v152, s22, v138
	v_add_u32_e32 v165, s25, v138
	s_add_u32 s8, s17, s6
	ds_read_b128 v[140:143], v152
	ds_read_b128 v[144:147], v152 offset:1024
	ds_read_b128 v[148:151], v152 offset:2048
	ds_read_b128 v[152:155], v152 offset:3072
	ds_read_b128 v[156:159], v165
	ds_read_b128 v[160:163], v165 offset:1024
	ds_read_b128 v[168:171], v165 offset:2048
	ds_read_b128 v[172:175], v165 offset:3072
	s_addc_u32 s9, s18, s7
	s_add_u32 s6, s20, s6
	s_addc_u32 s7, s21, s7
	s_cmp_eq_u32 s64, s60
	s_cselect_b32 s10, s2, s8
	s_cselect_b32 s11, s3, s9
	s_cselect_b32 s9, s5, s7
	s_cselect_b32 s8, s4, s6
	s_add_u32 s6, s10, s47
	s_addc_u32 s7, s11, 0
	s_add_u32 s40, s51, s40
	s_addc_u32 s41, s55, s41
	s_add_i32 m0, s28, 0xc000
	ds_read_b128 v[180:183], v139
	ds_read_b128 v[184:187], v139 offset:1024
	ds_read_b128 v[188:191], v139 offset:2048
	ds_read_b128 v[192:195], v139 offset:3072
	ds_read_b128 v[196:199], v139 offset:4096
	ds_read_b128 v[212:215], v139 offset:5120
	ds_read_b128 v[216:219], v139 offset:6144
	ds_read_b128 v[220:223], v139 offset:7168
	global_load_lds_dwordx4 v134, s[40:41]
	s_add_i32 m0, s28, 0xe000
	s_nop 0
	global_load_lds_dwordx4 v136, s[40:41]
	s_waitcnt vmcnt(8)
	s_waitcnt lgkmcnt(0)
	s_barrier
	s_setprio 1
	s_waitcnt lgkmcnt(0)
	v_mfma_f32_16x16x32_bf16 v[126:129], v[140:143], v[180:183], v[126:129]
	v_mfma_f32_16x16x32_bf16 v[122:125], v[148:151], v[180:183], v[122:125]
	v_mfma_f32_16x16x32_bf16 v[110:113], v[140:143], v[188:191], v[110:113]
	v_mfma_f32_16x16x32_bf16 v[106:109], v[148:151], v[188:191], v[106:109]
	v_mfma_f32_16x16x32_bf16 v[94:97], v[140:143], v[196:199], v[94:97]
	v_mfma_f32_16x16x32_bf16 v[90:93], v[148:151], v[196:199], v[90:93]
	v_mfma_f32_16x16x32_bf16 v[78:81], v[140:143], v[216:219], v[78:81]
	v_mfma_f32_16x16x32_bf16 v[74:77], v[148:151], v[216:219], v[74:77]
	v_mfma_f32_16x16x32_bf16 v[126:129], v[144:147], v[184:187], v[126:129]
	v_mfma_f32_16x16x32_bf16 v[122:125], v[152:155], v[184:187], v[122:125]
	v_mfma_f32_16x16x32_bf16 v[110:113], v[144:147], v[192:195], v[110:113]
	v_mfma_f32_16x16x32_bf16 v[106:109], v[152:155], v[192:195], v[106:109]
	v_mfma_f32_16x16x32_bf16 v[94:97], v[144:147], v[212:215], v[94:97]
	v_mfma_f32_16x16x32_bf16 v[90:93], v[152:155], v[212:215], v[90:93]
	v_mfma_f32_16x16x32_bf16 v[78:81], v[144:147], v[220:223], v[78:81]
	v_mfma_f32_16x16x32_bf16 v[74:77], v[152:155], v[220:223], v[74:77]
	s_setprio 0
	s_setprio 1
	v_mfma_f32_16x16x32_bf16 v[118:121], v[156:159], v[180:183], v[118:121]
	v_mfma_f32_16x16x32_bf16 v[114:117], v[168:171], v[180:183], v[114:117]
	v_mfma_f32_16x16x32_bf16 v[102:105], v[156:159], v[188:191], v[102:105]
	v_mfma_f32_16x16x32_bf16 v[98:101], v[168:171], v[188:191], v[98:101]
	v_mfma_f32_16x16x32_bf16 v[86:89], v[156:159], v[196:199], v[86:89]
	v_mfma_f32_16x16x32_bf16 v[82:85], v[168:171], v[196:199], v[82:85]
	v_mfma_f32_16x16x32_bf16 v[70:73], v[156:159], v[216:219], v[70:73]
	v_mfma_f32_16x16x32_bf16 v[66:69], v[168:171], v[216:219], v[66:69]
	v_mfma_f32_16x16x32_bf16 v[118:121], v[160:163], v[184:187], v[118:121]
	v_mfma_f32_16x16x32_bf16 v[114:117], v[172:175], v[184:187], v[114:117]
	v_mfma_f32_16x16x32_bf16 v[102:105], v[160:163], v[192:195], v[102:105]
	v_mfma_f32_16x16x32_bf16 v[98:101], v[172:175], v[192:195], v[98:101]
	v_mfma_f32_16x16x32_bf16 v[86:89], v[160:163], v[212:215], v[86:89]
	v_mfma_f32_16x16x32_bf16 v[82:85], v[172:175], v[212:215], v[82:85]
	v_mfma_f32_16x16x32_bf16 v[70:73], v[160:163], v[220:223], v[70:73]
	v_mfma_f32_16x16x32_bf16 v[66:69], v[172:175], v[220:223], v[66:69]
	s_setprio 0
	s_barrier
	s_mov_b32 m0, s23
	s_add_u32 s40, s8, s16
	ds_read_b128 v[180:183], v139 offset:16384
	ds_read_b128 v[184:187], v139 offset:17408
	ds_read_b128 v[188:191], v139 offset:18432
	ds_read_b128 v[192:195], v139 offset:19456
	ds_read_b128 v[196:199], v139 offset:20480
	ds_read_b128 v[212:215], v139 offset:21504
	ds_read_b128 v[216:219], v139 offset:22528
	ds_read_b128 v[220:223], v139 offset:23552
	global_load_lds_dwordx4 v134, s[8:9]
	s_mov_b32 m0, s24
	s_addc_u32 s41, s9, s15
	global_load_lds_dwordx4 v136, s[8:9]
	s_mov_b32 m0, s26
	s_nop 0
	global_load_lds_dwordx4 v134, s[40:41]
	s_mov_b32 m0, s27
	s_nop 0
	global_load_lds_dwordx4 v136, s[40:41]
	s_mov_b32 m0, s28
	s_nop 0
	global_load_lds_dwordx4 v134, s[10:11]
	s_mov_b32 m0, s29
	s_nop 0
	global_load_lds_dwordx4 v136, s[10:11]
	s_waitcnt vmcnt(8)
	s_waitcnt lgkmcnt(0)
	s_barrier
	s_setprio 1
	s_waitcnt lgkmcnt(0)
	v_mfma_f32_16x16x32_bf16 v[62:65], v[140:143], v[180:183], v[62:65]
	v_mfma_f32_16x16x32_bf16 v[58:61], v[148:151], v[180:183], v[58:61]
	v_mfma_f32_16x16x32_bf16 v[46:49], v[140:143], v[188:191], v[46:49]
	v_mfma_f32_16x16x32_bf16 v[42:45], v[148:151], v[188:191], v[42:45]
	v_mfma_f32_16x16x32_bf16 v[30:33], v[140:143], v[196:199], v[30:33]
	v_mfma_f32_16x16x32_bf16 v[26:29], v[148:151], v[196:199], v[26:29]
	v_mfma_f32_16x16x32_bf16 v[14:17], v[140:143], v[216:219], v[14:17]
	v_mfma_f32_16x16x32_bf16 v[10:13], v[148:151], v[216:219], v[10:13]
	v_mfma_f32_16x16x32_bf16 v[62:65], v[144:147], v[184:187], v[62:65]
	v_mfma_f32_16x16x32_bf16 v[58:61], v[152:155], v[184:187], v[58:61]
	v_mfma_f32_16x16x32_bf16 v[46:49], v[144:147], v[192:195], v[46:49]
	v_mfma_f32_16x16x32_bf16 v[42:45], v[152:155], v[192:195], v[42:45]
	v_mfma_f32_16x16x32_bf16 v[30:33], v[144:147], v[212:215], v[30:33]
	v_mfma_f32_16x16x32_bf16 v[26:29], v[152:155], v[212:215], v[26:29]
	v_mfma_f32_16x16x32_bf16 v[14:17], v[144:147], v[220:223], v[14:17]
	v_mfma_f32_16x16x32_bf16 v[10:13], v[152:155], v[220:223], v[10:13]
	s_setprio 0
	s_setprio 1
	v_mfma_f32_16x16x32_bf16 v[54:57], v[156:159], v[180:183], v[54:57]
	v_mfma_f32_16x16x32_bf16 v[50:53], v[168:171], v[180:183], v[50:53]
	v_mfma_f32_16x16x32_bf16 v[38:41], v[156:159], v[188:191], v[38:41]
	v_mfma_f32_16x16x32_bf16 v[34:37], v[168:171], v[188:191], v[34:37]
	v_mfma_f32_16x16x32_bf16 v[22:25], v[156:159], v[196:199], v[22:25]
	v_mfma_f32_16x16x32_bf16 v[18:21], v[168:171], v[196:199], v[18:21]
	v_mfma_f32_16x16x32_bf16 v[6:9], v[156:159], v[216:219], v[6:9]
	v_mfma_f32_16x16x32_bf16 v[2:5], v[168:171], v[216:219], v[2:5]
	v_mfma_f32_16x16x32_bf16 v[54:57], v[160:163], v[184:187], v[54:57]
	v_mfma_f32_16x16x32_bf16 v[50:53], v[172:175], v[184:187], v[50:53]
	v_mfma_f32_16x16x32_bf16 v[38:41], v[160:163], v[192:195], v[38:41]
	v_mfma_f32_16x16x32_bf16 v[34:37], v[172:175], v[192:195], v[34:37]
	v_mfma_f32_16x16x32_bf16 v[22:25], v[160:163], v[212:215], v[22:25]
	v_mfma_f32_16x16x32_bf16 v[18:21], v[172:175], v[212:215], v[18:21]
	v_mfma_f32_16x16x32_bf16 v[6:9], v[160:163], v[220:223], v[6:9]
	v_mfma_f32_16x16x32_bf16 v[2:5], v[172:175], v[220:223], v[2:5]
	s_setprio 0
	s_barrier
	v_add_u32_e32 v152, s33, v138
	v_add_u32_e32 v165, s38, v138
	ds_read_b128 v[140:143], v152
	ds_read_b128 v[144:147], v152 offset:1024
	ds_read_b128 v[148:151], v152 offset:2048
	ds_read_b128 v[152:155], v152 offset:3072
	ds_read_b128 v[156:159], v165
	ds_read_b128 v[160:163], v165 offset:1024
	ds_read_b128 v[168:171], v165 offset:2048
	ds_read_b128 v[172:175], v165 offset:3072
	s_add_u32 s10, s10, s16
	s_addc_u32 s11, s11, s15
	s_mov_b32 m0, s30
	ds_read_b128 v[180:183], v139 offset:32768
	ds_read_b128 v[184:187], v139 offset:33792
	ds_read_b128 v[188:191], v139 offset:34816
	ds_read_b128 v[192:195], v139 offset:35840
	ds_read_b128 v[196:199], v139 offset:36864
	ds_read_b128 v[212:215], v139 offset:37888
	ds_read_b128 v[216:219], v139 offset:38912
	ds_read_b128 v[220:223], v139 offset:39936
	global_load_lds_dwordx4 v134, s[10:11]
	s_mov_b32 m0, s31
	s_nop 0
	global_load_lds_dwordx4 v136, s[10:11]
	s_waitcnt vmcnt(8)
	s_waitcnt lgkmcnt(0)
	s_barrier
	s_setprio 1
	s_waitcnt lgkmcnt(0)
	v_mfma_f32_16x16x32_bf16 v[126:129], v[140:143], v[180:183], v[126:129]
	v_mfma_f32_16x16x32_bf16 v[122:125], v[148:151], v[180:183], v[122:125]
	v_mfma_f32_16x16x32_bf16 v[110:113], v[140:143], v[188:191], v[110:113]
	v_mfma_f32_16x16x32_bf16 v[106:109], v[148:151], v[188:191], v[106:109]
	v_mfma_f32_16x16x32_bf16 v[94:97], v[140:143], v[196:199], v[94:97]
	v_mfma_f32_16x16x32_bf16 v[90:93], v[148:151], v[196:199], v[90:93]
	v_mfma_f32_16x16x32_bf16 v[78:81], v[140:143], v[216:219], v[78:81]
	v_mfma_f32_16x16x32_bf16 v[74:77], v[148:151], v[216:219], v[74:77]
	v_mfma_f32_16x16x32_bf16 v[126:129], v[144:147], v[184:187], v[126:129]
	v_mfma_f32_16x16x32_bf16 v[122:125], v[152:155], v[184:187], v[122:125]
	v_mfma_f32_16x16x32_bf16 v[110:113], v[144:147], v[192:195], v[110:113]
	v_mfma_f32_16x16x32_bf16 v[106:109], v[152:155], v[192:195], v[106:109]
	v_mfma_f32_16x16x32_bf16 v[94:97], v[144:147], v[212:215], v[94:97]
	v_mfma_f32_16x16x32_bf16 v[90:93], v[152:155], v[212:215], v[90:93]
	v_mfma_f32_16x16x32_bf16 v[78:81], v[144:147], v[220:223], v[78:81]
	v_mfma_f32_16x16x32_bf16 v[74:77], v[152:155], v[220:223], v[74:77]
	s_setprio 0
	s_setprio 1
	v_mfma_f32_16x16x32_bf16 v[118:121], v[156:159], v[180:183], v[118:121]
	v_mfma_f32_16x16x32_bf16 v[114:117], v[168:171], v[180:183], v[114:117]
	v_mfma_f32_16x16x32_bf16 v[102:105], v[156:159], v[188:191], v[102:105]
	v_mfma_f32_16x16x32_bf16 v[98:101], v[168:171], v[188:191], v[98:101]
	v_mfma_f32_16x16x32_bf16 v[86:89], v[156:159], v[196:199], v[86:89]
	v_mfma_f32_16x16x32_bf16 v[82:85], v[168:171], v[196:199], v[82:85]
	v_mfma_f32_16x16x32_bf16 v[70:73], v[156:159], v[216:219], v[70:73]
	v_mfma_f32_16x16x32_bf16 v[66:69], v[168:171], v[216:219], v[66:69]
	v_mfma_f32_16x16x32_bf16 v[118:121], v[160:163], v[184:187], v[118:121]
	v_mfma_f32_16x16x32_bf16 v[114:117], v[172:175], v[184:187], v[114:117]
	v_mfma_f32_16x16x32_bf16 v[102:105], v[160:163], v[192:195], v[102:105]
	v_mfma_f32_16x16x32_bf16 v[98:101], v[172:175], v[192:195], v[98:101]
	v_mfma_f32_16x16x32_bf16 v[86:89], v[160:163], v[212:215], v[86:89]
	v_mfma_f32_16x16x32_bf16 v[82:85], v[172:175], v[212:215], v[82:85]
	v_mfma_f32_16x16x32_bf16 v[70:73], v[160:163], v[220:223], v[70:73]
	v_mfma_f32_16x16x32_bf16 v[66:69], v[172:175], v[220:223], v[66:69]
	s_setprio 0
	s_barrier
	s_add_u32 s8, s8, s47
	s_addc_u32 s9, s9, 0
	s_mov_b32 m0, s34
	ds_read_b128 v[180:183], v139 offset:49152
	ds_read_b128 v[184:187], v139 offset:50176
	ds_read_b128 v[188:191], v139 offset:51200
	ds_read_b128 v[192:195], v139 offset:52224
	ds_read_b128 v[196:199], v139 offset:53248
	ds_read_b128 v[212:215], v139 offset:54272
	ds_read_b128 v[216:219], v139 offset:55296
	ds_read_b128 v[220:223], v139 offset:56320
	global_load_lds_dwordx4 v134, s[8:9]
	v_lshl_add_u64 v[224:225], s[8:9], 0, v[136:137]
	s_add_u32 s8, s8, s16
	s_mov_b32 m0, s35
	s_addc_u32 s9, s9, s15
	global_load_lds_dwordx4 v[224:225], off
	s_mov_b32 m0, s48
	s_nop 0
	global_load_lds_dwordx4 v134, s[8:9]
	s_mov_b32 m0, s50
	s_nop 0
	global_load_lds_dwordx4 v136, s[8:9]
	s_mov_b32 m0, s36
	s_nop 0
	global_load_lds_dwordx4 v134, s[6:7]
	s_mov_b32 m0, s37
	s_nop 0
	global_load_lds_dwordx4 v136, s[6:7]
	s_waitcnt vmcnt(8)
	s_waitcnt lgkmcnt(0)
	s_barrier
	s_setprio 1
	s_waitcnt lgkmcnt(0)
	v_mfma_f32_16x16x32_bf16 v[62:65], v[140:143], v[180:183], v[62:65]
	v_mfma_f32_16x16x32_bf16 v[58:61], v[148:151], v[180:183], v[58:61]
	v_mfma_f32_16x16x32_bf16 v[46:49], v[140:143], v[188:191], v[46:49]
	v_mfma_f32_16x16x32_bf16 v[42:45], v[148:151], v[188:191], v[42:45]
	v_mfma_f32_16x16x32_bf16 v[30:33], v[140:143], v[196:199], v[30:33]
	v_mfma_f32_16x16x32_bf16 v[26:29], v[148:151], v[196:199], v[26:29]
	v_mfma_f32_16x16x32_bf16 v[14:17], v[140:143], v[216:219], v[14:17]
	v_mfma_f32_16x16x32_bf16 v[10:13], v[148:151], v[216:219], v[10:13]
	v_mfma_f32_16x16x32_bf16 v[62:65], v[144:147], v[184:187], v[62:65]
	v_mfma_f32_16x16x32_bf16 v[58:61], v[152:155], v[184:187], v[58:61]
	v_mfma_f32_16x16x32_bf16 v[46:49], v[144:147], v[192:195], v[46:49]
	v_mfma_f32_16x16x32_bf16 v[42:45], v[152:155], v[192:195], v[42:45]
	v_mfma_f32_16x16x32_bf16 v[30:33], v[144:147], v[212:215], v[30:33]
	v_mfma_f32_16x16x32_bf16 v[26:29], v[152:155], v[212:215], v[26:29]
	v_mfma_f32_16x16x32_bf16 v[14:17], v[144:147], v[220:223], v[14:17]
	v_mfma_f32_16x16x32_bf16 v[10:13], v[152:155], v[220:223], v[10:13]
	s_setprio 0
	s_setprio 1
	v_mfma_f32_16x16x32_bf16 v[54:57], v[156:159], v[180:183], v[54:57]
	v_mfma_f32_16x16x32_bf16 v[50:53], v[168:171], v[180:183], v[50:53]
	v_mfma_f32_16x16x32_bf16 v[38:41], v[156:159], v[188:191], v[38:41]
	v_mfma_f32_16x16x32_bf16 v[34:37], v[168:171], v[188:191], v[34:37]
	v_mfma_f32_16x16x32_bf16 v[22:25], v[156:159], v[196:199], v[22:25]
	v_mfma_f32_16x16x32_bf16 v[18:21], v[168:171], v[196:199], v[18:21]
	v_mfma_f32_16x16x32_bf16 v[6:9], v[156:159], v[216:219], v[6:9]
	v_mfma_f32_16x16x32_bf16 v[2:5], v[168:171], v[216:219], v[2:5]
	v_mfma_f32_16x16x32_bf16 v[54:57], v[160:163], v[184:187], v[54:57]
	v_mfma_f32_16x16x32_bf16 v[50:53], v[172:175], v[184:187], v[50:53]
	v_mfma_f32_16x16x32_bf16 v[38:41], v[160:163], v[192:195], v[38:41]
	v_mfma_f32_16x16x32_bf16 v[34:37], v[172:175], v[192:195], v[34:37]
	v_mfma_f32_16x16x32_bf16 v[22:25], v[160:163], v[212:215], v[22:25]
	v_mfma_f32_16x16x32_bf16 v[18:21], v[172:175], v[212:215], v[18:21]
	v_mfma_f32_16x16x32_bf16 v[6:9], v[160:163], v[220:223], v[6:9]
	v_mfma_f32_16x16x32_bf16 v[2:5], v[172:175], v[220:223], v[2:5]
	s_setprio 0
	s_barrier
	s_add_i32 s6, s60, 2
	s_cmp_ge_i32 s60, s64
	s_mov_b32 s60, s6
	s_cbranch_scc0 .LBB0_2391

.LBB0_2791:
	s_sext_i32_i8 s68, s12
	s_load_dword s12, s[96:97], 0xc0
	v_lshrrev_b32_e32 v4, 1, v2
	v_and_b32_e32 v4, 24, v4
	v_and_b32_e32 v3, 15, v2
	v_lshlrev_b32_e32 v5, 1, v4
	s_waitcnt lgkmcnt(0)
	s_add_i32 s50, s20, s12
	s_add_u32 s12, s14, 0x13a00000
	s_addc_u32 s13, s15, 0
	s_add_u32 s14, s14, 0x190000
	s_addc_u32 s15, s15, 0
	s_add_i32 s30, s20, 0x400
	s_ashr_i32 s31, s30, 31
	s_lshr_b32 s31, s31, 26
	s_add_i32 s30, s30, s31
	s_ashr_i32 s51, s30, 6
	s_add_i32 s52, s51, -2
	s_and_b64 s[0:1], s[0:1], exec
	s_movk_i32 s0, 0x80
	v_lshlrev_b32_e32 v2, 2, v2
	s_cselect_b32 s53, s0, 0x8000
	v_lshl_or_b32 v139, s29, 6, v3
	v_lshl_or_b32 v3, v3, 6, v5
	s_lshl_b32 s0, s29, 13
	v_and_b32_e32 v2, 32, v2
	v_bitop3_b32 v5, v3, s0, v2 bitop3:0xde
	s_lshl_b32 s0, s28, 5
	s_and_b32 s28, s0, 0x60
	s_lshl_b32 s0, s28, 7
	v_bitop3_b32 v141, s0, v3, v2 bitop3:0xf6
	s_add_u32 s0, s18, s53
	s_addc_u32 s1, s19, 0
	s_add_i32 s55, s21, 0x18000
	s_add_i32 s56, s55, s27
	v_mov_b32_e32 v131, v1
	s_mov_b32 m0, s56
	s_add_i32 s57, s56, 0x2000
	s_waitcnt vmcnt(2)
	s_barrier
	global_load_lds_dwordx4 v0, s[0:1]
	v_lshl_add_u64 v[2:3], s[0:1], 0, v[130:131]
	s_add_u32 s0, s2, s53
	v_mov_b32_e32 v135, v1
	s_mov_b32 m0, s57
	s_addc_u32 s1, s3, 0
	s_add_i32 s58, s46, 0x8000
	v_mov_b32_e32 v133, v1
	global_load_lds_dwordx4 v[2:3], off
	s_mov_b32 m0, s58
	s_add_i32 s59, s46, 0xa000
	global_load_lds_dwordx4 v134, s[0:1]
	v_lshl_add_u64 v[2:3], s[0:1], 0, v[132:133]
	s_add_u32 s0, s16, s53
	s_addc_u32 s1, s17, 0
	s_add_i32 s60, s21, 0x1c000
	s_mov_b32 m0, s59
	s_add_i32 s62, s60, s27
	global_load_lds_dwordx4 v[2:3], off
	s_mov_b32 m0, s62
	s_add_i32 s63, s62, 0x2000
	global_load_lds_dwordx4 v0, s[0:1]
	s_mov_b32 m0, s63
	s_cmpk_gt_i32 s20, 0xfc3f
	global_load_lds_dwordx4 v130, s[0:1]
	s_waitcnt vmcnt(6)
	s_cselect_b64 s[16:17], -1, 0
	s_cmpk_lt_u32 s26, 0x100
	s_mov_b32 s54, 0
	s_cselect_b64 s[18:19], -1, 0
	s_ashr_i32 s64, s50, 31
	v_or_b32_e32 v143, s28, v4
	v_add_u32_e32 v145, s21, v5
	s_barrier
	s_branch .LBB0_2794

.LBB0_2802:
	s_add_i32 s28, s4, s75
	s_add_i32 s26, s28, 1
	s_cmp_ge_i32 s26, s51
	s_cselect_b32 s27, s51, 0
	s_sub_i32 s26, s26, s27
	s_ashr_i32 s27, s26, 31
	s_lshl_b64 s[76:77], s[26:27], s39
	s_add_i32 s28, s28, 2
	s_cmp_ge_i32 s28, s51
	s_cselect_b32 s26, s51, 0
	s_sub_i32 s26, s28, s26
	s_ashr_i32 s27, s26, 31
	v_add_u32_e32 v136, s5, v141
	s_lshl_b64 s[26:27], s[26:27], s39
	ds_read_b128 v[146:149], v136
	ds_read_b128 v[150:153], v136 offset:1024
	ds_read_b128 v[154:157], v136 offset:2048
	ds_read_b128 v[158:161], v136 offset:3072
	v_add_u32_e32 v136, s43, v141
	s_add_u32 s28, s22, s26
	ds_read_b128 v[172:175], v136
	ds_read_b128 v[176:179], v136 offset:1024
	ds_read_b128 v[180:183], v136 offset:2048
	ds_read_b128 v[184:187], v136 offset:3072
	s_addc_u32 s29, s23, s27
	s_add_u32 s26, s24, s26
	s_addc_u32 s27, s25, s27
	s_cmp_eq_u32 s52, s75
	s_cselect_b32 s30, s71, s28
	s_cselect_b32 s31, s72, s29
	s_cselect_b32 s29, s74, s27
	s_cselect_b32 s28, s73, s26
	s_add_u32 s26, s30, s53
	s_addc_u32 s27, s31, 0
	s_add_u32 s76, s69, s76
	s_addc_u32 s77, s70, s77
	s_add_i32 m0, s46, 0xc000
	ds_read_b128 v[188:191], v145
	ds_read_b128 v[192:195], v145 offset:1024
	ds_read_b128 v[196:199], v145 offset:2048
	ds_read_b128 v[212:215], v145 offset:3072
	ds_read_b128 v[216:219], v145 offset:4096
	ds_read_b128 v[220:223], v145 offset:5120
	ds_read_b128 v[224:227], v145 offset:6144
	ds_read_b128 v[228:231], v145 offset:7168
	global_load_lds_dwordx4 v134, s[76:77]
	s_add_i32 m0, s46, 0xe000
	s_nop 0
	global_load_lds_dwordx4 v132, s[76:77]
	s_waitcnt vmcnt(8)
	s_waitcnt lgkmcnt(0)
	s_barrier
	s_setprio 1
	s_waitcnt lgkmcnt(0)
	v_mfma_f32_16x16x32_bf16 v[122:125], v[146:149], v[188:191], v[122:125]
	v_mfma_f32_16x16x32_bf16 v[114:117], v[154:157], v[188:191], v[114:117]
	v_mfma_f32_16x16x32_bf16 v[106:109], v[146:149], v[196:199], v[106:109]
	v_mfma_f32_16x16x32_bf16 v[98:101], v[154:157], v[196:199], v[98:101]
	v_mfma_f32_16x16x32_bf16 v[90:93], v[146:149], v[216:219], v[90:93]
	v_mfma_f32_16x16x32_bf16 v[82:85], v[154:157], v[216:219], v[82:85]
	v_mfma_f32_16x16x32_bf16 v[74:77], v[146:149], v[224:227], v[74:77]
	v_mfma_f32_16x16x32_bf16 v[66:69], v[154:157], v[224:227], v[66:69]
	v_mfma_f32_16x16x32_bf16 v[122:125], v[150:153], v[192:195], v[122:125]
	v_mfma_f32_16x16x32_bf16 v[114:117], v[158:161], v[192:195], v[114:117]
	v_mfma_f32_16x16x32_bf16 v[106:109], v[150:153], v[212:215], v[106:109]
	v_mfma_f32_16x16x32_bf16 v[98:101], v[158:161], v[212:215], v[98:101]
	v_mfma_f32_16x16x32_bf16 v[90:93], v[150:153], v[220:223], v[90:93]
	v_mfma_f32_16x16x32_bf16 v[82:85], v[158:161], v[220:223], v[82:85]
	v_mfma_f32_16x16x32_bf16 v[74:77], v[150:153], v[228:231], v[74:77]
	v_mfma_f32_16x16x32_bf16 v[66:69], v[158:161], v[228:231], v[66:69]
	s_setprio 0
	s_setprio 1
	v_mfma_f32_16x16x32_bf16 v[126:129], v[172:175], v[188:191], v[126:129]
	v_mfma_f32_16x16x32_bf16 v[118:121], v[180:183], v[188:191], v[118:121]
	v_mfma_f32_16x16x32_bf16 v[110:113], v[172:175], v[196:199], v[110:113]
	v_mfma_f32_16x16x32_bf16 v[102:105], v[180:183], v[196:199], v[102:105]
	v_mfma_f32_16x16x32_bf16 v[94:97], v[172:175], v[216:219], v[94:97]
	v_mfma_f32_16x16x32_bf16 v[86:89], v[180:183], v[216:219], v[86:89]
	v_mfma_f32_16x16x32_bf16 v[78:81], v[172:175], v[224:227], v[78:81]
	v_mfma_f32_16x16x32_bf16 v[70:73], v[180:183], v[224:227], v[70:73]
	v_mfma_f32_16x16x32_bf16 v[126:129], v[176:179], v[192:195], v[126:129]
	v_mfma_f32_16x16x32_bf16 v[118:121], v[184:187], v[192:195], v[118:121]
	v_mfma_f32_16x16x32_bf16 v[110:113], v[176:179], v[212:215], v[110:113]
	v_mfma_f32_16x16x32_bf16 v[102:105], v[184:187], v[212:215], v[102:105]
	v_mfma_f32_16x16x32_bf16 v[94:97], v[176:179], v[220:223], v[94:97]
	v_mfma_f32_16x16x32_bf16 v[86:89], v[184:187], v[220:223], v[86:89]
	v_mfma_f32_16x16x32_bf16 v[78:81], v[176:179], v[228:231], v[78:81]
	v_mfma_f32_16x16x32_bf16 v[70:73], v[184:187], v[228:231], v[70:73]
	s_setprio 0
	s_barrier
	s_mov_b32 m0, s41
	s_add_u32 s76, s28, s38
	ds_read_b128 v[188:191], v145 offset:16384
	ds_read_b128 v[192:195], v145 offset:17408
	ds_read_b128 v[196:199], v145 offset:18432
	ds_read_b128 v[212:215], v145 offset:19456
	ds_read_b128 v[216:219], v145 offset:20480
	ds_read_b128 v[220:223], v145 offset:21504
	ds_read_b128 v[224:227], v145 offset:22528
	ds_read_b128 v[228:231], v145 offset:23552
	global_load_lds_dwordx4 v0, s[28:29]
	s_mov_b32 m0, s42
	s_addc_u32 s77, s29, 0
	global_load_lds_dwordx4 v130, s[28:29]
	s_mov_b32 m0, s44
	s_nop 0
	global_load_lds_dwordx4 v0, s[76:77]
	s_mov_b32 m0, s45
	s_nop 0
	global_load_lds_dwordx4 v130, s[76:77]
	s_mov_b32 m0, s46
	s_nop 0
	global_load_lds_dwordx4 v134, s[30:31]
	s_mov_b32 m0, s47
	s_nop 0
	global_load_lds_dwordx4 v132, s[30:31]
	s_waitcnt vmcnt(8)
	s_waitcnt lgkmcnt(0)
	s_barrier
	s_setprio 1
	s_waitcnt lgkmcnt(0)
	v_mfma_f32_16x16x32_bf16 v[58:61], v[146:149], v[188:191], v[58:61]
	v_mfma_f32_16x16x32_bf16 v[50:53], v[154:157], v[188:191], v[50:53]
	v_mfma_f32_16x16x32_bf16 v[42:45], v[146:149], v[196:199], v[42:45]
	v_mfma_f32_16x16x32_bf16 v[38:41], v[154:157], v[196:199], v[38:41]
	v_mfma_f32_16x16x32_bf16 v[26:29], v[146:149], v[216:219], v[26:29]
	v_mfma_f32_16x16x32_bf16 v[18:21], v[154:157], v[216:219], v[18:21]
	v_mfma_f32_16x16x32_bf16 v[10:13], v[146:149], v[224:227], v[10:13]
	v_mfma_f32_16x16x32_bf16 v[6:9], v[154:157], v[224:227], v[6:9]
	v_mfma_f32_16x16x32_bf16 v[58:61], v[150:153], v[192:195], v[58:61]
	v_mfma_f32_16x16x32_bf16 v[50:53], v[158:161], v[192:195], v[50:53]
	v_mfma_f32_16x16x32_bf16 v[42:45], v[150:153], v[212:215], v[42:45]
	v_mfma_f32_16x16x32_bf16 v[38:41], v[158:161], v[212:215], v[38:41]
	v_mfma_f32_16x16x32_bf16 v[26:29], v[150:153], v[220:223], v[26:29]
	v_mfma_f32_16x16x32_bf16 v[18:21], v[158:161], v[220:223], v[18:21]
	v_mfma_f32_16x16x32_bf16 v[10:13], v[150:153], v[228:231], v[10:13]
	v_mfma_f32_16x16x32_bf16 v[6:9], v[158:161], v[228:231], v[6:9]
	s_setprio 0
	s_setprio 1
	v_mfma_f32_16x16x32_bf16 v[62:65], v[172:175], v[188:191], v[62:65]
	v_mfma_f32_16x16x32_bf16 v[54:57], v[180:183], v[188:191], v[54:57]
	v_mfma_f32_16x16x32_bf16 v[46:49], v[172:175], v[196:199], v[46:49]
	v_mfma_f32_16x16x32_bf16 v[34:37], v[180:183], v[196:199], v[34:37]
	v_mfma_f32_16x16x32_bf16 v[30:33], v[172:175], v[216:219], v[30:33]
	v_mfma_f32_16x16x32_bf16 v[22:25], v[180:183], v[216:219], v[22:25]
	v_mfma_f32_16x16x32_bf16 v[14:17], v[172:175], v[224:227], v[14:17]
	v_mfma_f32_16x16x32_bf16 v[2:5], v[180:183], v[224:227], v[2:5]
	v_mfma_f32_16x16x32_bf16 v[62:65], v[176:179], v[192:195], v[62:65]
	v_mfma_f32_16x16x32_bf16 v[54:57], v[184:187], v[192:195], v[54:57]
	v_mfma_f32_16x16x32_bf16 v[46:49], v[176:179], v[212:215], v[46:49]
	v_mfma_f32_16x16x32_bf16 v[34:37], v[184:187], v[212:215], v[34:37]
	v_mfma_f32_16x16x32_bf16 v[30:33], v[176:179], v[220:223], v[30:33]
	v_mfma_f32_16x16x32_bf16 v[22:25], v[184:187], v[220:223], v[22:25]
	v_mfma_f32_16x16x32_bf16 v[14:17], v[176:179], v[228:231], v[14:17]
	v_mfma_f32_16x16x32_bf16 v[2:5], v[184:187], v[228:231], v[2:5]
	s_setprio 0
	s_barrier
	v_add_u32_e32 v136, s55, v141
	ds_read_b128 v[146:149], v136
	ds_read_b128 v[150:153], v136 offset:1024
	ds_read_b128 v[154:157], v136 offset:2048
	ds_read_b128 v[158:161], v136 offset:3072
	v_add_u32_e32 v136, s60, v141
	ds_read_b128 v[172:175], v136
	ds_read_b128 v[176:179], v136 offset:1024
	ds_read_b128 v[180:183], v136 offset:2048
	ds_read_b128 v[184:187], v136 offset:3072
	s_add_u32 s30, s30, s38
	s_addc_u32 s31, s31, 0
	s_mov_b32 m0, s48
	ds_read_b128 v[188:191], v145 offset:32768
	ds_read_b128 v[192:195], v145 offset:33792
	ds_read_b128 v[196:199], v145 offset:34816
	ds_read_b128 v[212:215], v145 offset:35840
	ds_read_b128 v[216:219], v145 offset:36864
	ds_read_b128 v[220:223], v145 offset:37888
	ds_read_b128 v[224:227], v145 offset:38912
	ds_read_b128 v[228:231], v145 offset:39936
	global_load_lds_dwordx4 v134, s[30:31]
	s_mov_b32 m0, s49
	s_nop 0
	global_load_lds_dwordx4 v132, s[30:31]
	s_waitcnt vmcnt(8)
	s_waitcnt lgkmcnt(0)
	s_barrier
	s_setprio 1
	s_waitcnt lgkmcnt(0)
	v_mfma_f32_16x16x32_bf16 v[122:125], v[146:149], v[188:191], v[122:125]
	v_mfma_f32_16x16x32_bf16 v[114:117], v[154:157], v[188:191], v[114:117]
	v_mfma_f32_16x16x32_bf16 v[106:109], v[146:149], v[196:199], v[106:109]
	v_mfma_f32_16x16x32_bf16 v[98:101], v[154:157], v[196:199], v[98:101]
	v_mfma_f32_16x16x32_bf16 v[90:93], v[146:149], v[216:219], v[90:93]
	v_mfma_f32_16x16x32_bf16 v[82:85], v[154:157], v[216:219], v[82:85]
	v_mfma_f32_16x16x32_bf16 v[74:77], v[146:149], v[224:227], v[74:77]
	v_mfma_f32_16x16x32_bf16 v[66:69], v[154:157], v[224:227], v[66:69]
	v_mfma_f32_16x16x32_bf16 v[122:125], v[150:153], v[192:195], v[122:125]
	v_mfma_f32_16x16x32_bf16 v[114:117], v[158:161], v[192:195], v[114:117]
	v_mfma_f32_16x16x32_bf16 v[106:109], v[150:153], v[212:215], v[106:109]
	v_mfma_f32_16x16x32_bf16 v[98:101], v[158:161], v[212:215], v[98:101]
	v_mfma_f32_16x16x32_bf16 v[90:93], v[150:153], v[220:223], v[90:93]
	v_mfma_f32_16x16x32_bf16 v[82:85], v[158:161], v[220:223], v[82:85]
	v_mfma_f32_16x16x32_bf16 v[74:77], v[150:153], v[228:231], v[74:77]
	v_mfma_f32_16x16x32_bf16 v[66:69], v[158:161], v[228:231], v[66:69]
	s_setprio 0
	s_setprio 1
	v_mfma_f32_16x16x32_bf16 v[126:129], v[172:175], v[188:191], v[126:129]
	v_mfma_f32_16x16x32_bf16 v[118:121], v[180:183], v[188:191], v[118:121]
	v_mfma_f32_16x16x32_bf16 v[110:113], v[172:175], v[196:199], v[110:113]
	v_mfma_f32_16x16x32_bf16 v[102:105], v[180:183], v[196:199], v[102:105]
	v_mfma_f32_16x16x32_bf16 v[94:97], v[172:175], v[216:219], v[94:97]
	v_mfma_f32_16x16x32_bf16 v[86:89], v[180:183], v[216:219], v[86:89]
	v_mfma_f32_16x16x32_bf16 v[78:81], v[172:175], v[224:227], v[78:81]
	v_mfma_f32_16x16x32_bf16 v[70:73], v[180:183], v[224:227], v[70:73]
	v_mfma_f32_16x16x32_bf16 v[126:129], v[176:179], v[192:195], v[126:129]
	v_mfma_f32_16x16x32_bf16 v[118:121], v[184:187], v[192:195], v[118:121]
	v_mfma_f32_16x16x32_bf16 v[110:113], v[176:179], v[212:215], v[110:113]
	v_mfma_f32_16x16x32_bf16 v[102:105], v[184:187], v[212:215], v[102:105]
	v_mfma_f32_16x16x32_bf16 v[94:97], v[176:179], v[220:223], v[94:97]
	v_mfma_f32_16x16x32_bf16 v[86:89], v[184:187], v[220:223], v[86:89]
	v_mfma_f32_16x16x32_bf16 v[78:81], v[176:179], v[228:231], v[78:81]
	v_mfma_f32_16x16x32_bf16 v[70:73], v[184:187], v[228:231], v[70:73]
	s_setprio 0
	s_barrier
	s_add_u32 s28, s28, s53
	s_addc_u32 s29, s29, 0
	s_mov_b32 m0, s56
	ds_read_b128 v[188:191], v145 offset:49152
	ds_read_b128 v[192:195], v145 offset:50176
	ds_read_b128 v[196:199], v145 offset:51200
	ds_read_b128 v[212:215], v145 offset:52224
	ds_read_b128 v[216:219], v145 offset:53248
	ds_read_b128 v[220:223], v145 offset:54272
	ds_read_b128 v[224:227], v145 offset:55296
	ds_read_b128 v[228:231], v145 offset:56320
	global_load_lds_dwordx4 v0, s[28:29]
	v_lshl_add_u64 v[136:137], s[28:29], 0, v[130:131]
	s_add_u32 s28, s28, s38
	s_mov_b32 m0, s57
	s_addc_u32 s29, s29, 0
	global_load_lds_dwordx4 v[136:137], off
	s_mov_b32 m0, s62
	s_nop 0
	global_load_lds_dwordx4 v0, s[28:29]
	s_mov_b32 m0, s63
	s_nop 0
	global_load_lds_dwordx4 v130, s[28:29]
	s_mov_b32 m0, s58
	s_nop 0
	global_load_lds_dwordx4 v134, s[26:27]
	s_mov_b32 m0, s59
	s_nop 0
	global_load_lds_dwordx4 v132, s[26:27]
	s_waitcnt vmcnt(8)
	s_waitcnt lgkmcnt(0)
	s_barrier
	s_setprio 1
	s_waitcnt lgkmcnt(0)
	v_mfma_f32_16x16x32_bf16 v[58:61], v[146:149], v[188:191], v[58:61]
	v_mfma_f32_16x16x32_bf16 v[50:53], v[154:157], v[188:191], v[50:53]
	v_mfma_f32_16x16x32_bf16 v[42:45], v[146:149], v[196:199], v[42:45]
	v_mfma_f32_16x16x32_bf16 v[38:41], v[154:157], v[196:199], v[38:41]
	v_mfma_f32_16x16x32_bf16 v[26:29], v[146:149], v[216:219], v[26:29]
	v_mfma_f32_16x16x32_bf16 v[18:21], v[154:157], v[216:219], v[18:21]
	v_mfma_f32_16x16x32_bf16 v[10:13], v[146:149], v[224:227], v[10:13]
	v_mfma_f32_16x16x32_bf16 v[6:9], v[154:157], v[224:227], v[6:9]
	v_mfma_f32_16x16x32_bf16 v[58:61], v[150:153], v[192:195], v[58:61]
	v_mfma_f32_16x16x32_bf16 v[50:53], v[158:161], v[192:195], v[50:53]
	v_mfma_f32_16x16x32_bf16 v[42:45], v[150:153], v[212:215], v[42:45]
	v_mfma_f32_16x16x32_bf16 v[38:41], v[158:161], v[212:215], v[38:41]
	v_mfma_f32_16x16x32_bf16 v[26:29], v[150:153], v[220:223], v[26:29]
	v_mfma_f32_16x16x32_bf16 v[18:21], v[158:161], v[220:223], v[18:21]
	v_mfma_f32_16x16x32_bf16 v[10:13], v[150:153], v[228:231], v[10:13]
	v_mfma_f32_16x16x32_bf16 v[6:9], v[158:161], v[228:231], v[6:9]
	s_setprio 0
	s_setprio 1
	v_mfma_f32_16x16x32_bf16 v[62:65], v[172:175], v[188:191], v[62:65]
	v_mfma_f32_16x16x32_bf16 v[54:57], v[180:183], v[188:191], v[54:57]
	v_mfma_f32_16x16x32_bf16 v[46:49], v[172:175], v[196:199], v[46:49]
	v_mfma_f32_16x16x32_bf16 v[34:37], v[180:183], v[196:199], v[34:37]
	v_mfma_f32_16x16x32_bf16 v[30:33], v[172:175], v[216:219], v[30:33]
	v_mfma_f32_16x16x32_bf16 v[22:25], v[180:183], v[216:219], v[22:25]
	v_mfma_f32_16x16x32_bf16 v[14:17], v[172:175], v[224:227], v[14:17]
	v_mfma_f32_16x16x32_bf16 v[2:5], v[180:183], v[224:227], v[2:5]
	v_mfma_f32_16x16x32_bf16 v[62:65], v[176:179], v[192:195], v[62:65]
	v_mfma_f32_16x16x32_bf16 v[54:57], v[184:187], v[192:195], v[54:57]
	v_mfma_f32_16x16x32_bf16 v[46:49], v[176:179], v[212:215], v[46:49]
	v_mfma_f32_16x16x32_bf16 v[34:37], v[184:187], v[212:215], v[34:37]
	v_mfma_f32_16x16x32_bf16 v[30:33], v[176:179], v[220:223], v[30:33]
	v_mfma_f32_16x16x32_bf16 v[22:25], v[184:187], v[220:223], v[22:25]
	v_mfma_f32_16x16x32_bf16 v[14:17], v[176:179], v[228:231], v[14:17]
	v_mfma_f32_16x16x32_bf16 v[2:5], v[184:187], v[228:231], v[2:5]
	s_setprio 0
	s_barrier
	s_add_i32 s75, s75, 2
	s_cmp_ge_i32 s75, s51
	s_cbranch_scc0 .LBB0_2802

.LBB0_2871:
	s_sext_i32_i8 s66, s12
	s_load_dword s12, s[96:97], 0xc0
	v_bfe_u32 v4, v2, 4, 2
	v_and_b32_e32 v3, 15, v2
	v_lshlrev_b32_e32 v5, 4, v4
	v_lshlrev_b32_e32 v2, 2, v2
	s_waitcnt lgkmcnt(0)
	s_add_i32 s48, s18, s12
	s_add_u32 s12, s13, 0x32000000
	s_addc_u32 s13, s28, 0
	s_add_i32 s28, s18, 0xb00
	s_ashr_i32 s29, s28, 31
	s_lshr_b32 s29, s29, 26
	s_add_i32 s28, s28, s29
	s_ashr_i32 s49, s28, 6
	s_add_i32 s50, s49, -2
	s_and_b64 s[0:1], s[0:1], exec
	s_movk_i32 s0, 0x80
	s_cselect_b32 s51, s0, 0x8000
	v_lshl_or_b32 v154, s26, 6, v3
	v_lshl_or_b32 v3, v3, 6, v5
	s_lshl_b32 s0, s26, 13
	v_and_b32_e32 v2, 32, v2
	v_bitop3_b32 v5, v3, s0, v2 bitop3:0xde
	s_lshl_b32 s0, s25, 5
	s_and_b32 s25, s0, 0x60
	s_lshl_b32 s0, s25, 7
	v_bitop3_b32 v155, s0, v3, v2 bitop3:0xf6
	s_add_u32 s0, s16, s51
	s_addc_u32 s1, s17, 0
	s_add_i32 s53, s24, 0x18000
	s_add_i32 s54, s53, s27
	v_mov_b32_e32 v131, v1
	s_mov_b32 m0, s54
	s_add_i32 s55, s54, 0x2000
	s_waitcnt vmcnt(2)
	s_barrier
	global_load_lds_dwordx4 v0, s[0:1]
	v_lshl_add_u64 v[2:3], s[0:1], 0, v[130:131]
	s_add_u32 s0, s2, s51
	s_mov_b32 m0, s55
	s_addc_u32 s1, s3, 0
	s_add_i32 s56, s44, 0x8000
	global_load_lds_dwordx4 v[2:3], off
	s_mov_b32 m0, s56
	s_add_i32 s57, s44, 0xa000
	global_load_lds_dwordx4 v0, s[0:1]
	v_lshl_add_u64 v[2:3], s[0:1], 0, v[130:131]
	s_add_u32 s0, s14, s51
	s_addc_u32 s1, s15, 0
	s_add_i32 s58, s24, 0x1c000
	s_mov_b32 m0, s57
	s_add_i32 s59, s58, s27
	global_load_lds_dwordx4 v[2:3], off
	s_mov_b32 m0, s59
	s_add_i32 s60, s59, 0x2000
	global_load_lds_dwordx4 v0, s[0:1]
	s_mov_b32 m0, s60
	s_cmpk_gt_i32 s18, 0xf53f
	global_load_lds_dwordx4 v130, s[0:1]
	s_waitcnt vmcnt(6)
	s_cselect_b64 s[14:15], -1, 0
	s_cmpk_lt_u32 s19, 0x100
	s_mov_b32 s52, 0
	s_cselect_b64 s[16:17], -1, 0
	s_ashr_i32 s62, s48, 31
	v_lshl_or_b32 v156, v4, 2, s25
	v_add_u32_e32 v157, s24, v5
	s_barrier
	s_branch .LBB0_2874

.LBB0_2886:
	s_add_i32 s26, s4, s73
	s_add_i32 s24, s26, 1
	s_cmp_ge_i32 s24, s49
	s_cselect_b32 s25, s49, 0
	s_sub_i32 s24, s24, s25
	s_ashr_i32 s25, s24, 31
	s_lshl_b64 s[74:75], s[24:25], s38
	s_add_i32 s26, s26, 2
	s_cmp_ge_i32 s26, s49
	s_cselect_b32 s24, s49, 0
	s_sub_i32 s24, s26, s24
	s_ashr_i32 s25, s24, 31
	s_lshl_b64 s[24:25], s[24:25], s38
	v_add_u32_e32 v144, s5, v155
	v_add_u32_e32 v152, s41, v155
	s_add_u32 s26, s20, s24
	ds_read_b128 v[132:135], v144
	ds_read_b128 v[136:139], v144 offset:1024
	ds_read_b128 v[140:143], v144 offset:2048
	ds_read_b128 v[144:147], v144 offset:3072
	ds_read_b128 v[148:151], v152
	ds_read_b128 v[158:161], v152 offset:1024
	ds_read_b128 v[172:175], v152 offset:2048
	ds_read_b128 v[176:179], v152 offset:3072
	s_addc_u32 s27, s21, s25
	s_add_u32 s24, s22, s24
	s_addc_u32 s25, s23, s25
	s_cmp_eq_u32 s50, s73
	s_cselect_b32 s28, s69, s26
	s_cselect_b32 s29, s70, s27
	s_cselect_b32 s27, s72, s25
	s_cselect_b32 s26, s71, s24
	s_add_u32 s24, s28, s51
	s_addc_u32 s25, s29, 0
	s_add_u32 s74, s67, s74
	s_addc_u32 s75, s68, s75
	s_add_i32 m0, s44, 0xc000
	ds_read_b128 v[180:183], v157
	ds_read_b128 v[184:187], v157 offset:1024
	ds_read_b128 v[188:191], v157 offset:2048
	ds_read_b128 v[192:195], v157 offset:3072
	ds_read_b128 v[196:199], v157 offset:4096
	ds_read_b128 v[212:215], v157 offset:5120
	ds_read_b128 v[216:219], v157 offset:6144
	ds_read_b128 v[220:223], v157 offset:7168
	global_load_lds_dwordx4 v0, s[74:75]
	s_add_i32 m0, s44, 0xe000
	s_nop 0
	global_load_lds_dwordx4 v130, s[74:75]
	s_waitcnt vmcnt(8)
	s_waitcnt lgkmcnt(0)
	s_barrier
	s_setprio 1
	s_waitcnt lgkmcnt(0)
	v_mfma_f32_16x16x32_bf16 v[126:129], v[132:135], v[180:183], v[126:129]
	v_mfma_f32_16x16x32_bf16 v[122:125], v[140:143], v[180:183], v[122:125]
	v_mfma_f32_16x16x32_bf16 v[110:113], v[132:135], v[188:191], v[110:113]
	v_mfma_f32_16x16x32_bf16 v[106:109], v[140:143], v[188:191], v[106:109]
	v_mfma_f32_16x16x32_bf16 v[94:97], v[132:135], v[196:199], v[94:97]
	v_mfma_f32_16x16x32_bf16 v[90:93], v[140:143], v[196:199], v[90:93]
	v_mfma_f32_16x16x32_bf16 v[78:81], v[132:135], v[216:219], v[78:81]
	v_mfma_f32_16x16x32_bf16 v[74:77], v[140:143], v[216:219], v[74:77]
	v_mfma_f32_16x16x32_bf16 v[126:129], v[136:139], v[184:187], v[126:129]
	v_mfma_f32_16x16x32_bf16 v[122:125], v[144:147], v[184:187], v[122:125]
	v_mfma_f32_16x16x32_bf16 v[110:113], v[136:139], v[192:195], v[110:113]
	v_mfma_f32_16x16x32_bf16 v[106:109], v[144:147], v[192:195], v[106:109]
	v_mfma_f32_16x16x32_bf16 v[94:97], v[136:139], v[212:215], v[94:97]
	v_mfma_f32_16x16x32_bf16 v[90:93], v[144:147], v[212:215], v[90:93]
	v_mfma_f32_16x16x32_bf16 v[78:81], v[136:139], v[220:223], v[78:81]
	v_mfma_f32_16x16x32_bf16 v[74:77], v[144:147], v[220:223], v[74:77]
	s_setprio 0
	s_setprio 1
	v_mfma_f32_16x16x32_bf16 v[118:121], v[148:151], v[180:183], v[118:121]
	v_mfma_f32_16x16x32_bf16 v[114:117], v[172:175], v[180:183], v[114:117]
	v_mfma_f32_16x16x32_bf16 v[102:105], v[148:151], v[188:191], v[102:105]
	v_mfma_f32_16x16x32_bf16 v[98:101], v[172:175], v[188:191], v[98:101]
	v_mfma_f32_16x16x32_bf16 v[86:89], v[148:151], v[196:199], v[86:89]
	v_mfma_f32_16x16x32_bf16 v[82:85], v[172:175], v[196:199], v[82:85]
	v_mfma_f32_16x16x32_bf16 v[70:73], v[148:151], v[216:219], v[70:73]
	v_mfma_f32_16x16x32_bf16 v[66:69], v[172:175], v[216:219], v[66:69]
	v_mfma_f32_16x16x32_bf16 v[118:121], v[158:161], v[184:187], v[118:121]
	v_mfma_f32_16x16x32_bf16 v[114:117], v[176:179], v[184:187], v[114:117]
	v_mfma_f32_16x16x32_bf16 v[102:105], v[158:161], v[192:195], v[102:105]
	v_mfma_f32_16x16x32_bf16 v[98:101], v[176:179], v[192:195], v[98:101]
	v_mfma_f32_16x16x32_bf16 v[86:89], v[158:161], v[212:215], v[86:89]
	v_mfma_f32_16x16x32_bf16 v[82:85], v[176:179], v[212:215], v[82:85]
	v_mfma_f32_16x16x32_bf16 v[70:73], v[158:161], v[220:223], v[70:73]
	v_mfma_f32_16x16x32_bf16 v[66:69], v[176:179], v[220:223], v[66:69]
	s_setprio 0
	s_barrier
	s_mov_b32 m0, s39
	s_add_u32 s74, s26, s37
	ds_read_b128 v[180:183], v157 offset:16384
	ds_read_b128 v[184:187], v157 offset:17408
	ds_read_b128 v[188:191], v157 offset:18432
	ds_read_b128 v[192:195], v157 offset:19456
	ds_read_b128 v[196:199], v157 offset:20480
	ds_read_b128 v[212:215], v157 offset:21504
	ds_read_b128 v[216:219], v157 offset:22528
	ds_read_b128 v[220:223], v157 offset:23552
	global_load_lds_dwordx4 v0, s[26:27]
	s_mov_b32 m0, s40
	s_addc_u32 s75, s27, 0
	global_load_lds_dwordx4 v130, s[26:27]
	s_mov_b32 m0, s42
	s_nop 0
	global_load_lds_dwordx4 v0, s[74:75]
	s_mov_b32 m0, s43
	s_nop 0
	global_load_lds_dwordx4 v130, s[74:75]
	s_mov_b32 m0, s44
	s_nop 0
	global_load_lds_dwordx4 v0, s[28:29]
	s_mov_b32 m0, s45
	s_nop 0
	global_load_lds_dwordx4 v130, s[28:29]
	s_waitcnt vmcnt(8)
	s_waitcnt lgkmcnt(0)
	s_barrier
	s_setprio 1
	s_waitcnt lgkmcnt(0)
	v_mfma_f32_16x16x32_bf16 v[62:65], v[132:135], v[180:183], v[62:65]
	v_mfma_f32_16x16x32_bf16 v[58:61], v[140:143], v[180:183], v[58:61]
	v_mfma_f32_16x16x32_bf16 v[46:49], v[132:135], v[188:191], v[46:49]
	v_mfma_f32_16x16x32_bf16 v[42:45], v[140:143], v[188:191], v[42:45]
	v_mfma_f32_16x16x32_bf16 v[30:33], v[132:135], v[196:199], v[30:33]
	v_mfma_f32_16x16x32_bf16 v[26:29], v[140:143], v[196:199], v[26:29]
	v_mfma_f32_16x16x32_bf16 v[14:17], v[132:135], v[216:219], v[14:17]
	v_mfma_f32_16x16x32_bf16 v[10:13], v[140:143], v[216:219], v[10:13]
	v_mfma_f32_16x16x32_bf16 v[62:65], v[136:139], v[184:187], v[62:65]
	v_mfma_f32_16x16x32_bf16 v[58:61], v[144:147], v[184:187], v[58:61]
	v_mfma_f32_16x16x32_bf16 v[46:49], v[136:139], v[192:195], v[46:49]
	v_mfma_f32_16x16x32_bf16 v[42:45], v[144:147], v[192:195], v[42:45]
	v_mfma_f32_16x16x32_bf16 v[30:33], v[136:139], v[212:215], v[30:33]
	v_mfma_f32_16x16x32_bf16 v[26:29], v[144:147], v[212:215], v[26:29]
	v_mfma_f32_16x16x32_bf16 v[14:17], v[136:139], v[220:223], v[14:17]
	v_mfma_f32_16x16x32_bf16 v[10:13], v[144:147], v[220:223], v[10:13]
	s_setprio 0
	s_setprio 1
	v_mfma_f32_16x16x32_bf16 v[54:57], v[148:151], v[180:183], v[54:57]
	v_mfma_f32_16x16x32_bf16 v[50:53], v[172:175], v[180:183], v[50:53]
	v_mfma_f32_16x16x32_bf16 v[38:41], v[148:151], v[188:191], v[38:41]
	v_mfma_f32_16x16x32_bf16 v[34:37], v[172:175], v[188:191], v[34:37]
	v_mfma_f32_16x16x32_bf16 v[22:25], v[148:151], v[196:199], v[22:25]
	v_mfma_f32_16x16x32_bf16 v[18:21], v[172:175], v[196:199], v[18:21]
	v_mfma_f32_16x16x32_bf16 v[6:9], v[148:151], v[216:219], v[6:9]
	v_mfma_f32_16x16x32_bf16 v[2:5], v[172:175], v[216:219], v[2:5]
	v_mfma_f32_16x16x32_bf16 v[54:57], v[158:161], v[184:187], v[54:57]
	v_mfma_f32_16x16x32_bf16 v[50:53], v[176:179], v[184:187], v[50:53]
	v_mfma_f32_16x16x32_bf16 v[38:41], v[158:161], v[192:195], v[38:41]
	v_mfma_f32_16x16x32_bf16 v[34:37], v[176:179], v[192:195], v[34:37]
	v_mfma_f32_16x16x32_bf16 v[22:25], v[158:161], v[212:215], v[22:25]
	v_mfma_f32_16x16x32_bf16 v[18:21], v[176:179], v[212:215], v[18:21]
	v_mfma_f32_16x16x32_bf16 v[6:9], v[158:161], v[220:223], v[6:9]
	v_mfma_f32_16x16x32_bf16 v[2:5], v[176:179], v[220:223], v[2:5]
	s_setprio 0
	s_barrier
	v_add_u32_e32 v144, s53, v155
	v_add_u32_e32 v152, s58, v155
	ds_read_b128 v[132:135], v144
	ds_read_b128 v[136:139], v144 offset:1024
	ds_read_b128 v[140:143], v144 offset:2048
	ds_read_b128 v[144:147], v144 offset:3072
	ds_read_b128 v[148:151], v152
	ds_read_b128 v[158:161], v152 offset:1024
	ds_read_b128 v[172:175], v152 offset:2048
	ds_read_b128 v[176:179], v152 offset:3072
	s_add_u32 s28, s28, s37
	s_addc_u32 s29, s29, 0
	s_mov_b32 m0, s46
	ds_read_b128 v[180:183], v157 offset:32768
	ds_read_b128 v[184:187], v157 offset:33792
	ds_read_b128 v[188:191], v157 offset:34816
	ds_read_b128 v[192:195], v157 offset:35840
	ds_read_b128 v[196:199], v157 offset:36864
	ds_read_b128 v[212:215], v157 offset:37888
	ds_read_b128 v[216:219], v157 offset:38912
	ds_read_b128 v[220:223], v157 offset:39936
	global_load_lds_dwordx4 v0, s[28:29]
	s_mov_b32 m0, s47
	s_nop 0
	global_load_lds_dwordx4 v130, s[28:29]
	s_waitcnt vmcnt(8)
	s_waitcnt lgkmcnt(0)
	s_barrier
	s_setprio 1
	s_waitcnt lgkmcnt(0)
	v_mfma_f32_16x16x32_bf16 v[126:129], v[132:135], v[180:183], v[126:129]
	v_mfma_f32_16x16x32_bf16 v[122:125], v[140:143], v[180:183], v[122:125]
	v_mfma_f32_16x16x32_bf16 v[110:113], v[132:135], v[188:191], v[110:113]
	v_mfma_f32_16x16x32_bf16 v[106:109], v[140:143], v[188:191], v[106:109]
	v_mfma_f32_16x16x32_bf16 v[94:97], v[132:135], v[196:199], v[94:97]
	v_mfma_f32_16x16x32_bf16 v[90:93], v[140:143], v[196:199], v[90:93]
	v_mfma_f32_16x16x32_bf16 v[78:81], v[132:135], v[216:219], v[78:81]
	v_mfma_f32_16x16x32_bf16 v[74:77], v[140:143], v[216:219], v[74:77]
	v_mfma_f32_16x16x32_bf16 v[126:129], v[136:139], v[184:187], v[126:129]
	v_mfma_f32_16x16x32_bf16 v[122:125], v[144:147], v[184:187], v[122:125]
	v_mfma_f32_16x16x32_bf16 v[110:113], v[136:139], v[192:195], v[110:113]
	v_mfma_f32_16x16x32_bf16 v[106:109], v[144:147], v[192:195], v[106:109]
	v_mfma_f32_16x16x32_bf16 v[94:97], v[136:139], v[212:215], v[94:97]
	v_mfma_f32_16x16x32_bf16 v[90:93], v[144:147], v[212:215], v[90:93]
	v_mfma_f32_16x16x32_bf16 v[78:81], v[136:139], v[220:223], v[78:81]
	v_mfma_f32_16x16x32_bf16 v[74:77], v[144:147], v[220:223], v[74:77]
	s_setprio 0
	s_setprio 1
	v_mfma_f32_16x16x32_bf16 v[118:121], v[148:151], v[180:183], v[118:121]
	v_mfma_f32_16x16x32_bf16 v[114:117], v[172:175], v[180:183], v[114:117]
	v_mfma_f32_16x16x32_bf16 v[102:105], v[148:151], v[188:191], v[102:105]
	v_mfma_f32_16x16x32_bf16 v[98:101], v[172:175], v[188:191], v[98:101]
	v_mfma_f32_16x16x32_bf16 v[86:89], v[148:151], v[196:199], v[86:89]
	v_mfma_f32_16x16x32_bf16 v[82:85], v[172:175], v[196:199], v[82:85]
	v_mfma_f32_16x16x32_bf16 v[70:73], v[148:151], v[216:219], v[70:73]
	v_mfma_f32_16x16x32_bf16 v[66:69], v[172:175], v[216:219], v[66:69]
	v_mfma_f32_16x16x32_bf16 v[118:121], v[158:161], v[184:187], v[118:121]
	v_mfma_f32_16x16x32_bf16 v[114:117], v[176:179], v[184:187], v[114:117]
	v_mfma_f32_16x16x32_bf16 v[102:105], v[158:161], v[192:195], v[102:105]
	v_mfma_f32_16x16x32_bf16 v[98:101], v[176:179], v[192:195], v[98:101]
	v_mfma_f32_16x16x32_bf16 v[86:89], v[158:161], v[212:215], v[86:89]
	v_mfma_f32_16x16x32_bf16 v[82:85], v[176:179], v[212:215], v[82:85]
	v_mfma_f32_16x16x32_bf16 v[70:73], v[158:161], v[220:223], v[70:73]
	v_mfma_f32_16x16x32_bf16 v[66:69], v[176:179], v[220:223], v[66:69]
	s_setprio 0
	s_barrier
	s_add_u32 s26, s26, s51
	s_addc_u32 s27, s27, 0
	s_mov_b32 m0, s54
	ds_read_b128 v[180:183], v157 offset:49152
	ds_read_b128 v[184:187], v157 offset:50176
	ds_read_b128 v[188:191], v157 offset:51200
	ds_read_b128 v[192:195], v157 offset:52224
	ds_read_b128 v[196:199], v157 offset:53248
	ds_read_b128 v[212:215], v157 offset:54272
	ds_read_b128 v[216:219], v157 offset:55296
	ds_read_b128 v[220:223], v157 offset:56320
	global_load_lds_dwordx4 v0, s[26:27]
	v_lshl_add_u64 v[152:153], s[26:27], 0, v[130:131]
	s_add_u32 s26, s26, s37
	s_mov_b32 m0, s55
	s_addc_u32 s27, s27, 0
	global_load_lds_dwordx4 v[152:153], off
	s_mov_b32 m0, s59
	s_nop 0
	global_load_lds_dwordx4 v0, s[26:27]
	s_mov_b32 m0, s60
	s_nop 0
	global_load_lds_dwordx4 v130, s[26:27]
	s_mov_b32 m0, s56
	s_nop 0
	global_load_lds_dwordx4 v0, s[24:25]
	s_mov_b32 m0, s57
	s_nop 0
	global_load_lds_dwordx4 v130, s[24:25]
	s_waitcnt vmcnt(8)
	s_waitcnt lgkmcnt(0)
	s_barrier
	s_setprio 1
	s_waitcnt lgkmcnt(0)
	v_mfma_f32_16x16x32_bf16 v[62:65], v[132:135], v[180:183], v[62:65]
	v_mfma_f32_16x16x32_bf16 v[58:61], v[140:143], v[180:183], v[58:61]
	v_mfma_f32_16x16x32_bf16 v[46:49], v[132:135], v[188:191], v[46:49]
	v_mfma_f32_16x16x32_bf16 v[42:45], v[140:143], v[188:191], v[42:45]
	v_mfma_f32_16x16x32_bf16 v[30:33], v[132:135], v[196:199], v[30:33]
	v_mfma_f32_16x16x32_bf16 v[26:29], v[140:143], v[196:199], v[26:29]
	v_mfma_f32_16x16x32_bf16 v[14:17], v[132:135], v[216:219], v[14:17]
	v_mfma_f32_16x16x32_bf16 v[10:13], v[140:143], v[216:219], v[10:13]
	v_mfma_f32_16x16x32_bf16 v[62:65], v[136:139], v[184:187], v[62:65]
	v_mfma_f32_16x16x32_bf16 v[58:61], v[144:147], v[184:187], v[58:61]
	v_mfma_f32_16x16x32_bf16 v[46:49], v[136:139], v[192:195], v[46:49]
	v_mfma_f32_16x16x32_bf16 v[42:45], v[144:147], v[192:195], v[42:45]
	v_mfma_f32_16x16x32_bf16 v[30:33], v[136:139], v[212:215], v[30:33]
	v_mfma_f32_16x16x32_bf16 v[26:29], v[144:147], v[212:215], v[26:29]
	v_mfma_f32_16x16x32_bf16 v[14:17], v[136:139], v[220:223], v[14:17]
	v_mfma_f32_16x16x32_bf16 v[10:13], v[144:147], v[220:223], v[10:13]
	s_setprio 0
	s_setprio 1
	v_mfma_f32_16x16x32_bf16 v[54:57], v[148:151], v[180:183], v[54:57]
	v_mfma_f32_16x16x32_bf16 v[50:53], v[172:175], v[180:183], v[50:53]
	v_mfma_f32_16x16x32_bf16 v[38:41], v[148:151], v[188:191], v[38:41]
	v_mfma_f32_16x16x32_bf16 v[34:37], v[172:175], v[188:191], v[34:37]
	v_mfma_f32_16x16x32_bf16 v[22:25], v[148:151], v[196:199], v[22:25]
	v_mfma_f32_16x16x32_bf16 v[18:21], v[172:175], v[196:199], v[18:21]
	v_mfma_f32_16x16x32_bf16 v[6:9], v[148:151], v[216:219], v[6:9]
	v_mfma_f32_16x16x32_bf16 v[2:5], v[172:175], v[216:219], v[2:5]
	v_mfma_f32_16x16x32_bf16 v[54:57], v[158:161], v[184:187], v[54:57]
	v_mfma_f32_16x16x32_bf16 v[50:53], v[176:179], v[184:187], v[50:53]
	v_mfma_f32_16x16x32_bf16 v[38:41], v[158:161], v[192:195], v[38:41]
	v_mfma_f32_16x16x32_bf16 v[34:37], v[176:179], v[192:195], v[34:37]
	v_mfma_f32_16x16x32_bf16 v[22:25], v[158:161], v[212:215], v[22:25]
	v_mfma_f32_16x16x32_bf16 v[18:21], v[176:179], v[212:215], v[18:21]
	v_mfma_f32_16x16x32_bf16 v[6:9], v[158:161], v[220:223], v[6:9]
	v_mfma_f32_16x16x32_bf16 v[2:5], v[176:179], v[220:223], v[2:5]
	s_setprio 0
	s_barrier
	s_add_i32 s73, s73, 2
	s_cmp_ge_i32 s73, s49
	s_cbranch_scc0 .LBB0_2886
